# PEER down re-timed: each row buffer refilled (token two ahead) right after its last use inside the maths instead of a 16-load burst; exact 128-token loop without tail tests
# speedup vs baseline: 1.0255x; 1.0143x over previous
; DI int tidx() { int t = threadIdx.x & 255; asm volatile("" : "+v"(t)); return t; }
; DI int ftid() { int t = threadIdx.x; asm volatile("" : "+v"(t)); return t; }
; #define PD_E(t, E) do { const char* eb_ = eiu + (size_t)(t) * 512; _Pragma("unroll") for (int q = 0; q < 4; ++q) E[q] = *(const i32x4_t*)(eb_ + (eio + 16u * q)); } while (0)
; #define PD_H(t, H) do { const char* hb_ = h2u + (size_t)(t) * 2048; H[0] = *(const u32x4*)(hb_ + h2o); H[1] = *(const u32x4*)(hb_ + (h2o + 16u)); } while (0)
; #define PD_TAB(E, W) do { _Pragma("unroll") for (int q = 0; q < 16; ++q) W[q] = *(const u32x4*)(tabu + ((unsigned)E[q >> 2][q & 3] * 128u + tabo)); } while (0)
; DI void phase_peerdown(const Params& p, int bid, int nb) {
;   const int lane = tidx() & 63, wid = __builtin_amdgcn_readfirstlane(ftid() >> 6), e8 = lane >> 3, c = lane & 7;
;   const int x = bid & 7, gw = (bid >> 3) * 8 + wid, nw = (nb >> 3) * 8;
;   const char* h2u = p.ws + WS_H + 256 * x; const unsigned h2o = 32u * c;
;   const char* tabu = p.ws + WS_PU + (size_t)x * 16384 * 128; const unsigned tabo = 16u * c;
;   const char* eiu = p.ws + WS_EIDX; const unsigned eio = 64u * e8;
;   char* pdu = p.ws + WS_PD + (size_t)x * T_ * 256; const unsigned pdo = 32u * e8 + 4u * c;
;   const bool c0 = (lane & 1) != 0, c1 = (lane & 2) != 0, c2 = (lane & 4) != 0;
;     ...
;   i32x4_t eA[4], eB[4]; u32x4 hA[2], hB[2], wA[16], wB[16];
;   int t = gw; if (t >= T_) return;
;   int t1 = t + nw;
;   PD_E(t, eA); PD_H(t, hA); PD_TAB(eA, wA);
;   if (t1 < T_) { PD_E(t1, eB); PD_H(t1, hB); }
.LBB0_1735:
	s_or_b64 exec, exec, s[0:1]
	v_mov_b32_e32 v116, v206
	s_waitcnt lgkmcnt(0)
	v_mov_b32_e32 v0, v207
	s_barrier
	v_readlane_b32 s2, v250, 0
	v_readfirstlane_b32 s0, v0
	s_ashr_i32 s0, s0, 6
	s_and_b32 s19, s2, 7
	s_and_b32 s49, s2, -8
	s_add_i32 s12, s0, s49
	s_and_b32 s18, s86, -8
	s_lshl_b32 s48, s19, 21
	s_add_u32 s16, s84, 0x12000000
	s_addc_u32 s17, s85, 0
	s_cmpk_gt_i32 s12, 0x7fff
	v_readlane_b32 s3, v250, 1
	s_cbranch_scc1 .LBB0_1753
	s_lshl_b32 s0, s19, 8
	s_add_u32 s8, s56, s0
	s_addc_u32 s9, s57, 0
	s_add_u32 s0, s84, s48
	s_addc_u32 s1, s85, 0
	s_add_u32 s6, s0, 0xe000000
	s_addc_u32 s7, s1, 0
	v_bfe_u32 v117, v116, 3, 3
	v_and_b32_e32 v118, 7, v116
	v_lshlrev_b32_e32 v209, 4, v118
	v_lshlrev_b32_e32 v112, 6, v117
	v_lshlrev_b32_e32 v114, 5, v118
	v_mov_b32_e32 v113, 0
	v_mov_b32_e32 v115, 0
	v_lshl_add_u64 v[180:181], s[16:17], 0, v[112:113]
	v_lshl_add_u64 v[182:183], s[8:9], 0, v[114:115]
	s_lshl_b32 s0, s19, 23
	s_add_u32 s10, s84, s0
	s_addc_u32 s11, s85, 0
	s_add_u32 s10, s10, 0x14000000
	s_addc_u32 s11, s11, 0
	v_lshlrev_b32_e32 v118, 2, v118
	v_lshl_or_b32 v118, v117, 5, v118
	v_mov_b32_e32 v119, 0
	v_lshl_add_u64 v[178:179], s[10:11], 0, v[118:119]
	v_and_b32_e32 v117, 1, v116
	v_cmp_eq_u32_e64 s[0:1], 0, v117
	v_and_b32_e32 v117, 2, v116
	v_cmp_eq_u32_e64 s[2:3], 0, v117
	v_and_b32_e32 v117, 4, v116
	v_cmp_eq_u32_e64 s[4:5], 0, v117
	s_mov_b32 s21, 0
	s_add_u32 s20, s12, 0x0
	s_lshl_b32 s20, s20, 9
	v_lshl_add_u64 v[0:1], v[180:181], 0, s[20:21]
	global_load_dwordx4 v[12:15], v[0:1], off offset:48
	global_load_dwordx4 v[8:11], v[0:1], off offset:32
	global_load_dwordx4 v[4:7], v[0:1], off offset:16
	s_nop 0
	global_load_dwordx4 v[0:3], v[0:1], off
	s_add_u32 s20, s12, 0x100
	s_lshl_b32 s20, s20, 9
	v_lshl_add_u64 v[80:81], v[180:181], 0, s[20:21]
	global_load_dwordx4 v[64:67], v[80:81], off offset:48
	global_load_dwordx4 v[68:71], v[80:81], off offset:32
	global_load_dwordx4 v[72:75], v[80:81], off offset:16
	s_nop 0
	global_load_dwordx4 v[80:83], v[80:81], off
	s_add_u32 s20, s12, 0x0
	s_lshl_b32 s20, s20, 11
	v_lshl_add_u64 v[20:21], v[182:183], 0, s[20:21]
	global_load_dwordx4 v[16:19], v[20:21], off offset:16
	s_nop 0
	global_load_dwordx4 v[20:23], v[20:21], off
	s_add_u32 s20, s12, 0x100
	s_lshl_b32 s20, s20, 11
	v_lshl_add_u64 v[108:109], v[182:183], 0, s[20:21]
	global_load_dwordx4 v[100:103], v[108:109], off offset:16
	s_nop 0
	global_load_dwordx4 v[108:111], v[108:109], off
	s_waitcnt vmcnt(8)
	v_lshl_or_b32 v0, v0, 7, v209
	global_load_dwordx4 v[24:27], v0, s[6:7]
	v_lshl_or_b32 v1, v1, 7, v209
	global_load_dwordx4 v[28:31], v1, s[6:7]
	v_lshl_or_b32 v2, v2, 7, v209
	global_load_dwordx4 v[32:35], v2, s[6:7]
	v_lshl_or_b32 v3, v3, 7, v209
	global_load_dwordx4 v[36:39], v3, s[6:7]
	v_lshl_or_b32 v4, v4, 7, v209
	global_load_dwordx4 v[40:43], v4, s[6:7]
	v_lshl_or_b32 v5, v5, 7, v209
	global_load_dwordx4 v[44:47], v5, s[6:7]
	v_lshl_or_b32 v6, v6, 7, v209
	global_load_dwordx4 v[48:51], v6, s[6:7]
	v_lshl_or_b32 v7, v7, 7, v209
	global_load_dwordx4 v[52:55], v7, s[6:7]
	v_lshl_or_b32 v8, v8, 7, v209
	global_load_dwordx4 v[56:59], v8, s[6:7]
	v_lshl_or_b32 v9, v9, 7, v209
	global_load_dwordx4 v[60:63], v9, s[6:7]
	v_lshl_or_b32 v10, v10, 7, v209
	global_load_dwordx4 v[76:79], v10, s[6:7]
	v_lshl_or_b32 v11, v11, 7, v209
	global_load_dwordx4 v[84:87], v11, s[6:7]
	v_lshl_or_b32 v12, v12, 7, v209
	global_load_dwordx4 v[88:91], v12, s[6:7]
	v_lshl_or_b32 v13, v13, 7, v209
	global_load_dwordx4 v[92:95], v13, s[6:7]
	v_lshl_or_b32 v14, v14, 7, v209
	global_load_dwordx4 v[96:99], v14, s[6:7]
	v_lshl_or_b32 v15, v15, 7, v209
	global_load_dwordx4 v[104:107], v15, s[6:7]
	s_add_u32 s20, s12, 0x200
	s_lshl_b32 s20, s20, 9
	v_lshl_add_u64 v[0:1], v[180:181], 0, s[20:21]
	global_load_dwordx4 v[12:15], v[0:1], off offset:48
	global_load_dwordx4 v[8:11], v[0:1], off offset:32
	global_load_dwordx4 v[4:7], v[0:1], off offset:16
	s_nop 0
	global_load_dwordx4 v[0:3], v[0:1], off
	s_waitcnt vmcnt(24)
	v_lshl_or_b32 v80, v80, 7, v209
	global_load_dwordx4 v[112:115], v80, s[6:7]
	v_lshl_or_b32 v81, v81, 7, v209
	global_load_dwordx4 v[116:119], v81, s[6:7]
	v_lshl_or_b32 v82, v82, 7, v209
	global_load_dwordx4 v[120:123], v82, s[6:7]
	v_lshl_or_b32 v83, v83, 7, v209
	global_load_dwordx4 v[124:127], v83, s[6:7]
	v_lshl_or_b32 v72, v72, 7, v209
	global_load_dwordx4 v[128:131], v72, s[6:7]
	v_lshl_or_b32 v73, v73, 7, v209
	global_load_dwordx4 v[132:135], v73, s[6:7]
	v_lshl_or_b32 v74, v74, 7, v209
	global_load_dwordx4 v[136:139], v74, s[6:7]
	v_lshl_or_b32 v75, v75, 7, v209
	global_load_dwordx4 v[140:143], v75, s[6:7]
	v_lshl_or_b32 v68, v68, 7, v209
	global_load_dwordx4 v[144:147], v68, s[6:7]
	v_lshl_or_b32 v69, v69, 7, v209
	global_load_dwordx4 v[148:151], v69, s[6:7]
	v_lshl_or_b32 v70, v70, 7, v209
	global_load_dwordx4 v[152:155], v70, s[6:7]
	v_lshl_or_b32 v71, v71, 7, v209
	global_load_dwordx4 v[156:159], v71, s[6:7]
	v_lshl_or_b32 v64, v64, 7, v209
	global_load_dwordx4 v[160:163], v64, s[6:7]
	v_lshl_or_b32 v65, v65, 7, v209
	global_load_dwordx4 v[164:167], v65, s[6:7]
	v_lshl_or_b32 v66, v66, 7, v209
	global_load_dwordx4 v[168:171], v66, s[6:7]
	v_lshl_or_b32 v67, v67, 7, v209
	global_load_dwordx4 v[172:175], v67, s[6:7]
	s_add_u32 s20, s12, 0x300
	s_lshl_b32 s20, s20, 9
	v_lshl_add_u64 v[80:81], v[180:181], 0, s[20:21]
	global_load_dwordx4 v[64:67], v[80:81], off offset:48
	global_load_dwordx4 v[68:71], v[80:81], off offset:32
	global_load_dwordx4 v[72:75], v[80:81], off offset:16
	s_nop 0
	global_load_dwordx4 v[80:83], v[80:81], off
	s_mov_b32 s14, s12
	s_waitcnt vmcnt(20)
	v_cvt_pk_f32_fp8_e32 v[200:201], v24
	v_cvt_pk_f32_fp8_sdwa v[202:203], v24 src0_sel:WORD_1
	v_cvt_pk_f32_fp8_e32 v[204:205], v25
	v_lshlrev_b32_e32 v186, 16, v20
	v_and_b32_e32 v187, 0xffff0000, v20
	v_cvt_pk_f32_fp8_sdwa v[210:211], v25 src0_sel:WORD_1
	v_lshlrev_b32_e32 v190, 16, v21
	v_and_b32_e32 v191, 0xffff0000, v21
	v_cvt_pk_f32_fp8_e32 v[212:213], v26
	v_pk_mul_f32 v[200:201], v[200:201], v[186:187]
	v_lshlrev_b32_e32 v194, 16, v22
	v_and_b32_e32 v195, 0xffff0000, v22
	v_cvt_pk_f32_fp8_sdwa v[214:215], v26 src0_sel:WORD_1
	v_pk_fma_f32 v[200:201], v[202:203], v[190:191], v[200:201]
	v_cvt_pk_f32_fp8_e32 v[202:203], v28
	v_lshlrev_b32_e32 v198, 16, v23
	v_and_b32_e32 v199, 0xffff0000, v23
	v_cvt_pk_f32_fp8_e32 v[216:217], v27
	v_pk_fma_f32 v[200:201], v[204:205], v[194:195], v[200:201]
	v_cvt_pk_f32_fp8_sdwa v[204:205], v28 src0_sel:WORD_1
	v_lshlrev_b32_e32 v184, 16, v16
	v_and_b32_e32 v185, 0xffff0000, v16
	v_cvt_pk_f32_fp8_sdwa v[218:219], v27 src0_sel:WORD_1
	v_lshl_or_b32 v0, v0, 7, v209
	global_load_dwordx4 v[24:27], v0, s[6:7]
	v_pk_fma_f32 v[200:201], v[210:211], v[198:199], v[200:201]
	v_cvt_pk_f32_fp8_e32 v[210:211], v29
	v_lshlrev_b32_e32 v188, 16, v17
	v_and_b32_e32 v189, 0xffff0000, v17
	v_pk_fma_f32 v[200:201], v[212:213], v[184:185], v[200:201]
	v_cvt_pk_f32_fp8_sdwa v[212:213], v29 src0_sel:WORD_1
	v_lshlrev_b32_e32 v192, 16, v18
	v_and_b32_e32 v193, 0xffff0000, v18
	v_pk_fma_f32 v[200:201], v[214:215], v[188:189], v[200:201]
	v_cvt_pk_f32_fp8_e32 v[214:215], v30
	v_pk_mul_f32 v[202:203], v[202:203], v[186:187]
	v_lshlrev_b32_e32 v196, 16, v19
	v_and_b32_e32 v197, 0xffff0000, v19
	v_pk_fma_f32 v[200:201], v[216:217], v[192:193], v[200:201]
	v_cvt_pk_f32_fp8_sdwa v[216:217], v30 src0_sel:WORD_1
	v_pk_fma_f32 v[202:203], v[204:205], v[190:191], v[202:203]
	v_cvt_pk_f32_fp8_e32 v[204:205], v32
	v_pk_fma_f32 v[200:201], v[218:219], v[196:197], v[200:201]
	v_cvt_pk_f32_fp8_e32 v[218:219], v31
	v_pk_fma_f32 v[202:203], v[210:211], v[194:195], v[202:203]
	v_cvt_pk_f32_fp8_sdwa v[210:211], v32 src0_sel:WORD_1
	v_cvt_pk_f32_fp8_sdwa v[220:221], v31 src0_sel:WORD_1
	v_lshl_or_b32 v1, v1, 7, v209
	global_load_dwordx4 v[28:31], v1, s[6:7]
	v_pk_fma_f32 v[202:203], v[212:213], v[198:199], v[202:203]
	v_cvt_pk_f32_fp8_e32 v[212:213], v33
	v_pk_fma_f32 v[202:203], v[214:215], v[184:185], v[202:203]
	v_cvt_pk_f32_fp8_sdwa v[214:215], v33 src0_sel:WORD_1
	v_pk_fma_f32 v[202:203], v[216:217], v[188:189], v[202:203]
	v_cvt_pk_f32_fp8_e32 v[216:217], v34
	v_pk_mul_f32 v[204:205], v[204:205], v[186:187]
	v_pk_fma_f32 v[202:203], v[218:219], v[192:193], v[202:203]
	v_cvt_pk_f32_fp8_sdwa v[218:219], v34 src0_sel:WORD_1
	v_pk_fma_f32 v[204:205], v[210:211], v[190:191], v[204:205]
	v_cvt_pk_f32_fp8_e32 v[210:211], v36
	v_pk_fma_f32 v[202:203], v[220:221], v[196:197], v[202:203]
	v_cvt_pk_f32_fp8_e32 v[220:221], v35
	v_pk_fma_f32 v[204:205], v[212:213], v[194:195], v[204:205]
	v_cvt_pk_f32_fp8_sdwa v[212:213], v36 src0_sel:WORD_1
	v_cvt_pk_f32_fp8_sdwa v[222:223], v35 src0_sel:WORD_1
	v_lshl_or_b32 v2, v2, 7, v209
	global_load_dwordx4 v[32:35], v2, s[6:7]
	v_pk_fma_f32 v[204:205], v[214:215], v[198:199], v[204:205]
	v_cvt_pk_f32_fp8_e32 v[214:215], v37
	v_pk_fma_f32 v[204:205], v[216:217], v[184:185], v[204:205]
	v_cvt_pk_f32_fp8_sdwa v[216:217], v37 src0_sel:WORD_1
	v_pk_fma_f32 v[204:205], v[218:219], v[188:189], v[204:205]
	v_cvt_pk_f32_fp8_e32 v[218:219], v38
	v_pk_mul_f32 v[210:211], v[210:211], v[186:187]
	v_pk_fma_f32 v[204:205], v[220:221], v[192:193], v[204:205]
	v_cvt_pk_f32_fp8_sdwa v[220:221], v38 src0_sel:WORD_1
	v_pk_fma_f32 v[210:211], v[212:213], v[190:191], v[210:211]
	v_cvt_pk_f32_fp8_e32 v[212:213], v40
	v_pk_fma_f32 v[204:205], v[222:223], v[196:197], v[204:205]
	v_cvt_pk_f32_fp8_e32 v[222:223], v39
	v_pk_fma_f32 v[210:211], v[214:215], v[194:195], v[210:211]
	v_cvt_pk_f32_fp8_sdwa v[214:215], v40 src0_sel:WORD_1
	v_cvt_pk_f32_fp8_sdwa v[224:225], v39 src0_sel:WORD_1
	v_lshl_or_b32 v3, v3, 7, v209
	global_load_dwordx4 v[36:39], v3, s[6:7]
	v_pk_fma_f32 v[210:211], v[216:217], v[198:199], v[210:211]
	v_cvt_pk_f32_fp8_e32 v[216:217], v41
	v_pk_fma_f32 v[210:211], v[218:219], v[184:185], v[210:211]
	v_cvt_pk_f32_fp8_sdwa v[218:219], v41 src0_sel:WORD_1
	v_pk_fma_f32 v[210:211], v[220:221], v[188:189], v[210:211]
	v_cvt_pk_f32_fp8_e32 v[220:221], v42
	v_pk_mul_f32 v[212:213], v[212:213], v[186:187]
	v_pk_fma_f32 v[210:211], v[222:223], v[192:193], v[210:211]
	v_cvt_pk_f32_fp8_sdwa v[222:223], v42 src0_sel:WORD_1
	v_pk_fma_f32 v[212:213], v[214:215], v[190:191], v[212:213]
	v_cvt_pk_f32_fp8_e32 v[214:215], v44
	v_pk_fma_f32 v[210:211], v[224:225], v[196:197], v[210:211]
	v_cvt_pk_f32_fp8_e32 v[224:225], v43
	v_pk_fma_f32 v[212:213], v[216:217], v[194:195], v[212:213]
	v_cvt_pk_f32_fp8_sdwa v[216:217], v44 src0_sel:WORD_1
	v_cvt_pk_f32_fp8_sdwa v[226:227], v43 src0_sel:WORD_1
	v_lshl_or_b32 v4, v4, 7, v209
	global_load_dwordx4 v[40:43], v4, s[6:7]
	v_pk_fma_f32 v[212:213], v[218:219], v[198:199], v[212:213]
	v_cvt_pk_f32_fp8_e32 v[218:219], v45
	v_pk_fma_f32 v[212:213], v[220:221], v[184:185], v[212:213]
	v_cvt_pk_f32_fp8_sdwa v[220:221], v45 src0_sel:WORD_1
	v_pk_fma_f32 v[212:213], v[222:223], v[188:189], v[212:213]
	v_cvt_pk_f32_fp8_e32 v[222:223], v46
	v_pk_mul_f32 v[214:215], v[214:215], v[186:187]
	v_pk_fma_f32 v[212:213], v[224:225], v[192:193], v[212:213]
	v_cvt_pk_f32_fp8_sdwa v[224:225], v46 src0_sel:WORD_1
	v_pk_fma_f32 v[214:215], v[216:217], v[190:191], v[214:215]
	v_cvt_pk_f32_fp8_e32 v[216:217], v48
	v_pk_fma_f32 v[212:213], v[226:227], v[196:197], v[212:213]
	v_cvt_pk_f32_fp8_e32 v[226:227], v47
	v_pk_fma_f32 v[214:215], v[218:219], v[194:195], v[214:215]
	v_cvt_pk_f32_fp8_sdwa v[218:219], v48 src0_sel:WORD_1
	v_cvt_pk_f32_fp8_sdwa v[228:229], v47 src0_sel:WORD_1
	v_lshl_or_b32 v5, v5, 7, v209
	global_load_dwordx4 v[44:47], v5, s[6:7]
	v_pk_fma_f32 v[214:215], v[220:221], v[198:199], v[214:215]
	v_cvt_pk_f32_fp8_e32 v[220:221], v49
	v_pk_fma_f32 v[214:215], v[222:223], v[184:185], v[214:215]
	v_cvt_pk_f32_fp8_sdwa v[222:223], v49 src0_sel:WORD_1
	v_pk_fma_f32 v[214:215], v[224:225], v[188:189], v[214:215]
	v_cvt_pk_f32_fp8_e32 v[224:225], v50
	v_pk_mul_f32 v[216:217], v[216:217], v[186:187]
	v_pk_fma_f32 v[214:215], v[226:227], v[192:193], v[214:215]
	v_cvt_pk_f32_fp8_sdwa v[226:227], v50 src0_sel:WORD_1
	v_pk_fma_f32 v[216:217], v[218:219], v[190:191], v[216:217]
	v_cvt_pk_f32_fp8_e32 v[218:219], v52
	v_pk_fma_f32 v[214:215], v[228:229], v[196:197], v[214:215]
	v_cvt_pk_f32_fp8_e32 v[228:229], v51
	v_pk_fma_f32 v[216:217], v[220:221], v[194:195], v[216:217]
	v_cvt_pk_f32_fp8_sdwa v[220:221], v52 src0_sel:WORD_1
	v_cvt_pk_f32_fp8_sdwa v[230:231], v51 src0_sel:WORD_1
	v_lshl_or_b32 v6, v6, 7, v209
	global_load_dwordx4 v[48:51], v6, s[6:7]
	v_pk_fma_f32 v[216:217], v[222:223], v[198:199], v[216:217]
	v_cvt_pk_f32_fp8_e32 v[222:223], v53
	v_pk_fma_f32 v[216:217], v[224:225], v[184:185], v[216:217]
	v_cvt_pk_f32_fp8_sdwa v[224:225], v53 src0_sel:WORD_1
	v_pk_fma_f32 v[216:217], v[226:227], v[188:189], v[216:217]
	v_cvt_pk_f32_fp8_e32 v[226:227], v54
	v_pk_mul_f32 v[218:219], v[218:219], v[186:187]
	v_pk_fma_f32 v[216:217], v[228:229], v[192:193], v[216:217]
	v_cvt_pk_f32_fp8_sdwa v[228:229], v54 src0_sel:WORD_1
	v_pk_fma_f32 v[218:219], v[220:221], v[190:191], v[218:219]
	v_cvt_pk_f32_fp8_e32 v[220:221], v56
	v_pk_fma_f32 v[216:217], v[230:231], v[196:197], v[216:217]
	v_cvt_pk_f32_fp8_e32 v[230:231], v55
	v_pk_fma_f32 v[218:219], v[222:223], v[194:195], v[218:219]
	v_cvt_pk_f32_fp8_sdwa v[222:223], v56 src0_sel:WORD_1
	v_cvt_pk_f32_fp8_sdwa v[232:233], v55 src0_sel:WORD_1
	v_lshl_or_b32 v7, v7, 7, v209
	global_load_dwordx4 v[52:55], v7, s[6:7]
	v_pk_fma_f32 v[218:219], v[224:225], v[198:199], v[218:219]
	v_cvt_pk_f32_fp8_e32 v[224:225], v57
	v_pk_fma_f32 v[218:219], v[226:227], v[184:185], v[218:219]
	v_cvt_pk_f32_fp8_sdwa v[226:227], v57 src0_sel:WORD_1
	v_pk_fma_f32 v[218:219], v[228:229], v[188:189], v[218:219]
	v_cvt_pk_f32_fp8_e32 v[228:229], v58
	v_pk_mul_f32 v[220:221], v[220:221], v[186:187]
	v_pk_fma_f32 v[218:219], v[230:231], v[192:193], v[218:219]
	v_cvt_pk_f32_fp8_sdwa v[230:231], v58 src0_sel:WORD_1
	v_pk_fma_f32 v[220:221], v[222:223], v[190:191], v[220:221]
	v_cvt_pk_f32_fp8_e32 v[222:223], v60
	v_pk_fma_f32 v[218:219], v[232:233], v[196:197], v[218:219]
	v_cvt_pk_f32_fp8_e32 v[232:233], v59
	v_pk_fma_f32 v[220:221], v[224:225], v[194:195], v[220:221]
	v_cvt_pk_f32_fp8_sdwa v[224:225], v60 src0_sel:WORD_1
	v_cvt_pk_f32_fp8_sdwa v[234:235], v59 src0_sel:WORD_1
	v_lshl_or_b32 v8, v8, 7, v209
	global_load_dwordx4 v[56:59], v8, s[6:7]
	v_pk_fma_f32 v[220:221], v[226:227], v[198:199], v[220:221]
	v_cvt_pk_f32_fp8_e32 v[226:227], v61
	v_pk_fma_f32 v[220:221], v[228:229], v[184:185], v[220:221]
	v_cvt_pk_f32_fp8_sdwa v[228:229], v61 src0_sel:WORD_1
	v_pk_fma_f32 v[220:221], v[230:231], v[188:189], v[220:221]
	v_cvt_pk_f32_fp8_e32 v[230:231], v62
	v_pk_mul_f32 v[222:223], v[222:223], v[186:187]
	v_pk_fma_f32 v[220:221], v[232:233], v[192:193], v[220:221]
	v_cvt_pk_f32_fp8_sdwa v[232:233], v62 src0_sel:WORD_1
	v_pk_fma_f32 v[222:223], v[224:225], v[190:191], v[222:223]
	v_cvt_pk_f32_fp8_e32 v[224:225], v76
	v_pk_fma_f32 v[220:221], v[234:235], v[196:197], v[220:221]
	v_cvt_pk_f32_fp8_e32 v[234:235], v63
	v_pk_fma_f32 v[222:223], v[226:227], v[194:195], v[222:223]
	v_cvt_pk_f32_fp8_sdwa v[226:227], v76 src0_sel:WORD_1
	v_cvt_pk_f32_fp8_sdwa v[236:237], v63 src0_sel:WORD_1
	v_lshl_or_b32 v9, v9, 7, v209
	global_load_dwordx4 v[60:63], v9, s[6:7]
	v_pk_fma_f32 v[222:223], v[228:229], v[198:199], v[222:223]
	v_cvt_pk_f32_fp8_e32 v[228:229], v77
	v_pk_fma_f32 v[222:223], v[230:231], v[184:185], v[222:223]
	v_cvt_pk_f32_fp8_sdwa v[230:231], v77 src0_sel:WORD_1
	v_pk_fma_f32 v[222:223], v[232:233], v[188:189], v[222:223]
	v_cvt_pk_f32_fp8_e32 v[232:233], v78
	v_pk_mul_f32 v[224:225], v[224:225], v[186:187]
	v_pk_fma_f32 v[222:223], v[234:235], v[192:193], v[222:223]
	v_cvt_pk_f32_fp8_sdwa v[234:235], v78 src0_sel:WORD_1
	v_pk_fma_f32 v[224:225], v[226:227], v[190:191], v[224:225]
	v_cvt_pk_f32_fp8_e32 v[226:227], v84
	v_pk_fma_f32 v[222:223], v[236:237], v[196:197], v[222:223]
	v_cvt_pk_f32_fp8_e32 v[236:237], v79
	v_pk_fma_f32 v[224:225], v[228:229], v[194:195], v[224:225]
	v_cvt_pk_f32_fp8_sdwa v[228:229], v84 src0_sel:WORD_1
	v_cvt_pk_f32_fp8_sdwa v[238:239], v79 src0_sel:WORD_1
	v_lshl_or_b32 v10, v10, 7, v209
	global_load_dwordx4 v[76:79], v10, s[6:7]
	v_pk_fma_f32 v[224:225], v[230:231], v[198:199], v[224:225]
	v_cvt_pk_f32_fp8_e32 v[230:231], v85
	v_pk_fma_f32 v[224:225], v[232:233], v[184:185], v[224:225]
	v_cvt_pk_f32_fp8_sdwa v[232:233], v85 src0_sel:WORD_1
	v_pk_fma_f32 v[224:225], v[234:235], v[188:189], v[224:225]
	v_cvt_pk_f32_fp8_e32 v[234:235], v86
	v_pk_mul_f32 v[226:227], v[226:227], v[186:187]
	v_pk_fma_f32 v[224:225], v[236:237], v[192:193], v[224:225]
	v_cvt_pk_f32_fp8_sdwa v[236:237], v86 src0_sel:WORD_1
	v_pk_fma_f32 v[226:227], v[228:229], v[190:191], v[226:227]
	v_cvt_pk_f32_fp8_e32 v[228:229], v88
	v_pk_fma_f32 v[224:225], v[238:239], v[196:197], v[224:225]
	v_cvt_pk_f32_fp8_e32 v[238:239], v87
	v_pk_fma_f32 v[226:227], v[230:231], v[194:195], v[226:227]
	v_cvt_pk_f32_fp8_sdwa v[230:231], v88 src0_sel:WORD_1
	v_cvt_pk_f32_fp8_sdwa v[240:241], v87 src0_sel:WORD_1
	v_lshl_or_b32 v11, v11, 7, v209
	global_load_dwordx4 v[84:87], v11, s[6:7]
	v_pk_fma_f32 v[226:227], v[232:233], v[198:199], v[226:227]
	v_cvt_pk_f32_fp8_e32 v[232:233], v89
	v_pk_fma_f32 v[226:227], v[234:235], v[184:185], v[226:227]
	v_cvt_pk_f32_fp8_sdwa v[234:235], v89 src0_sel:WORD_1
	v_pk_fma_f32 v[226:227], v[236:237], v[188:189], v[226:227]
	v_cvt_pk_f32_fp8_e32 v[236:237], v90
	v_pk_mul_f32 v[228:229], v[228:229], v[186:187]
	v_pk_fma_f32 v[226:227], v[238:239], v[192:193], v[226:227]
	v_cvt_pk_f32_fp8_sdwa v[238:239], v90 src0_sel:WORD_1
	v_pk_fma_f32 v[228:229], v[230:231], v[190:191], v[228:229]
	v_cvt_pk_f32_fp8_e32 v[230:231], v92
	v_pk_fma_f32 v[226:227], v[240:241], v[196:197], v[226:227]
	v_cvt_pk_f32_fp8_e32 v[240:241], v91
	v_pk_fma_f32 v[228:229], v[232:233], v[194:195], v[228:229]
	v_cvt_pk_f32_fp8_sdwa v[232:233], v92 src0_sel:WORD_1
	v_cvt_pk_f32_fp8_sdwa v[242:243], v91 src0_sel:WORD_1
	v_lshl_or_b32 v12, v12, 7, v209
	global_load_dwordx4 v[88:91], v12, s[6:7]
	v_pk_fma_f32 v[228:229], v[234:235], v[198:199], v[228:229]
	v_cvt_pk_f32_fp8_e32 v[234:235], v93
	v_pk_fma_f32 v[228:229], v[236:237], v[184:185], v[228:229]
	v_cvt_pk_f32_fp8_sdwa v[236:237], v93 src0_sel:WORD_1
	v_pk_fma_f32 v[228:229], v[238:239], v[188:189], v[228:229]
	v_cvt_pk_f32_fp8_e32 v[238:239], v94
	v_pk_mul_f32 v[230:231], v[230:231], v[186:187]
	v_pk_fma_f32 v[228:229], v[240:241], v[192:193], v[228:229]
	v_cvt_pk_f32_fp8_sdwa v[240:241], v94 src0_sel:WORD_1
	v_pk_fma_f32 v[230:231], v[232:233], v[190:191], v[230:231]
	v_cvt_pk_f32_fp8_e32 v[232:233], v96
	v_pk_fma_f32 v[228:229], v[242:243], v[196:197], v[228:229]
	v_cvt_pk_f32_fp8_e32 v[242:243], v95
	v_pk_fma_f32 v[230:231], v[234:235], v[194:195], v[230:231]
	v_cvt_pk_f32_fp8_sdwa v[234:235], v96 src0_sel:WORD_1
	v_cvt_pk_f32_fp8_sdwa v[244:245], v95 src0_sel:WORD_1
	v_lshl_or_b32 v13, v13, 7, v209
	global_load_dwordx4 v[92:95], v13, s[6:7]
	v_pk_fma_f32 v[230:231], v[236:237], v[198:199], v[230:231]
	v_cvt_pk_f32_fp8_e32 v[236:237], v97
	v_pk_fma_f32 v[230:231], v[238:239], v[184:185], v[230:231]
	v_cvt_pk_f32_fp8_sdwa v[238:239], v97 src0_sel:WORD_1
	v_pk_fma_f32 v[230:231], v[240:241], v[188:189], v[230:231]
	v_cvt_pk_f32_fp8_e32 v[240:241], v98
	v_pk_mul_f32 v[232:233], v[232:233], v[186:187]
	v_pk_fma_f32 v[230:231], v[242:243], v[192:193], v[230:231]
	v_cvt_pk_f32_fp8_sdwa v[242:243], v98 src0_sel:WORD_1
	v_pk_fma_f32 v[232:233], v[234:235], v[190:191], v[232:233]
	v_cvt_pk_f32_fp8_e32 v[234:235], v104
	v_pk_fma_f32 v[230:231], v[244:245], v[196:197], v[230:231]
	v_cvt_pk_f32_fp8_e32 v[244:245], v99
	v_pk_fma_f32 v[232:233], v[236:237], v[194:195], v[232:233]
	v_cvt_pk_f32_fp8_sdwa v[236:237], v104 src0_sel:WORD_1
	v_cvt_pk_f32_fp8_sdwa v[246:247], v99 src0_sel:WORD_1
	v_lshl_or_b32 v14, v14, 7, v209
	global_load_dwordx4 v[96:99], v14, s[6:7]
	v_pk_fma_f32 v[232:233], v[238:239], v[198:199], v[232:233]
	v_cvt_pk_f32_fp8_e32 v[238:239], v105
	v_pk_fma_f32 v[232:233], v[240:241], v[184:185], v[232:233]
	v_cvt_pk_f32_fp8_sdwa v[240:241], v105 src0_sel:WORD_1
	v_pk_fma_f32 v[232:233], v[242:243], v[188:189], v[232:233]
	v_cvt_pk_f32_fp8_e32 v[242:243], v106
	v_pk_mul_f32 v[186:187], v[234:235], v[186:187]
	v_pk_fma_f32 v[232:233], v[244:245], v[192:193], v[232:233]
	v_cvt_pk_f32_fp8_sdwa v[244:245], v106 src0_sel:WORD_1
	v_pk_fma_f32 v[186:187], v[236:237], v[190:191], v[186:187]
	v_pk_fma_f32 v[232:233], v[246:247], v[196:197], v[232:233]
	v_cvt_pk_f32_fp8_e32 v[246:247], v107
	v_pk_fma_f32 v[186:187], v[238:239], v[194:195], v[186:187]
	v_cvt_pk_f32_fp8_sdwa v[248:249], v107 src0_sel:WORD_1
	v_lshl_or_b32 v15, v15, 7, v209
	global_load_dwordx4 v[104:107], v15, s[6:7]
	v_pk_fma_f32 v[186:187], v[240:241], v[198:199], v[186:187]
	v_mov_b32_e32 v194, v220
	v_pk_fma_f32 v[184:185], v[242:243], v[184:185], v[186:187]
	v_mov_b32_e32 v186, v200
	v_pk_fma_f32 v[184:185], v[244:245], v[188:189], v[184:185]
	v_mov_b32_e32 v187, v202
	v_pk_fma_f32 v[184:185], v[246:247], v[192:193], v[184:185]
	v_mov_b32_e32 v202, v201
	v_pk_fma_f32 v[184:185], v[248:249], v[196:197], v[184:185]
	v_mov_b32_e32 v195, v222
	v_mov_b32_e32 v222, v221
	v_pk_add_f32 v[186:187], v[186:187], v[202:203]
	v_pk_add_f32 v[194:195], v[194:195], v[222:223]
	v_mov_b32_e32 v200, v232
	v_mov_b32_e32 v201, v184
	v_mov_b32_e32 v184, v233
	v_mov_b32_e32 v188, v204
	v_mov_b32_e32 v189, v210
	v_mov_b32_e32 v210, v205
	v_mov_b32_e32 v196, v224
	v_mov_b32_e32 v197, v226
	v_mov_b32_e32 v226, v225
	v_pk_add_f32 v[184:185], v[200:201], v[184:185]
	v_cndmask_b32_e64 v200, v186, v194, s[4:5]
	v_cndmask_b32_e64 v202, v194, v186, s[4:5]
	v_cndmask_b32_e64 v186, v187, v195, s[4:5]
	v_pk_add_f32 v[188:189], v[188:189], v[210:211]
	v_pk_add_f32 v[196:197], v[196:197], v[226:227]
	v_mov_b32_dpp v200, v200 row_half_mirror row_mask:0xf bank_mask:0xf bound_ctrl:1
	v_cndmask_b32_e64 v203, v195, v187, s[4:5]
	v_mov_b32_dpp v201, v186 row_half_mirror row_mask:0xf bank_mask:0xf bound_ctrl:1
	v_mov_b32_e32 v190, v212
	v_mov_b32_e32 v191, v214
	v_mov_b32_e32 v214, v213
	v_mov_b32_e32 v198, v228
	v_mov_b32_e32 v199, v230
	v_mov_b32_e32 v230, v229
	v_pk_add_f32 v[186:187], v[202:203], v[200:201]
	v_cndmask_b32_e64 v194, v188, v196, s[4:5]
	v_cndmask_b32_e64 v200, v196, v188, s[4:5]
	v_cndmask_b32_e64 v188, v189, v197, s[4:5]
	v_pk_add_f32 v[190:191], v[190:191], v[214:215]
	v_pk_add_f32 v[198:199], v[198:199], v[230:231]
	v_mov_b32_dpp v194, v194 row_half_mirror row_mask:0xf bank_mask:0xf bound_ctrl:1
	v_cndmask_b32_e64 v201, v197, v189, s[4:5]
	v_mov_b32_dpp v195, v188 row_half_mirror row_mask:0xf bank_mask:0xf bound_ctrl:1
	v_mov_b32_e32 v192, v216
	v_mov_b32_e32 v193, v218
	v_mov_b32_e32 v218, v217
	v_pk_add_f32 v[188:189], v[200:201], v[194:195]
	v_cndmask_b32_e64 v194, v190, v198, s[4:5]
	v_cndmask_b32_e64 v196, v198, v190, s[4:5]
	v_cndmask_b32_e64 v190, v191, v199, s[4:5]
	v_pk_add_f32 v[192:193], v[192:193], v[218:219]
	v_mov_b32_dpp v194, v194 row_half_mirror row_mask:0xf bank_mask:0xf bound_ctrl:1
	v_cndmask_b32_e64 v197, v199, v191, s[4:5]
	v_mov_b32_dpp v195, v190 row_half_mirror row_mask:0xf bank_mask:0xf bound_ctrl:1
	v_pk_add_f32 v[190:191], v[196:197], v[194:195]
	v_cndmask_b32_e64 v194, v192, v184, s[4:5]
	v_cndmask_b32_e64 v196, v184, v192, s[4:5]
	v_cndmask_b32_e64 v184, v193, v185, s[4:5]
	v_mov_b32_dpp v194, v194 row_half_mirror row_mask:0xf bank_mask:0xf bound_ctrl:1
	v_cndmask_b32_e64 v197, v185, v193, s[4:5]
	v_mov_b32_dpp v195, v184 row_half_mirror row_mask:0xf bank_mask:0xf bound_ctrl:1
	v_pk_add_f32 v[184:185], v[196:197], v[194:195]
	v_cndmask_b32_e64 v192, v186, v190, s[2:3]
	v_cndmask_b32_e64 v194, v190, v186, s[2:3]
	v_cndmask_b32_e64 v186, v187, v191, s[2:3]
	v_mov_b32_dpp v192, v192 quad_perm:[2,3,0,1] row_mask:0xf bank_mask:0xf bound_ctrl:1
	v_cndmask_b32_e64 v195, v191, v187, s[2:3]
	v_mov_b32_dpp v193, v186 quad_perm:[2,3,0,1] row_mask:0xf bank_mask:0xf bound_ctrl:1
	v_pk_add_f32 v[186:187], v[194:195], v[192:193]
	v_cndmask_b32_e64 v190, v188, v184, s[2:3]
	v_cndmask_b32_e64 v192, v184, v188, s[2:3]
	v_cndmask_b32_e64 v184, v189, v185, s[2:3]
	v_mov_b32_dpp v190, v190 quad_perm:[2,3,0,1] row_mask:0xf bank_mask:0xf bound_ctrl:1
	v_cndmask_b32_e64 v193, v185, v189, s[2:3]
	v_mov_b32_dpp v191, v184 quad_perm:[2,3,0,1] row_mask:0xf bank_mask:0xf bound_ctrl:1
	v_pk_add_f32 v[184:185], v[192:193], v[190:191]
	s_ashr_i32 s15, s14, 31
	v_cndmask_b32_e64 v188, v186, v184, s[0:1]
	v_cndmask_b32_e64 v190, v184, v186, s[0:1]
	v_cndmask_b32_e64 v184, v187, v185, s[0:1]
	v_mov_b32_dpp v188, v188 quad_perm:[1,0,3,2] row_mask:0xf bank_mask:0xf bound_ctrl:1
	v_cndmask_b32_e64 v191, v185, v187, s[0:1]
	v_mov_b32_dpp v189, v184 quad_perm:[1,0,3,2] row_mask:0xf bank_mask:0xf bound_ctrl:1
	v_pk_add_f32 v[184:185], v[190:191], v[188:189]
	s_lshl_b64 s[14:15], s[14:15], 8
	v_cvt_pk_bf16_f32 v186, v184, v185
	v_lshl_add_u64 v[184:185], v[178:179], 0, s[14:15]
	global_store_dword v[184:185], v186, off
	s_add_u32 s20, s12, 0x200
	s_lshl_b32 s20, s20, 11
	v_lshl_add_u64 v[20:21], v[182:183], 0, s[20:21]
	global_load_dwordx4 v[16:19], v[20:21], off offset:16
	s_nop 0
	global_load_dwordx4 v[20:23], v[20:21], off
	s_add_u32 s20, s12, 0x400
	s_lshl_b32 s20, s20, 9
	v_lshl_add_u64 v[0:1], v[180:181], 0, s[20:21]
	global_load_dwordx4 v[12:15], v[0:1], off offset:48
	global_load_dwordx4 v[8:11], v[0:1], off offset:32
	global_load_dwordx4 v[4:7], v[0:1], off offset:16
	s_nop 0
	global_load_dwordx4 v[0:3], v[0:1], off
	s_add_u32 s10, s12, 0x100
	s_waitcnt vmcnt(23)
	v_cvt_pk_f32_fp8_e32 v[200:201], v112
	v_cvt_pk_f32_fp8_sdwa v[202:203], v112 src0_sel:WORD_1
	v_cvt_pk_f32_fp8_e32 v[204:205], v113
	v_lshlrev_b32_e32 v186, 16, v108
	v_and_b32_e32 v187, 0xffff0000, v108
	v_cvt_pk_f32_fp8_sdwa v[210:211], v113 src0_sel:WORD_1
	v_lshlrev_b32_e32 v190, 16, v109
	v_and_b32_e32 v191, 0xffff0000, v109
	v_cvt_pk_f32_fp8_e32 v[212:213], v114
	v_pk_mul_f32 v[200:201], v[200:201], v[186:187]
	v_lshlrev_b32_e32 v194, 16, v110
	v_and_b32_e32 v195, 0xffff0000, v110
	v_cvt_pk_f32_fp8_sdwa v[214:215], v114 src0_sel:WORD_1
	v_pk_fma_f32 v[200:201], v[202:203], v[190:191], v[200:201]
	v_cvt_pk_f32_fp8_e32 v[202:203], v116
	v_lshlrev_b32_e32 v198, 16, v111
	v_and_b32_e32 v199, 0xffff0000, v111
	v_cvt_pk_f32_fp8_e32 v[216:217], v115
	v_pk_fma_f32 v[200:201], v[204:205], v[194:195], v[200:201]
	v_cvt_pk_f32_fp8_sdwa v[204:205], v116 src0_sel:WORD_1
	v_lshlrev_b32_e32 v184, 16, v100
	v_and_b32_e32 v185, 0xffff0000, v100
	v_cvt_pk_f32_fp8_sdwa v[218:219], v115 src0_sel:WORD_1
	v_lshl_or_b32 v80, v80, 7, v209
	global_load_dwordx4 v[112:115], v80, s[6:7]
	v_pk_fma_f32 v[200:201], v[210:211], v[198:199], v[200:201]
	v_cvt_pk_f32_fp8_e32 v[210:211], v117
	v_lshlrev_b32_e32 v188, 16, v101
	v_and_b32_e32 v189, 0xffff0000, v101
	v_pk_fma_f32 v[200:201], v[212:213], v[184:185], v[200:201]
	v_cvt_pk_f32_fp8_sdwa v[212:213], v117 src0_sel:WORD_1
	v_lshlrev_b32_e32 v192, 16, v102
	v_and_b32_e32 v193, 0xffff0000, v102
	v_pk_fma_f32 v[200:201], v[214:215], v[188:189], v[200:201]
	v_cvt_pk_f32_fp8_e32 v[214:215], v118
	v_pk_mul_f32 v[202:203], v[202:203], v[186:187]
	v_lshlrev_b32_e32 v196, 16, v103
	v_and_b32_e32 v197, 0xffff0000, v103
	v_pk_fma_f32 v[200:201], v[216:217], v[192:193], v[200:201]
	v_cvt_pk_f32_fp8_sdwa v[216:217], v118 src0_sel:WORD_1
	v_pk_fma_f32 v[202:203], v[204:205], v[190:191], v[202:203]
	v_cvt_pk_f32_fp8_e32 v[204:205], v120
	v_pk_fma_f32 v[200:201], v[218:219], v[196:197], v[200:201]
	v_cvt_pk_f32_fp8_e32 v[218:219], v119
	v_pk_fma_f32 v[202:203], v[210:211], v[194:195], v[202:203]
	v_cvt_pk_f32_fp8_sdwa v[210:211], v120 src0_sel:WORD_1
	v_cvt_pk_f32_fp8_sdwa v[220:221], v119 src0_sel:WORD_1
	v_lshl_or_b32 v81, v81, 7, v209
	global_load_dwordx4 v[116:119], v81, s[6:7]
	v_pk_fma_f32 v[202:203], v[212:213], v[198:199], v[202:203]
	v_cvt_pk_f32_fp8_e32 v[212:213], v121
	v_pk_fma_f32 v[202:203], v[214:215], v[184:185], v[202:203]
	v_cvt_pk_f32_fp8_sdwa v[214:215], v121 src0_sel:WORD_1
	v_pk_fma_f32 v[202:203], v[216:217], v[188:189], v[202:203]
	v_cvt_pk_f32_fp8_e32 v[216:217], v122
	v_pk_mul_f32 v[204:205], v[204:205], v[186:187]
	v_pk_fma_f32 v[202:203], v[218:219], v[192:193], v[202:203]
	v_cvt_pk_f32_fp8_sdwa v[218:219], v122 src0_sel:WORD_1
	v_pk_fma_f32 v[204:205], v[210:211], v[190:191], v[204:205]
	v_cvt_pk_f32_fp8_e32 v[210:211], v124
	v_pk_fma_f32 v[202:203], v[220:221], v[196:197], v[202:203]
	v_cvt_pk_f32_fp8_e32 v[220:221], v123
	v_pk_fma_f32 v[204:205], v[212:213], v[194:195], v[204:205]
	v_cvt_pk_f32_fp8_sdwa v[212:213], v124 src0_sel:WORD_1
	v_cvt_pk_f32_fp8_sdwa v[222:223], v123 src0_sel:WORD_1
	v_lshl_or_b32 v82, v82, 7, v209
	global_load_dwordx4 v[120:123], v82, s[6:7]
	v_pk_fma_f32 v[204:205], v[214:215], v[198:199], v[204:205]
	v_cvt_pk_f32_fp8_e32 v[214:215], v125
	v_pk_fma_f32 v[204:205], v[216:217], v[184:185], v[204:205]
	v_cvt_pk_f32_fp8_sdwa v[216:217], v125 src0_sel:WORD_1
	v_pk_fma_f32 v[204:205], v[218:219], v[188:189], v[204:205]
	v_cvt_pk_f32_fp8_e32 v[218:219], v126
	v_pk_mul_f32 v[210:211], v[210:211], v[186:187]
	v_pk_fma_f32 v[204:205], v[220:221], v[192:193], v[204:205]
	v_cvt_pk_f32_fp8_sdwa v[220:221], v126 src0_sel:WORD_1
	v_pk_fma_f32 v[210:211], v[212:213], v[190:191], v[210:211]
	v_cvt_pk_f32_fp8_e32 v[212:213], v128
	v_pk_fma_f32 v[204:205], v[222:223], v[196:197], v[204:205]
	v_cvt_pk_f32_fp8_e32 v[222:223], v127
	v_pk_fma_f32 v[210:211], v[214:215], v[194:195], v[210:211]
	v_cvt_pk_f32_fp8_sdwa v[214:215], v128 src0_sel:WORD_1
	v_cvt_pk_f32_fp8_sdwa v[224:225], v127 src0_sel:WORD_1
	v_lshl_or_b32 v83, v83, 7, v209
	global_load_dwordx4 v[124:127], v83, s[6:7]
	v_pk_fma_f32 v[210:211], v[216:217], v[198:199], v[210:211]
	v_cvt_pk_f32_fp8_e32 v[216:217], v129
	v_pk_fma_f32 v[210:211], v[218:219], v[184:185], v[210:211]
	v_cvt_pk_f32_fp8_sdwa v[218:219], v129 src0_sel:WORD_1
	v_pk_fma_f32 v[210:211], v[220:221], v[188:189], v[210:211]
	v_cvt_pk_f32_fp8_e32 v[220:221], v130
	v_pk_mul_f32 v[212:213], v[212:213], v[186:187]
	v_pk_fma_f32 v[210:211], v[222:223], v[192:193], v[210:211]
	v_cvt_pk_f32_fp8_sdwa v[222:223], v130 src0_sel:WORD_1
	v_pk_fma_f32 v[212:213], v[214:215], v[190:191], v[212:213]
	v_cvt_pk_f32_fp8_e32 v[214:215], v132
	v_pk_fma_f32 v[210:211], v[224:225], v[196:197], v[210:211]
	v_cvt_pk_f32_fp8_e32 v[224:225], v131
	v_pk_fma_f32 v[212:213], v[216:217], v[194:195], v[212:213]
	v_cvt_pk_f32_fp8_sdwa v[216:217], v132 src0_sel:WORD_1
	v_cvt_pk_f32_fp8_sdwa v[226:227], v131 src0_sel:WORD_1
	v_lshl_or_b32 v72, v72, 7, v209
	global_load_dwordx4 v[128:131], v72, s[6:7]
	v_pk_fma_f32 v[212:213], v[218:219], v[198:199], v[212:213]
	v_cvt_pk_f32_fp8_e32 v[218:219], v133
	v_pk_fma_f32 v[212:213], v[220:221], v[184:185], v[212:213]
	v_cvt_pk_f32_fp8_sdwa v[220:221], v133 src0_sel:WORD_1
	v_pk_fma_f32 v[212:213], v[222:223], v[188:189], v[212:213]
	v_cvt_pk_f32_fp8_e32 v[222:223], v134
	v_pk_mul_f32 v[214:215], v[214:215], v[186:187]
	v_pk_fma_f32 v[212:213], v[224:225], v[192:193], v[212:213]
	v_cvt_pk_f32_fp8_sdwa v[224:225], v134 src0_sel:WORD_1
	v_pk_fma_f32 v[214:215], v[216:217], v[190:191], v[214:215]
	v_cvt_pk_f32_fp8_e32 v[216:217], v136
	v_pk_fma_f32 v[212:213], v[226:227], v[196:197], v[212:213]
	v_cvt_pk_f32_fp8_e32 v[226:227], v135
	v_pk_fma_f32 v[214:215], v[218:219], v[194:195], v[214:215]
	v_cvt_pk_f32_fp8_sdwa v[218:219], v136 src0_sel:WORD_1
	v_cvt_pk_f32_fp8_sdwa v[228:229], v135 src0_sel:WORD_1
	v_lshl_or_b32 v73, v73, 7, v209
	global_load_dwordx4 v[132:135], v73, s[6:7]
	v_pk_fma_f32 v[214:215], v[220:221], v[198:199], v[214:215]
	v_cvt_pk_f32_fp8_e32 v[220:221], v137
	v_pk_fma_f32 v[214:215], v[222:223], v[184:185], v[214:215]
	v_cvt_pk_f32_fp8_sdwa v[222:223], v137 src0_sel:WORD_1
	v_pk_fma_f32 v[214:215], v[224:225], v[188:189], v[214:215]
	v_cvt_pk_f32_fp8_e32 v[224:225], v138
	v_pk_mul_f32 v[216:217], v[216:217], v[186:187]
	v_pk_fma_f32 v[214:215], v[226:227], v[192:193], v[214:215]
	v_cvt_pk_f32_fp8_sdwa v[226:227], v138 src0_sel:WORD_1
	v_pk_fma_f32 v[216:217], v[218:219], v[190:191], v[216:217]
	v_cvt_pk_f32_fp8_e32 v[218:219], v140
	v_pk_fma_f32 v[214:215], v[228:229], v[196:197], v[214:215]
	v_cvt_pk_f32_fp8_e32 v[228:229], v139
	v_pk_fma_f32 v[216:217], v[220:221], v[194:195], v[216:217]
	v_cvt_pk_f32_fp8_sdwa v[220:221], v140 src0_sel:WORD_1
	v_cvt_pk_f32_fp8_sdwa v[230:231], v139 src0_sel:WORD_1
	v_lshl_or_b32 v74, v74, 7, v209
	global_load_dwordx4 v[136:139], v74, s[6:7]
	v_pk_fma_f32 v[216:217], v[222:223], v[198:199], v[216:217]
	v_cvt_pk_f32_fp8_e32 v[222:223], v141
	v_pk_fma_f32 v[216:217], v[224:225], v[184:185], v[216:217]
	v_cvt_pk_f32_fp8_sdwa v[224:225], v141 src0_sel:WORD_1
	v_pk_fma_f32 v[216:217], v[226:227], v[188:189], v[216:217]
	v_cvt_pk_f32_fp8_e32 v[226:227], v142
	v_pk_mul_f32 v[218:219], v[218:219], v[186:187]
	v_pk_fma_f32 v[216:217], v[228:229], v[192:193], v[216:217]
	v_cvt_pk_f32_fp8_sdwa v[228:229], v142 src0_sel:WORD_1
	v_pk_fma_f32 v[218:219], v[220:221], v[190:191], v[218:219]
	v_cvt_pk_f32_fp8_e32 v[220:221], v144
	v_pk_fma_f32 v[216:217], v[230:231], v[196:197], v[216:217]
	v_cvt_pk_f32_fp8_e32 v[230:231], v143
	v_pk_fma_f32 v[218:219], v[222:223], v[194:195], v[218:219]
	v_cvt_pk_f32_fp8_sdwa v[222:223], v144 src0_sel:WORD_1
	v_cvt_pk_f32_fp8_sdwa v[232:233], v143 src0_sel:WORD_1
	v_lshl_or_b32 v75, v75, 7, v209
	global_load_dwordx4 v[140:143], v75, s[6:7]
	v_pk_fma_f32 v[218:219], v[224:225], v[198:199], v[218:219]
	v_cvt_pk_f32_fp8_e32 v[224:225], v145
	v_pk_fma_f32 v[218:219], v[226:227], v[184:185], v[218:219]
	v_cvt_pk_f32_fp8_sdwa v[226:227], v145 src0_sel:WORD_1
	v_pk_fma_f32 v[218:219], v[228:229], v[188:189], v[218:219]
	v_cvt_pk_f32_fp8_e32 v[228:229], v146
	v_pk_mul_f32 v[220:221], v[220:221], v[186:187]
	v_pk_fma_f32 v[218:219], v[230:231], v[192:193], v[218:219]
	v_cvt_pk_f32_fp8_sdwa v[230:231], v146 src0_sel:WORD_1
	v_pk_fma_f32 v[220:221], v[222:223], v[190:191], v[220:221]
	v_cvt_pk_f32_fp8_e32 v[222:223], v148
	v_pk_fma_f32 v[218:219], v[232:233], v[196:197], v[218:219]
	v_cvt_pk_f32_fp8_e32 v[232:233], v147
	v_pk_fma_f32 v[220:221], v[224:225], v[194:195], v[220:221]
	v_cvt_pk_f32_fp8_sdwa v[224:225], v148 src0_sel:WORD_1
	v_cvt_pk_f32_fp8_sdwa v[234:235], v147 src0_sel:WORD_1
	v_lshl_or_b32 v68, v68, 7, v209
	global_load_dwordx4 v[144:147], v68, s[6:7]
	v_pk_fma_f32 v[220:221], v[226:227], v[198:199], v[220:221]
	v_cvt_pk_f32_fp8_e32 v[226:227], v149
	v_pk_fma_f32 v[220:221], v[228:229], v[184:185], v[220:221]
	v_cvt_pk_f32_fp8_sdwa v[228:229], v149 src0_sel:WORD_1
	v_pk_fma_f32 v[220:221], v[230:231], v[188:189], v[220:221]
	v_cvt_pk_f32_fp8_e32 v[230:231], v150
	v_pk_mul_f32 v[222:223], v[222:223], v[186:187]
	v_pk_fma_f32 v[220:221], v[232:233], v[192:193], v[220:221]
	v_cvt_pk_f32_fp8_sdwa v[232:233], v150 src0_sel:WORD_1
	v_pk_fma_f32 v[222:223], v[224:225], v[190:191], v[222:223]
	v_cvt_pk_f32_fp8_e32 v[224:225], v152
	v_pk_fma_f32 v[220:221], v[234:235], v[196:197], v[220:221]
	v_cvt_pk_f32_fp8_e32 v[234:235], v151
	v_pk_fma_f32 v[222:223], v[226:227], v[194:195], v[222:223]
	v_cvt_pk_f32_fp8_sdwa v[226:227], v152 src0_sel:WORD_1
	v_cvt_pk_f32_fp8_sdwa v[236:237], v151 src0_sel:WORD_1
	v_lshl_or_b32 v69, v69, 7, v209
	global_load_dwordx4 v[148:151], v69, s[6:7]
	v_pk_fma_f32 v[222:223], v[228:229], v[198:199], v[222:223]
	v_cvt_pk_f32_fp8_e32 v[228:229], v153
	v_pk_fma_f32 v[222:223], v[230:231], v[184:185], v[222:223]
	v_cvt_pk_f32_fp8_sdwa v[230:231], v153 src0_sel:WORD_1
	v_pk_fma_f32 v[222:223], v[232:233], v[188:189], v[222:223]
	v_cvt_pk_f32_fp8_e32 v[232:233], v154
	v_pk_mul_f32 v[224:225], v[224:225], v[186:187]
	v_pk_fma_f32 v[222:223], v[234:235], v[192:193], v[222:223]
	v_cvt_pk_f32_fp8_sdwa v[234:235], v154 src0_sel:WORD_1
	v_pk_fma_f32 v[224:225], v[226:227], v[190:191], v[224:225]
	v_cvt_pk_f32_fp8_e32 v[226:227], v156
	v_pk_fma_f32 v[222:223], v[236:237], v[196:197], v[222:223]
	v_cvt_pk_f32_fp8_e32 v[236:237], v155
	v_pk_fma_f32 v[224:225], v[228:229], v[194:195], v[224:225]
	v_cvt_pk_f32_fp8_sdwa v[228:229], v156 src0_sel:WORD_1
	v_cvt_pk_f32_fp8_sdwa v[238:239], v155 src0_sel:WORD_1
	v_lshl_or_b32 v70, v70, 7, v209
	global_load_dwordx4 v[152:155], v70, s[6:7]
	v_pk_fma_f32 v[224:225], v[230:231], v[198:199], v[224:225]
	v_cvt_pk_f32_fp8_e32 v[230:231], v157
	v_pk_fma_f32 v[224:225], v[232:233], v[184:185], v[224:225]
	v_cvt_pk_f32_fp8_sdwa v[232:233], v157 src0_sel:WORD_1
	v_pk_fma_f32 v[224:225], v[234:235], v[188:189], v[224:225]
	v_cvt_pk_f32_fp8_e32 v[234:235], v158
	v_pk_mul_f32 v[226:227], v[226:227], v[186:187]
	v_pk_fma_f32 v[224:225], v[236:237], v[192:193], v[224:225]
	v_cvt_pk_f32_fp8_sdwa v[236:237], v158 src0_sel:WORD_1
	v_pk_fma_f32 v[226:227], v[228:229], v[190:191], v[226:227]
	v_cvt_pk_f32_fp8_e32 v[228:229], v160
	v_pk_fma_f32 v[224:225], v[238:239], v[196:197], v[224:225]
	v_cvt_pk_f32_fp8_e32 v[238:239], v159
	v_pk_fma_f32 v[226:227], v[230:231], v[194:195], v[226:227]
	v_cvt_pk_f32_fp8_sdwa v[230:231], v160 src0_sel:WORD_1
	v_cvt_pk_f32_fp8_sdwa v[240:241], v159 src0_sel:WORD_1
	v_lshl_or_b32 v71, v71, 7, v209
	global_load_dwordx4 v[156:159], v71, s[6:7]
	v_pk_fma_f32 v[226:227], v[232:233], v[198:199], v[226:227]
	v_cvt_pk_f32_fp8_e32 v[232:233], v161
	v_pk_fma_f32 v[226:227], v[234:235], v[184:185], v[226:227]
	v_cvt_pk_f32_fp8_sdwa v[234:235], v161 src0_sel:WORD_1
	v_pk_fma_f32 v[226:227], v[236:237], v[188:189], v[226:227]
	v_cvt_pk_f32_fp8_e32 v[236:237], v162
	v_pk_mul_f32 v[228:229], v[228:229], v[186:187]
	v_pk_fma_f32 v[226:227], v[238:239], v[192:193], v[226:227]
	v_cvt_pk_f32_fp8_sdwa v[238:239], v162 src0_sel:WORD_1
	v_pk_fma_f32 v[228:229], v[230:231], v[190:191], v[228:229]
	v_cvt_pk_f32_fp8_e32 v[230:231], v164
	v_pk_fma_f32 v[226:227], v[240:241], v[196:197], v[226:227]
	v_cvt_pk_f32_fp8_e32 v[240:241], v163
	v_pk_fma_f32 v[228:229], v[232:233], v[194:195], v[228:229]
	v_cvt_pk_f32_fp8_sdwa v[232:233], v164 src0_sel:WORD_1
	v_cvt_pk_f32_fp8_sdwa v[242:243], v163 src0_sel:WORD_1
	v_lshl_or_b32 v64, v64, 7, v209
	global_load_dwordx4 v[160:163], v64, s[6:7]
	v_pk_fma_f32 v[228:229], v[234:235], v[198:199], v[228:229]
	v_cvt_pk_f32_fp8_e32 v[234:235], v165
	v_pk_fma_f32 v[228:229], v[236:237], v[184:185], v[228:229]
	v_cvt_pk_f32_fp8_sdwa v[236:237], v165 src0_sel:WORD_1
	v_pk_fma_f32 v[228:229], v[238:239], v[188:189], v[228:229]
	v_cvt_pk_f32_fp8_e32 v[238:239], v166
	v_pk_mul_f32 v[230:231], v[230:231], v[186:187]
	v_pk_fma_f32 v[228:229], v[240:241], v[192:193], v[228:229]
	v_cvt_pk_f32_fp8_sdwa v[240:241], v166 src0_sel:WORD_1
	v_pk_fma_f32 v[230:231], v[232:233], v[190:191], v[230:231]
	v_cvt_pk_f32_fp8_e32 v[232:233], v168
	v_pk_fma_f32 v[228:229], v[242:243], v[196:197], v[228:229]
	v_cvt_pk_f32_fp8_e32 v[242:243], v167
	v_pk_fma_f32 v[230:231], v[234:235], v[194:195], v[230:231]
	v_cvt_pk_f32_fp8_sdwa v[234:235], v168 src0_sel:WORD_1
	v_cvt_pk_f32_fp8_sdwa v[244:245], v167 src0_sel:WORD_1
	v_lshl_or_b32 v65, v65, 7, v209
	global_load_dwordx4 v[164:167], v65, s[6:7]
	v_pk_fma_f32 v[230:231], v[236:237], v[198:199], v[230:231]
	v_cvt_pk_f32_fp8_e32 v[236:237], v169
	v_pk_fma_f32 v[230:231], v[238:239], v[184:185], v[230:231]
	v_cvt_pk_f32_fp8_sdwa v[238:239], v169 src0_sel:WORD_1
	v_pk_fma_f32 v[230:231], v[240:241], v[188:189], v[230:231]
	v_cvt_pk_f32_fp8_e32 v[240:241], v170
	v_pk_mul_f32 v[232:233], v[232:233], v[186:187]
	v_pk_fma_f32 v[230:231], v[242:243], v[192:193], v[230:231]
	v_cvt_pk_f32_fp8_sdwa v[242:243], v170 src0_sel:WORD_1
	v_pk_fma_f32 v[232:233], v[234:235], v[190:191], v[232:233]
	v_cvt_pk_f32_fp8_e32 v[234:235], v172
	v_pk_fma_f32 v[230:231], v[244:245], v[196:197], v[230:231]
	v_cvt_pk_f32_fp8_e32 v[244:245], v171
	v_pk_fma_f32 v[232:233], v[236:237], v[194:195], v[232:233]
	v_cvt_pk_f32_fp8_sdwa v[236:237], v172 src0_sel:WORD_1
	v_cvt_pk_f32_fp8_sdwa v[246:247], v171 src0_sel:WORD_1
	v_lshl_or_b32 v66, v66, 7, v209
	global_load_dwordx4 v[168:171], v66, s[6:7]
	v_pk_fma_f32 v[232:233], v[238:239], v[198:199], v[232:233]
	v_cvt_pk_f32_fp8_e32 v[238:239], v173
	v_pk_fma_f32 v[232:233], v[240:241], v[184:185], v[232:233]
	v_cvt_pk_f32_fp8_sdwa v[240:241], v173 src0_sel:WORD_1
	v_pk_fma_f32 v[232:233], v[242:243], v[188:189], v[232:233]
	v_cvt_pk_f32_fp8_e32 v[242:243], v174
	v_pk_mul_f32 v[186:187], v[234:235], v[186:187]
	v_pk_fma_f32 v[232:233], v[244:245], v[192:193], v[232:233]
	v_cvt_pk_f32_fp8_sdwa v[244:245], v174 src0_sel:WORD_1
	v_pk_fma_f32 v[186:187], v[236:237], v[190:191], v[186:187]
	v_pk_fma_f32 v[232:233], v[246:247], v[196:197], v[232:233]
	v_cvt_pk_f32_fp8_e32 v[246:247], v175
	v_pk_fma_f32 v[186:187], v[238:239], v[194:195], v[186:187]
	v_cvt_pk_f32_fp8_sdwa v[248:249], v175 src0_sel:WORD_1
	v_lshl_or_b32 v67, v67, 7, v209
	global_load_dwordx4 v[172:175], v67, s[6:7]
	v_pk_fma_f32 v[186:187], v[240:241], v[198:199], v[186:187]
	v_mov_b32_e32 v194, v220
	v_pk_fma_f32 v[184:185], v[242:243], v[184:185], v[186:187]
	v_mov_b32_e32 v186, v200
	v_pk_fma_f32 v[184:185], v[244:245], v[188:189], v[184:185]
	v_mov_b32_e32 v187, v202
	v_pk_fma_f32 v[184:185], v[246:247], v[192:193], v[184:185]
	v_mov_b32_e32 v202, v201
	v_pk_fma_f32 v[184:185], v[248:249], v[196:197], v[184:185]
	v_mov_b32_e32 v195, v222
	v_mov_b32_e32 v222, v221
	v_pk_add_f32 v[186:187], v[186:187], v[202:203]
	v_pk_add_f32 v[194:195], v[194:195], v[222:223]
	v_mov_b32_e32 v200, v232
	v_mov_b32_e32 v201, v184
	v_mov_b32_e32 v184, v233
	v_mov_b32_e32 v188, v204
	v_mov_b32_e32 v189, v210
	v_mov_b32_e32 v210, v205
	v_mov_b32_e32 v196, v224
	v_mov_b32_e32 v197, v226
	v_mov_b32_e32 v226, v225
	v_pk_add_f32 v[184:185], v[200:201], v[184:185]
	v_cndmask_b32_e64 v200, v186, v194, s[4:5]
	v_cndmask_b32_e64 v202, v194, v186, s[4:5]
	v_cndmask_b32_e64 v186, v187, v195, s[4:5]
	v_pk_add_f32 v[188:189], v[188:189], v[210:211]
	v_pk_add_f32 v[196:197], v[196:197], v[226:227]
	v_mov_b32_dpp v200, v200 row_half_mirror row_mask:0xf bank_mask:0xf bound_ctrl:1
	v_cndmask_b32_e64 v203, v195, v187, s[4:5]
	v_mov_b32_dpp v201, v186 row_half_mirror row_mask:0xf bank_mask:0xf bound_ctrl:1
	v_mov_b32_e32 v190, v212
	v_mov_b32_e32 v191, v214
	v_mov_b32_e32 v214, v213
	v_mov_b32_e32 v198, v228
	v_mov_b32_e32 v199, v230
	v_mov_b32_e32 v230, v229
	v_pk_add_f32 v[186:187], v[202:203], v[200:201]
	v_cndmask_b32_e64 v194, v188, v196, s[4:5]
	v_cndmask_b32_e64 v200, v196, v188, s[4:5]
	v_cndmask_b32_e64 v188, v189, v197, s[4:5]
	v_pk_add_f32 v[190:191], v[190:191], v[214:215]
	v_pk_add_f32 v[198:199], v[198:199], v[230:231]
	v_mov_b32_dpp v194, v194 row_half_mirror row_mask:0xf bank_mask:0xf bound_ctrl:1
	v_cndmask_b32_e64 v201, v197, v189, s[4:5]
	v_mov_b32_dpp v195, v188 row_half_mirror row_mask:0xf bank_mask:0xf bound_ctrl:1
	v_mov_b32_e32 v192, v216
	v_mov_b32_e32 v193, v218
	v_mov_b32_e32 v218, v217
	v_pk_add_f32 v[188:189], v[200:201], v[194:195]
	v_cndmask_b32_e64 v194, v190, v198, s[4:5]
	v_cndmask_b32_e64 v196, v198, v190, s[4:5]
	v_cndmask_b32_e64 v190, v191, v199, s[4:5]
	v_pk_add_f32 v[192:193], v[192:193], v[218:219]
	v_mov_b32_dpp v194, v194 row_half_mirror row_mask:0xf bank_mask:0xf bound_ctrl:1
	v_cndmask_b32_e64 v197, v199, v191, s[4:5]
	v_mov_b32_dpp v195, v190 row_half_mirror row_mask:0xf bank_mask:0xf bound_ctrl:1
	v_pk_add_f32 v[190:191], v[196:197], v[194:195]
	v_cndmask_b32_e64 v194, v192, v184, s[4:5]
	v_cndmask_b32_e64 v196, v184, v192, s[4:5]
	v_cndmask_b32_e64 v184, v193, v185, s[4:5]
	v_mov_b32_dpp v194, v194 row_half_mirror row_mask:0xf bank_mask:0xf bound_ctrl:1
	v_cndmask_b32_e64 v197, v185, v193, s[4:5]
	v_mov_b32_dpp v195, v184 row_half_mirror row_mask:0xf bank_mask:0xf bound_ctrl:1
	v_pk_add_f32 v[184:185], v[196:197], v[194:195]
	v_cndmask_b32_e64 v192, v186, v190, s[2:3]
	v_cndmask_b32_e64 v194, v190, v186, s[2:3]
	v_cndmask_b32_e64 v186, v187, v191, s[2:3]
	v_mov_b32_dpp v192, v192 quad_perm:[2,3,0,1] row_mask:0xf bank_mask:0xf bound_ctrl:1
	v_cndmask_b32_e64 v195, v191, v187, s[2:3]
	v_mov_b32_dpp v193, v186 quad_perm:[2,3,0,1] row_mask:0xf bank_mask:0xf bound_ctrl:1
	v_pk_add_f32 v[186:187], v[194:195], v[192:193]
	v_cndmask_b32_e64 v190, v188, v184, s[2:3]
	v_cndmask_b32_e64 v192, v184, v188, s[2:3]
	v_cndmask_b32_e64 v184, v189, v185, s[2:3]
	v_mov_b32_dpp v190, v190 quad_perm:[2,3,0,1] row_mask:0xf bank_mask:0xf bound_ctrl:1
	v_cndmask_b32_e64 v193, v185, v189, s[2:3]
	v_mov_b32_dpp v191, v184 quad_perm:[2,3,0,1] row_mask:0xf bank_mask:0xf bound_ctrl:1
	v_pk_add_f32 v[184:185], v[192:193], v[190:191]
	s_ashr_i32 s11, s10, 31
	v_cndmask_b32_e64 v188, v186, v184, s[0:1]
	v_cndmask_b32_e64 v190, v184, v186, s[0:1]
	v_cndmask_b32_e64 v184, v187, v185, s[0:1]
	v_mov_b32_dpp v188, v188 quad_perm:[1,0,3,2] row_mask:0xf bank_mask:0xf bound_ctrl:1
	v_cndmask_b32_e64 v191, v185, v187, s[0:1]
	v_mov_b32_dpp v189, v184 quad_perm:[1,0,3,2] row_mask:0xf bank_mask:0xf bound_ctrl:1
	v_pk_add_f32 v[184:185], v[190:191], v[188:189]
	s_lshl_b64 s[10:11], s[10:11], 8
	v_cvt_pk_bf16_f32 v186, v184, v185
	v_lshl_add_u64 v[184:185], v[178:179], 0, s[10:11]
	global_store_dword v[184:185], v186, off
	s_add_u32 s20, s12, 0x300
	s_lshl_b32 s20, s20, 11
	v_lshl_add_u64 v[108:109], v[182:183], 0, s[20:21]
	global_load_dwordx4 v[100:103], v[108:109], off offset:16
	s_nop 0
	global_load_dwordx4 v[108:111], v[108:109], off
	s_add_u32 s20, s12, 0x500
	s_lshl_b32 s20, s20, 9
	v_lshl_add_u64 v[80:81], v[180:181], 0, s[20:21]
	global_load_dwordx4 v[64:67], v[80:81], off offset:48
	global_load_dwordx4 v[68:71], v[80:81], off offset:32
	global_load_dwordx4 v[72:75], v[80:81], off offset:16
	s_nop 0
	global_load_dwordx4 v[80:83], v[80:81], off
	s_add_u32 s12, s12, 0x200
	s_mov_b32 s13, 61
.Lpd2_loop:
	s_mov_b32 s14, s12
	s_waitcnt vmcnt(23)
	v_cvt_pk_f32_fp8_e32 v[200:201], v24
	v_cvt_pk_f32_fp8_sdwa v[202:203], v24 src0_sel:WORD_1
	v_cvt_pk_f32_fp8_e32 v[204:205], v25
	v_lshlrev_b32_e32 v186, 16, v20
	v_and_b32_e32 v187, 0xffff0000, v20
	v_cvt_pk_f32_fp8_sdwa v[210:211], v25 src0_sel:WORD_1
	v_lshlrev_b32_e32 v190, 16, v21
	v_and_b32_e32 v191, 0xffff0000, v21
	v_cvt_pk_f32_fp8_e32 v[212:213], v26
	v_pk_mul_f32 v[200:201], v[200:201], v[186:187]
	v_lshlrev_b32_e32 v194, 16, v22
	v_and_b32_e32 v195, 0xffff0000, v22
	v_cvt_pk_f32_fp8_sdwa v[214:215], v26 src0_sel:WORD_1
	v_pk_fma_f32 v[200:201], v[202:203], v[190:191], v[200:201]
	v_cvt_pk_f32_fp8_e32 v[202:203], v28
	v_lshlrev_b32_e32 v198, 16, v23
	v_and_b32_e32 v199, 0xffff0000, v23
	v_cvt_pk_f32_fp8_e32 v[216:217], v27
	v_pk_fma_f32 v[200:201], v[204:205], v[194:195], v[200:201]
	v_cvt_pk_f32_fp8_sdwa v[204:205], v28 src0_sel:WORD_1
	v_lshlrev_b32_e32 v184, 16, v16
	v_and_b32_e32 v185, 0xffff0000, v16
	v_cvt_pk_f32_fp8_sdwa v[218:219], v27 src0_sel:WORD_1
	v_lshl_or_b32 v0, v0, 7, v209
	global_load_dwordx4 v[24:27], v0, s[6:7]
	v_pk_fma_f32 v[200:201], v[210:211], v[198:199], v[200:201]
	v_cvt_pk_f32_fp8_e32 v[210:211], v29
	v_lshlrev_b32_e32 v188, 16, v17
	v_and_b32_e32 v189, 0xffff0000, v17
	v_pk_fma_f32 v[200:201], v[212:213], v[184:185], v[200:201]
	v_cvt_pk_f32_fp8_sdwa v[212:213], v29 src0_sel:WORD_1
	v_lshlrev_b32_e32 v192, 16, v18
	v_and_b32_e32 v193, 0xffff0000, v18
	v_pk_fma_f32 v[200:201], v[214:215], v[188:189], v[200:201]
	v_cvt_pk_f32_fp8_e32 v[214:215], v30
	v_pk_mul_f32 v[202:203], v[202:203], v[186:187]
	v_lshlrev_b32_e32 v196, 16, v19
	v_and_b32_e32 v197, 0xffff0000, v19
	v_pk_fma_f32 v[200:201], v[216:217], v[192:193], v[200:201]
	v_cvt_pk_f32_fp8_sdwa v[216:217], v30 src0_sel:WORD_1
	v_pk_fma_f32 v[202:203], v[204:205], v[190:191], v[202:203]
	v_cvt_pk_f32_fp8_e32 v[204:205], v32
	v_pk_fma_f32 v[200:201], v[218:219], v[196:197], v[200:201]
	v_cvt_pk_f32_fp8_e32 v[218:219], v31
	v_pk_fma_f32 v[202:203], v[210:211], v[194:195], v[202:203]
	v_cvt_pk_f32_fp8_sdwa v[210:211], v32 src0_sel:WORD_1
	v_cvt_pk_f32_fp8_sdwa v[220:221], v31 src0_sel:WORD_1
	v_lshl_or_b32 v1, v1, 7, v209
	global_load_dwordx4 v[28:31], v1, s[6:7]
	v_pk_fma_f32 v[202:203], v[212:213], v[198:199], v[202:203]
	v_cvt_pk_f32_fp8_e32 v[212:213], v33
	v_pk_fma_f32 v[202:203], v[214:215], v[184:185], v[202:203]
	v_cvt_pk_f32_fp8_sdwa v[214:215], v33 src0_sel:WORD_1
	v_pk_fma_f32 v[202:203], v[216:217], v[188:189], v[202:203]
	v_cvt_pk_f32_fp8_e32 v[216:217], v34
	v_pk_mul_f32 v[204:205], v[204:205], v[186:187]
	v_pk_fma_f32 v[202:203], v[218:219], v[192:193], v[202:203]
	v_cvt_pk_f32_fp8_sdwa v[218:219], v34 src0_sel:WORD_1
	v_pk_fma_f32 v[204:205], v[210:211], v[190:191], v[204:205]
	v_cvt_pk_f32_fp8_e32 v[210:211], v36
	v_pk_fma_f32 v[202:203], v[220:221], v[196:197], v[202:203]
	v_cvt_pk_f32_fp8_e32 v[220:221], v35
	v_pk_fma_f32 v[204:205], v[212:213], v[194:195], v[204:205]
	v_cvt_pk_f32_fp8_sdwa v[212:213], v36 src0_sel:WORD_1
	v_cvt_pk_f32_fp8_sdwa v[222:223], v35 src0_sel:WORD_1
	v_lshl_or_b32 v2, v2, 7, v209
	global_load_dwordx4 v[32:35], v2, s[6:7]
	v_pk_fma_f32 v[204:205], v[214:215], v[198:199], v[204:205]
	v_cvt_pk_f32_fp8_e32 v[214:215], v37
	v_pk_fma_f32 v[204:205], v[216:217], v[184:185], v[204:205]
	v_cvt_pk_f32_fp8_sdwa v[216:217], v37 src0_sel:WORD_1
	v_pk_fma_f32 v[204:205], v[218:219], v[188:189], v[204:205]
	v_cvt_pk_f32_fp8_e32 v[218:219], v38
	v_pk_mul_f32 v[210:211], v[210:211], v[186:187]
	v_pk_fma_f32 v[204:205], v[220:221], v[192:193], v[204:205]
	v_cvt_pk_f32_fp8_sdwa v[220:221], v38 src0_sel:WORD_1
	v_pk_fma_f32 v[210:211], v[212:213], v[190:191], v[210:211]
	v_cvt_pk_f32_fp8_e32 v[212:213], v40
	v_pk_fma_f32 v[204:205], v[222:223], v[196:197], v[204:205]
	v_cvt_pk_f32_fp8_e32 v[222:223], v39
	v_pk_fma_f32 v[210:211], v[214:215], v[194:195], v[210:211]
	v_cvt_pk_f32_fp8_sdwa v[214:215], v40 src0_sel:WORD_1
	v_cvt_pk_f32_fp8_sdwa v[224:225], v39 src0_sel:WORD_1
	v_lshl_or_b32 v3, v3, 7, v209
	global_load_dwordx4 v[36:39], v3, s[6:7]
	v_pk_fma_f32 v[210:211], v[216:217], v[198:199], v[210:211]
	v_cvt_pk_f32_fp8_e32 v[216:217], v41
	v_pk_fma_f32 v[210:211], v[218:219], v[184:185], v[210:211]
	v_cvt_pk_f32_fp8_sdwa v[218:219], v41 src0_sel:WORD_1
	v_pk_fma_f32 v[210:211], v[220:221], v[188:189], v[210:211]
	v_cvt_pk_f32_fp8_e32 v[220:221], v42
	v_pk_mul_f32 v[212:213], v[212:213], v[186:187]
	v_pk_fma_f32 v[210:211], v[222:223], v[192:193], v[210:211]
	v_cvt_pk_f32_fp8_sdwa v[222:223], v42 src0_sel:WORD_1
	v_pk_fma_f32 v[212:213], v[214:215], v[190:191], v[212:213]
	v_cvt_pk_f32_fp8_e32 v[214:215], v44
	v_pk_fma_f32 v[210:211], v[224:225], v[196:197], v[210:211]
	v_cvt_pk_f32_fp8_e32 v[224:225], v43
	v_pk_fma_f32 v[212:213], v[216:217], v[194:195], v[212:213]
	v_cvt_pk_f32_fp8_sdwa v[216:217], v44 src0_sel:WORD_1
	v_cvt_pk_f32_fp8_sdwa v[226:227], v43 src0_sel:WORD_1
	v_lshl_or_b32 v4, v4, 7, v209
	global_load_dwordx4 v[40:43], v4, s[6:7]
	v_pk_fma_f32 v[212:213], v[218:219], v[198:199], v[212:213]
	v_cvt_pk_f32_fp8_e32 v[218:219], v45
	v_pk_fma_f32 v[212:213], v[220:221], v[184:185], v[212:213]
	v_cvt_pk_f32_fp8_sdwa v[220:221], v45 src0_sel:WORD_1
	v_pk_fma_f32 v[212:213], v[222:223], v[188:189], v[212:213]
	v_cvt_pk_f32_fp8_e32 v[222:223], v46
	v_pk_mul_f32 v[214:215], v[214:215], v[186:187]
	v_pk_fma_f32 v[212:213], v[224:225], v[192:193], v[212:213]
	v_cvt_pk_f32_fp8_sdwa v[224:225], v46 src0_sel:WORD_1
	v_pk_fma_f32 v[214:215], v[216:217], v[190:191], v[214:215]
	v_cvt_pk_f32_fp8_e32 v[216:217], v48
	v_pk_fma_f32 v[212:213], v[226:227], v[196:197], v[212:213]
	v_cvt_pk_f32_fp8_e32 v[226:227], v47
	v_pk_fma_f32 v[214:215], v[218:219], v[194:195], v[214:215]
	v_cvt_pk_f32_fp8_sdwa v[218:219], v48 src0_sel:WORD_1
	v_cvt_pk_f32_fp8_sdwa v[228:229], v47 src0_sel:WORD_1
	v_lshl_or_b32 v5, v5, 7, v209
	global_load_dwordx4 v[44:47], v5, s[6:7]
	v_pk_fma_f32 v[214:215], v[220:221], v[198:199], v[214:215]
	v_cvt_pk_f32_fp8_e32 v[220:221], v49
	v_pk_fma_f32 v[214:215], v[222:223], v[184:185], v[214:215]
	v_cvt_pk_f32_fp8_sdwa v[222:223], v49 src0_sel:WORD_1
	v_pk_fma_f32 v[214:215], v[224:225], v[188:189], v[214:215]
	v_cvt_pk_f32_fp8_e32 v[224:225], v50
	v_pk_mul_f32 v[216:217], v[216:217], v[186:187]
	v_pk_fma_f32 v[214:215], v[226:227], v[192:193], v[214:215]
	v_cvt_pk_f32_fp8_sdwa v[226:227], v50 src0_sel:WORD_1
	v_pk_fma_f32 v[216:217], v[218:219], v[190:191], v[216:217]
	v_cvt_pk_f32_fp8_e32 v[218:219], v52
	v_pk_fma_f32 v[214:215], v[228:229], v[196:197], v[214:215]
	v_cvt_pk_f32_fp8_e32 v[228:229], v51
	v_pk_fma_f32 v[216:217], v[220:221], v[194:195], v[216:217]
	v_cvt_pk_f32_fp8_sdwa v[220:221], v52 src0_sel:WORD_1
	v_cvt_pk_f32_fp8_sdwa v[230:231], v51 src0_sel:WORD_1
	v_lshl_or_b32 v6, v6, 7, v209
	global_load_dwordx4 v[48:51], v6, s[6:7]
	v_pk_fma_f32 v[216:217], v[222:223], v[198:199], v[216:217]
	v_cvt_pk_f32_fp8_e32 v[222:223], v53
	v_pk_fma_f32 v[216:217], v[224:225], v[184:185], v[216:217]
	v_cvt_pk_f32_fp8_sdwa v[224:225], v53 src0_sel:WORD_1
	v_pk_fma_f32 v[216:217], v[226:227], v[188:189], v[216:217]
	v_cvt_pk_f32_fp8_e32 v[226:227], v54
	v_pk_mul_f32 v[218:219], v[218:219], v[186:187]
	v_pk_fma_f32 v[216:217], v[228:229], v[192:193], v[216:217]
	v_cvt_pk_f32_fp8_sdwa v[228:229], v54 src0_sel:WORD_1
	v_pk_fma_f32 v[218:219], v[220:221], v[190:191], v[218:219]
	v_cvt_pk_f32_fp8_e32 v[220:221], v56
	v_pk_fma_f32 v[216:217], v[230:231], v[196:197], v[216:217]
	v_cvt_pk_f32_fp8_e32 v[230:231], v55
	v_pk_fma_f32 v[218:219], v[222:223], v[194:195], v[218:219]
	v_cvt_pk_f32_fp8_sdwa v[222:223], v56 src0_sel:WORD_1
	v_cvt_pk_f32_fp8_sdwa v[232:233], v55 src0_sel:WORD_1
	v_lshl_or_b32 v7, v7, 7, v209
	global_load_dwordx4 v[52:55], v7, s[6:7]
	v_pk_fma_f32 v[218:219], v[224:225], v[198:199], v[218:219]
	v_cvt_pk_f32_fp8_e32 v[224:225], v57
	v_pk_fma_f32 v[218:219], v[226:227], v[184:185], v[218:219]
	v_cvt_pk_f32_fp8_sdwa v[226:227], v57 src0_sel:WORD_1
	v_pk_fma_f32 v[218:219], v[228:229], v[188:189], v[218:219]
	v_cvt_pk_f32_fp8_e32 v[228:229], v58
	v_pk_mul_f32 v[220:221], v[220:221], v[186:187]
	v_pk_fma_f32 v[218:219], v[230:231], v[192:193], v[218:219]
	v_cvt_pk_f32_fp8_sdwa v[230:231], v58 src0_sel:WORD_1
	v_pk_fma_f32 v[220:221], v[222:223], v[190:191], v[220:221]
	v_cvt_pk_f32_fp8_e32 v[222:223], v60
	v_pk_fma_f32 v[218:219], v[232:233], v[196:197], v[218:219]
	v_cvt_pk_f32_fp8_e32 v[232:233], v59
	v_pk_fma_f32 v[220:221], v[224:225], v[194:195], v[220:221]
	v_cvt_pk_f32_fp8_sdwa v[224:225], v60 src0_sel:WORD_1
	v_cvt_pk_f32_fp8_sdwa v[234:235], v59 src0_sel:WORD_1
	v_lshl_or_b32 v8, v8, 7, v209
	global_load_dwordx4 v[56:59], v8, s[6:7]
	v_pk_fma_f32 v[220:221], v[226:227], v[198:199], v[220:221]
	v_cvt_pk_f32_fp8_e32 v[226:227], v61
	v_pk_fma_f32 v[220:221], v[228:229], v[184:185], v[220:221]
	v_cvt_pk_f32_fp8_sdwa v[228:229], v61 src0_sel:WORD_1
	v_pk_fma_f32 v[220:221], v[230:231], v[188:189], v[220:221]
	v_cvt_pk_f32_fp8_e32 v[230:231], v62
	v_pk_mul_f32 v[222:223], v[222:223], v[186:187]
	v_pk_fma_f32 v[220:221], v[232:233], v[192:193], v[220:221]
	v_cvt_pk_f32_fp8_sdwa v[232:233], v62 src0_sel:WORD_1
	v_pk_fma_f32 v[222:223], v[224:225], v[190:191], v[222:223]
	v_cvt_pk_f32_fp8_e32 v[224:225], v76
	v_pk_fma_f32 v[220:221], v[234:235], v[196:197], v[220:221]
	v_cvt_pk_f32_fp8_e32 v[234:235], v63
	v_pk_fma_f32 v[222:223], v[226:227], v[194:195], v[222:223]
	v_cvt_pk_f32_fp8_sdwa v[226:227], v76 src0_sel:WORD_1
	v_cvt_pk_f32_fp8_sdwa v[236:237], v63 src0_sel:WORD_1
	v_lshl_or_b32 v9, v9, 7, v209
	global_load_dwordx4 v[60:63], v9, s[6:7]
	v_pk_fma_f32 v[222:223], v[228:229], v[198:199], v[222:223]
	v_cvt_pk_f32_fp8_e32 v[228:229], v77
	v_pk_fma_f32 v[222:223], v[230:231], v[184:185], v[222:223]
	v_cvt_pk_f32_fp8_sdwa v[230:231], v77 src0_sel:WORD_1
	v_pk_fma_f32 v[222:223], v[232:233], v[188:189], v[222:223]
	v_cvt_pk_f32_fp8_e32 v[232:233], v78
	v_pk_mul_f32 v[224:225], v[224:225], v[186:187]
	v_pk_fma_f32 v[222:223], v[234:235], v[192:193], v[222:223]
	v_cvt_pk_f32_fp8_sdwa v[234:235], v78 src0_sel:WORD_1
	v_pk_fma_f32 v[224:225], v[226:227], v[190:191], v[224:225]
	v_cvt_pk_f32_fp8_e32 v[226:227], v84
	v_pk_fma_f32 v[222:223], v[236:237], v[196:197], v[222:223]
	v_cvt_pk_f32_fp8_e32 v[236:237], v79
	v_pk_fma_f32 v[224:225], v[228:229], v[194:195], v[224:225]
	v_cvt_pk_f32_fp8_sdwa v[228:229], v84 src0_sel:WORD_1
	v_cvt_pk_f32_fp8_sdwa v[238:239], v79 src0_sel:WORD_1
	v_lshl_or_b32 v10, v10, 7, v209
	global_load_dwordx4 v[76:79], v10, s[6:7]
	v_pk_fma_f32 v[224:225], v[230:231], v[198:199], v[224:225]
	v_cvt_pk_f32_fp8_e32 v[230:231], v85
	v_pk_fma_f32 v[224:225], v[232:233], v[184:185], v[224:225]
	v_cvt_pk_f32_fp8_sdwa v[232:233], v85 src0_sel:WORD_1
	v_pk_fma_f32 v[224:225], v[234:235], v[188:189], v[224:225]
	v_cvt_pk_f32_fp8_e32 v[234:235], v86
	v_pk_mul_f32 v[226:227], v[226:227], v[186:187]
	v_pk_fma_f32 v[224:225], v[236:237], v[192:193], v[224:225]
	v_cvt_pk_f32_fp8_sdwa v[236:237], v86 src0_sel:WORD_1
	v_pk_fma_f32 v[226:227], v[228:229], v[190:191], v[226:227]
	v_cvt_pk_f32_fp8_e32 v[228:229], v88
	v_pk_fma_f32 v[224:225], v[238:239], v[196:197], v[224:225]
	v_cvt_pk_f32_fp8_e32 v[238:239], v87
	v_pk_fma_f32 v[226:227], v[230:231], v[194:195], v[226:227]
	v_cvt_pk_f32_fp8_sdwa v[230:231], v88 src0_sel:WORD_1
	v_cvt_pk_f32_fp8_sdwa v[240:241], v87 src0_sel:WORD_1
	v_lshl_or_b32 v11, v11, 7, v209
	global_load_dwordx4 v[84:87], v11, s[6:7]
	v_pk_fma_f32 v[226:227], v[232:233], v[198:199], v[226:227]
	v_cvt_pk_f32_fp8_e32 v[232:233], v89
	v_pk_fma_f32 v[226:227], v[234:235], v[184:185], v[226:227]
	v_cvt_pk_f32_fp8_sdwa v[234:235], v89 src0_sel:WORD_1
	v_pk_fma_f32 v[226:227], v[236:237], v[188:189], v[226:227]
	v_cvt_pk_f32_fp8_e32 v[236:237], v90
	v_pk_mul_f32 v[228:229], v[228:229], v[186:187]
	v_pk_fma_f32 v[226:227], v[238:239], v[192:193], v[226:227]
	v_cvt_pk_f32_fp8_sdwa v[238:239], v90 src0_sel:WORD_1
	v_pk_fma_f32 v[228:229], v[230:231], v[190:191], v[228:229]
	v_cvt_pk_f32_fp8_e32 v[230:231], v92
	v_pk_fma_f32 v[226:227], v[240:241], v[196:197], v[226:227]
	v_cvt_pk_f32_fp8_e32 v[240:241], v91
	v_pk_fma_f32 v[228:229], v[232:233], v[194:195], v[228:229]
	v_cvt_pk_f32_fp8_sdwa v[232:233], v92 src0_sel:WORD_1
	v_cvt_pk_f32_fp8_sdwa v[242:243], v91 src0_sel:WORD_1
	v_lshl_or_b32 v12, v12, 7, v209
	global_load_dwordx4 v[88:91], v12, s[6:7]
	v_pk_fma_f32 v[228:229], v[234:235], v[198:199], v[228:229]
	v_cvt_pk_f32_fp8_e32 v[234:235], v93
	v_pk_fma_f32 v[228:229], v[236:237], v[184:185], v[228:229]
	v_cvt_pk_f32_fp8_sdwa v[236:237], v93 src0_sel:WORD_1
	v_pk_fma_f32 v[228:229], v[238:239], v[188:189], v[228:229]
	v_cvt_pk_f32_fp8_e32 v[238:239], v94
	v_pk_mul_f32 v[230:231], v[230:231], v[186:187]
	v_pk_fma_f32 v[228:229], v[240:241], v[192:193], v[228:229]
	v_cvt_pk_f32_fp8_sdwa v[240:241], v94 src0_sel:WORD_1
	v_pk_fma_f32 v[230:231], v[232:233], v[190:191], v[230:231]
	v_cvt_pk_f32_fp8_e32 v[232:233], v96
	v_pk_fma_f32 v[228:229], v[242:243], v[196:197], v[228:229]
	v_cvt_pk_f32_fp8_e32 v[242:243], v95
	v_pk_fma_f32 v[230:231], v[234:235], v[194:195], v[230:231]
	v_cvt_pk_f32_fp8_sdwa v[234:235], v96 src0_sel:WORD_1
	v_cvt_pk_f32_fp8_sdwa v[244:245], v95 src0_sel:WORD_1
	v_lshl_or_b32 v13, v13, 7, v209
	global_load_dwordx4 v[92:95], v13, s[6:7]
	v_pk_fma_f32 v[230:231], v[236:237], v[198:199], v[230:231]
	v_cvt_pk_f32_fp8_e32 v[236:237], v97
	v_pk_fma_f32 v[230:231], v[238:239], v[184:185], v[230:231]
	v_cvt_pk_f32_fp8_sdwa v[238:239], v97 src0_sel:WORD_1
	v_pk_fma_f32 v[230:231], v[240:241], v[188:189], v[230:231]
	v_cvt_pk_f32_fp8_e32 v[240:241], v98
	v_pk_mul_f32 v[232:233], v[232:233], v[186:187]
	v_pk_fma_f32 v[230:231], v[242:243], v[192:193], v[230:231]
	v_cvt_pk_f32_fp8_sdwa v[242:243], v98 src0_sel:WORD_1
	v_pk_fma_f32 v[232:233], v[234:235], v[190:191], v[232:233]
	v_cvt_pk_f32_fp8_e32 v[234:235], v104
	v_pk_fma_f32 v[230:231], v[244:245], v[196:197], v[230:231]
	v_cvt_pk_f32_fp8_e32 v[244:245], v99
	v_pk_fma_f32 v[232:233], v[236:237], v[194:195], v[232:233]
	v_cvt_pk_f32_fp8_sdwa v[236:237], v104 src0_sel:WORD_1
	v_cvt_pk_f32_fp8_sdwa v[246:247], v99 src0_sel:WORD_1
	v_lshl_or_b32 v14, v14, 7, v209
	global_load_dwordx4 v[96:99], v14, s[6:7]
	v_pk_fma_f32 v[232:233], v[238:239], v[198:199], v[232:233]
	v_cvt_pk_f32_fp8_e32 v[238:239], v105
	v_pk_fma_f32 v[232:233], v[240:241], v[184:185], v[232:233]
	v_cvt_pk_f32_fp8_sdwa v[240:241], v105 src0_sel:WORD_1
	v_pk_fma_f32 v[232:233], v[242:243], v[188:189], v[232:233]
	v_cvt_pk_f32_fp8_e32 v[242:243], v106
	v_pk_mul_f32 v[186:187], v[234:235], v[186:187]
	v_pk_fma_f32 v[232:233], v[244:245], v[192:193], v[232:233]
	v_cvt_pk_f32_fp8_sdwa v[244:245], v106 src0_sel:WORD_1
	v_pk_fma_f32 v[186:187], v[236:237], v[190:191], v[186:187]
	v_pk_fma_f32 v[232:233], v[246:247], v[196:197], v[232:233]
	v_cvt_pk_f32_fp8_e32 v[246:247], v107
	v_pk_fma_f32 v[186:187], v[238:239], v[194:195], v[186:187]
	v_cvt_pk_f32_fp8_sdwa v[248:249], v107 src0_sel:WORD_1
	v_lshl_or_b32 v15, v15, 7, v209
	global_load_dwordx4 v[104:107], v15, s[6:7]
	v_pk_fma_f32 v[186:187], v[240:241], v[198:199], v[186:187]
	v_mov_b32_e32 v194, v220
	v_pk_fma_f32 v[184:185], v[242:243], v[184:185], v[186:187]
	v_mov_b32_e32 v186, v200
	v_pk_fma_f32 v[184:185], v[244:245], v[188:189], v[184:185]
	v_mov_b32_e32 v187, v202
	v_pk_fma_f32 v[184:185], v[246:247], v[192:193], v[184:185]
	v_mov_b32_e32 v202, v201
	v_pk_fma_f32 v[184:185], v[248:249], v[196:197], v[184:185]
	v_mov_b32_e32 v195, v222
	v_mov_b32_e32 v222, v221
	v_pk_add_f32 v[186:187], v[186:187], v[202:203]
	v_pk_add_f32 v[194:195], v[194:195], v[222:223]
	v_mov_b32_e32 v200, v232
	v_mov_b32_e32 v201, v184
	v_mov_b32_e32 v184, v233
	v_mov_b32_e32 v188, v204
	v_mov_b32_e32 v189, v210
	v_mov_b32_e32 v210, v205
	v_mov_b32_e32 v196, v224
	v_mov_b32_e32 v197, v226
	v_mov_b32_e32 v226, v225
	v_pk_add_f32 v[184:185], v[200:201], v[184:185]
	v_cndmask_b32_e64 v200, v186, v194, s[4:5]
	v_cndmask_b32_e64 v202, v194, v186, s[4:5]
	v_cndmask_b32_e64 v186, v187, v195, s[4:5]
	v_pk_add_f32 v[188:189], v[188:189], v[210:211]
	v_pk_add_f32 v[196:197], v[196:197], v[226:227]
	v_mov_b32_dpp v200, v200 row_half_mirror row_mask:0xf bank_mask:0xf bound_ctrl:1
	v_cndmask_b32_e64 v203, v195, v187, s[4:5]
	v_mov_b32_dpp v201, v186 row_half_mirror row_mask:0xf bank_mask:0xf bound_ctrl:1
	v_mov_b32_e32 v190, v212
	v_mov_b32_e32 v191, v214
	v_mov_b32_e32 v214, v213
	v_mov_b32_e32 v198, v228
	v_mov_b32_e32 v199, v230
	v_mov_b32_e32 v230, v229
	v_pk_add_f32 v[186:187], v[202:203], v[200:201]
	v_cndmask_b32_e64 v194, v188, v196, s[4:5]
	v_cndmask_b32_e64 v200, v196, v188, s[4:5]
	v_cndmask_b32_e64 v188, v189, v197, s[4:5]
	v_pk_add_f32 v[190:191], v[190:191], v[214:215]
	v_pk_add_f32 v[198:199], v[198:199], v[230:231]
	v_mov_b32_dpp v194, v194 row_half_mirror row_mask:0xf bank_mask:0xf bound_ctrl:1
	v_cndmask_b32_e64 v201, v197, v189, s[4:5]
	v_mov_b32_dpp v195, v188 row_half_mirror row_mask:0xf bank_mask:0xf bound_ctrl:1
	v_mov_b32_e32 v192, v216
	v_mov_b32_e32 v193, v218
	v_mov_b32_e32 v218, v217
	v_pk_add_f32 v[188:189], v[200:201], v[194:195]
	v_cndmask_b32_e64 v194, v190, v198, s[4:5]
	v_cndmask_b32_e64 v196, v198, v190, s[4:5]
	v_cndmask_b32_e64 v190, v191, v199, s[4:5]
	v_pk_add_f32 v[192:193], v[192:193], v[218:219]
	v_mov_b32_dpp v194, v194 row_half_mirror row_mask:0xf bank_mask:0xf bound_ctrl:1
	v_cndmask_b32_e64 v197, v199, v191, s[4:5]
	v_mov_b32_dpp v195, v190 row_half_mirror row_mask:0xf bank_mask:0xf bound_ctrl:1
	v_pk_add_f32 v[190:191], v[196:197], v[194:195]
	v_cndmask_b32_e64 v194, v192, v184, s[4:5]
	v_cndmask_b32_e64 v196, v184, v192, s[4:5]
	v_cndmask_b32_e64 v184, v193, v185, s[4:5]
	v_mov_b32_dpp v194, v194 row_half_mirror row_mask:0xf bank_mask:0xf bound_ctrl:1
	v_cndmask_b32_e64 v197, v185, v193, s[4:5]
	v_mov_b32_dpp v195, v184 row_half_mirror row_mask:0xf bank_mask:0xf bound_ctrl:1
	v_pk_add_f32 v[184:185], v[196:197], v[194:195]
	v_cndmask_b32_e64 v192, v186, v190, s[2:3]
	v_cndmask_b32_e64 v194, v190, v186, s[2:3]
	v_cndmask_b32_e64 v186, v187, v191, s[2:3]
	v_mov_b32_dpp v192, v192 quad_perm:[2,3,0,1] row_mask:0xf bank_mask:0xf bound_ctrl:1
	v_cndmask_b32_e64 v195, v191, v187, s[2:3]
	v_mov_b32_dpp v193, v186 quad_perm:[2,3,0,1] row_mask:0xf bank_mask:0xf bound_ctrl:1
	v_pk_add_f32 v[186:187], v[194:195], v[192:193]
	v_cndmask_b32_e64 v190, v188, v184, s[2:3]
	v_cndmask_b32_e64 v192, v184, v188, s[2:3]
	v_cndmask_b32_e64 v184, v189, v185, s[2:3]
	v_mov_b32_dpp v190, v190 quad_perm:[2,3,0,1] row_mask:0xf bank_mask:0xf bound_ctrl:1
	v_cndmask_b32_e64 v193, v185, v189, s[2:3]
	v_mov_b32_dpp v191, v184 quad_perm:[2,3,0,1] row_mask:0xf bank_mask:0xf bound_ctrl:1
	v_pk_add_f32 v[184:185], v[192:193], v[190:191]
	s_ashr_i32 s15, s14, 31
	v_cndmask_b32_e64 v188, v186, v184, s[0:1]
	v_cndmask_b32_e64 v190, v184, v186, s[0:1]
	v_cndmask_b32_e64 v184, v187, v185, s[0:1]
	v_mov_b32_dpp v188, v188 quad_perm:[1,0,3,2] row_mask:0xf bank_mask:0xf bound_ctrl:1
	v_cndmask_b32_e64 v191, v185, v187, s[0:1]
	v_mov_b32_dpp v189, v184 quad_perm:[1,0,3,2] row_mask:0xf bank_mask:0xf bound_ctrl:1
	v_pk_add_f32 v[184:185], v[190:191], v[188:189]
	s_lshl_b64 s[14:15], s[14:15], 8
	v_cvt_pk_bf16_f32 v186, v184, v185
	v_lshl_add_u64 v[184:185], v[178:179], 0, s[14:15]
	global_store_dword v[184:185], v186, off
	s_add_u32 s20, s12, 0x200
	s_lshl_b32 s20, s20, 11
	v_lshl_add_u64 v[20:21], v[182:183], 0, s[20:21]
	global_load_dwordx4 v[16:19], v[20:21], off offset:16
	s_nop 0
	global_load_dwordx4 v[20:23], v[20:21], off
	s_add_u32 s20, s12, 0x400
	s_lshl_b32 s20, s20, 9
	v_lshl_add_u64 v[0:1], v[180:181], 0, s[20:21]
	global_load_dwordx4 v[12:15], v[0:1], off offset:48
	global_load_dwordx4 v[8:11], v[0:1], off offset:32
	global_load_dwordx4 v[4:7], v[0:1], off offset:16
	s_nop 0
	global_load_dwordx4 v[0:3], v[0:1], off
	s_add_u32 s10, s12, 0x100
	s_waitcnt vmcnt(23)
	v_cvt_pk_f32_fp8_e32 v[200:201], v112
	v_cvt_pk_f32_fp8_sdwa v[202:203], v112 src0_sel:WORD_1
	v_cvt_pk_f32_fp8_e32 v[204:205], v113
	v_lshlrev_b32_e32 v186, 16, v108
	v_and_b32_e32 v187, 0xffff0000, v108
	v_cvt_pk_f32_fp8_sdwa v[210:211], v113 src0_sel:WORD_1
	v_lshlrev_b32_e32 v190, 16, v109
	v_and_b32_e32 v191, 0xffff0000, v109
	v_cvt_pk_f32_fp8_e32 v[212:213], v114
	v_pk_mul_f32 v[200:201], v[200:201], v[186:187]
	v_lshlrev_b32_e32 v194, 16, v110
	v_and_b32_e32 v195, 0xffff0000, v110
	v_cvt_pk_f32_fp8_sdwa v[214:215], v114 src0_sel:WORD_1
	v_pk_fma_f32 v[200:201], v[202:203], v[190:191], v[200:201]
	v_cvt_pk_f32_fp8_e32 v[202:203], v116
	v_lshlrev_b32_e32 v198, 16, v111
	v_and_b32_e32 v199, 0xffff0000, v111
	v_cvt_pk_f32_fp8_e32 v[216:217], v115
	v_pk_fma_f32 v[200:201], v[204:205], v[194:195], v[200:201]
	v_cvt_pk_f32_fp8_sdwa v[204:205], v116 src0_sel:WORD_1
	v_lshlrev_b32_e32 v184, 16, v100
	v_and_b32_e32 v185, 0xffff0000, v100
	v_cvt_pk_f32_fp8_sdwa v[218:219], v115 src0_sel:WORD_1
	v_lshl_or_b32 v80, v80, 7, v209
	global_load_dwordx4 v[112:115], v80, s[6:7]
	v_pk_fma_f32 v[200:201], v[210:211], v[198:199], v[200:201]
	v_cvt_pk_f32_fp8_e32 v[210:211], v117
	v_lshlrev_b32_e32 v188, 16, v101
	v_and_b32_e32 v189, 0xffff0000, v101
	v_pk_fma_f32 v[200:201], v[212:213], v[184:185], v[200:201]
	v_cvt_pk_f32_fp8_sdwa v[212:213], v117 src0_sel:WORD_1
	v_lshlrev_b32_e32 v192, 16, v102
	v_and_b32_e32 v193, 0xffff0000, v102
	v_pk_fma_f32 v[200:201], v[214:215], v[188:189], v[200:201]
	v_cvt_pk_f32_fp8_e32 v[214:215], v118
	v_pk_mul_f32 v[202:203], v[202:203], v[186:187]
	v_lshlrev_b32_e32 v196, 16, v103
	v_and_b32_e32 v197, 0xffff0000, v103
	v_pk_fma_f32 v[200:201], v[216:217], v[192:193], v[200:201]
	v_cvt_pk_f32_fp8_sdwa v[216:217], v118 src0_sel:WORD_1
	v_pk_fma_f32 v[202:203], v[204:205], v[190:191], v[202:203]
	v_cvt_pk_f32_fp8_e32 v[204:205], v120
	v_pk_fma_f32 v[200:201], v[218:219], v[196:197], v[200:201]
	v_cvt_pk_f32_fp8_e32 v[218:219], v119
	v_pk_fma_f32 v[202:203], v[210:211], v[194:195], v[202:203]
	v_cvt_pk_f32_fp8_sdwa v[210:211], v120 src0_sel:WORD_1
	v_cvt_pk_f32_fp8_sdwa v[220:221], v119 src0_sel:WORD_1
	v_lshl_or_b32 v81, v81, 7, v209
	global_load_dwordx4 v[116:119], v81, s[6:7]
	v_pk_fma_f32 v[202:203], v[212:213], v[198:199], v[202:203]
	v_cvt_pk_f32_fp8_e32 v[212:213], v121
	v_pk_fma_f32 v[202:203], v[214:215], v[184:185], v[202:203]
	v_cvt_pk_f32_fp8_sdwa v[214:215], v121 src0_sel:WORD_1
	v_pk_fma_f32 v[202:203], v[216:217], v[188:189], v[202:203]
	v_cvt_pk_f32_fp8_e32 v[216:217], v122
	v_pk_mul_f32 v[204:205], v[204:205], v[186:187]
	v_pk_fma_f32 v[202:203], v[218:219], v[192:193], v[202:203]
	v_cvt_pk_f32_fp8_sdwa v[218:219], v122 src0_sel:WORD_1
	v_pk_fma_f32 v[204:205], v[210:211], v[190:191], v[204:205]
	v_cvt_pk_f32_fp8_e32 v[210:211], v124
	v_pk_fma_f32 v[202:203], v[220:221], v[196:197], v[202:203]
	v_cvt_pk_f32_fp8_e32 v[220:221], v123
	v_pk_fma_f32 v[204:205], v[212:213], v[194:195], v[204:205]
	v_cvt_pk_f32_fp8_sdwa v[212:213], v124 src0_sel:WORD_1
	v_cvt_pk_f32_fp8_sdwa v[222:223], v123 src0_sel:WORD_1
	v_lshl_or_b32 v82, v82, 7, v209
	global_load_dwordx4 v[120:123], v82, s[6:7]
	v_pk_fma_f32 v[204:205], v[214:215], v[198:199], v[204:205]
	v_cvt_pk_f32_fp8_e32 v[214:215], v125
	v_pk_fma_f32 v[204:205], v[216:217], v[184:185], v[204:205]
	v_cvt_pk_f32_fp8_sdwa v[216:217], v125 src0_sel:WORD_1
	v_pk_fma_f32 v[204:205], v[218:219], v[188:189], v[204:205]
	v_cvt_pk_f32_fp8_e32 v[218:219], v126
	v_pk_mul_f32 v[210:211], v[210:211], v[186:187]
	v_pk_fma_f32 v[204:205], v[220:221], v[192:193], v[204:205]
	v_cvt_pk_f32_fp8_sdwa v[220:221], v126 src0_sel:WORD_1
	v_pk_fma_f32 v[210:211], v[212:213], v[190:191], v[210:211]
	v_cvt_pk_f32_fp8_e32 v[212:213], v128
	v_pk_fma_f32 v[204:205], v[222:223], v[196:197], v[204:205]
	v_cvt_pk_f32_fp8_e32 v[222:223], v127
	v_pk_fma_f32 v[210:211], v[214:215], v[194:195], v[210:211]
	v_cvt_pk_f32_fp8_sdwa v[214:215], v128 src0_sel:WORD_1
	v_cvt_pk_f32_fp8_sdwa v[224:225], v127 src0_sel:WORD_1
	v_lshl_or_b32 v83, v83, 7, v209
	global_load_dwordx4 v[124:127], v83, s[6:7]
	v_pk_fma_f32 v[210:211], v[216:217], v[198:199], v[210:211]
	v_cvt_pk_f32_fp8_e32 v[216:217], v129
	v_pk_fma_f32 v[210:211], v[218:219], v[184:185], v[210:211]
	v_cvt_pk_f32_fp8_sdwa v[218:219], v129 src0_sel:WORD_1
	v_pk_fma_f32 v[210:211], v[220:221], v[188:189], v[210:211]
	v_cvt_pk_f32_fp8_e32 v[220:221], v130
	v_pk_mul_f32 v[212:213], v[212:213], v[186:187]
	v_pk_fma_f32 v[210:211], v[222:223], v[192:193], v[210:211]
	v_cvt_pk_f32_fp8_sdwa v[222:223], v130 src0_sel:WORD_1
	v_pk_fma_f32 v[212:213], v[214:215], v[190:191], v[212:213]
	v_cvt_pk_f32_fp8_e32 v[214:215], v132
	v_pk_fma_f32 v[210:211], v[224:225], v[196:197], v[210:211]
	v_cvt_pk_f32_fp8_e32 v[224:225], v131
	v_pk_fma_f32 v[212:213], v[216:217], v[194:195], v[212:213]
	v_cvt_pk_f32_fp8_sdwa v[216:217], v132 src0_sel:WORD_1
	v_cvt_pk_f32_fp8_sdwa v[226:227], v131 src0_sel:WORD_1
	v_lshl_or_b32 v72, v72, 7, v209
	global_load_dwordx4 v[128:131], v72, s[6:7]
	v_pk_fma_f32 v[212:213], v[218:219], v[198:199], v[212:213]
	v_cvt_pk_f32_fp8_e32 v[218:219], v133
	v_pk_fma_f32 v[212:213], v[220:221], v[184:185], v[212:213]
	v_cvt_pk_f32_fp8_sdwa v[220:221], v133 src0_sel:WORD_1
	v_pk_fma_f32 v[212:213], v[222:223], v[188:189], v[212:213]
	v_cvt_pk_f32_fp8_e32 v[222:223], v134
	v_pk_mul_f32 v[214:215], v[214:215], v[186:187]
	v_pk_fma_f32 v[212:213], v[224:225], v[192:193], v[212:213]
	v_cvt_pk_f32_fp8_sdwa v[224:225], v134 src0_sel:WORD_1
	v_pk_fma_f32 v[214:215], v[216:217], v[190:191], v[214:215]
	v_cvt_pk_f32_fp8_e32 v[216:217], v136
	v_pk_fma_f32 v[212:213], v[226:227], v[196:197], v[212:213]
	v_cvt_pk_f32_fp8_e32 v[226:227], v135
	v_pk_fma_f32 v[214:215], v[218:219], v[194:195], v[214:215]
	v_cvt_pk_f32_fp8_sdwa v[218:219], v136 src0_sel:WORD_1
	v_cvt_pk_f32_fp8_sdwa v[228:229], v135 src0_sel:WORD_1
	v_lshl_or_b32 v73, v73, 7, v209
	global_load_dwordx4 v[132:135], v73, s[6:7]
	v_pk_fma_f32 v[214:215], v[220:221], v[198:199], v[214:215]
	v_cvt_pk_f32_fp8_e32 v[220:221], v137
	v_pk_fma_f32 v[214:215], v[222:223], v[184:185], v[214:215]
	v_cvt_pk_f32_fp8_sdwa v[222:223], v137 src0_sel:WORD_1
	v_pk_fma_f32 v[214:215], v[224:225], v[188:189], v[214:215]
	v_cvt_pk_f32_fp8_e32 v[224:225], v138
	v_pk_mul_f32 v[216:217], v[216:217], v[186:187]
	v_pk_fma_f32 v[214:215], v[226:227], v[192:193], v[214:215]
	v_cvt_pk_f32_fp8_sdwa v[226:227], v138 src0_sel:WORD_1
	v_pk_fma_f32 v[216:217], v[218:219], v[190:191], v[216:217]
	v_cvt_pk_f32_fp8_e32 v[218:219], v140
	v_pk_fma_f32 v[214:215], v[228:229], v[196:197], v[214:215]
	v_cvt_pk_f32_fp8_e32 v[228:229], v139
	v_pk_fma_f32 v[216:217], v[220:221], v[194:195], v[216:217]
	v_cvt_pk_f32_fp8_sdwa v[220:221], v140 src0_sel:WORD_1
	v_cvt_pk_f32_fp8_sdwa v[230:231], v139 src0_sel:WORD_1
	v_lshl_or_b32 v74, v74, 7, v209
	global_load_dwordx4 v[136:139], v74, s[6:7]
	v_pk_fma_f32 v[216:217], v[222:223], v[198:199], v[216:217]
	v_cvt_pk_f32_fp8_e32 v[222:223], v141
	v_pk_fma_f32 v[216:217], v[224:225], v[184:185], v[216:217]
	v_cvt_pk_f32_fp8_sdwa v[224:225], v141 src0_sel:WORD_1
	v_pk_fma_f32 v[216:217], v[226:227], v[188:189], v[216:217]
	v_cvt_pk_f32_fp8_e32 v[226:227], v142
	v_pk_mul_f32 v[218:219], v[218:219], v[186:187]
	v_pk_fma_f32 v[216:217], v[228:229], v[192:193], v[216:217]
	v_cvt_pk_f32_fp8_sdwa v[228:229], v142 src0_sel:WORD_1
	v_pk_fma_f32 v[218:219], v[220:221], v[190:191], v[218:219]
	v_cvt_pk_f32_fp8_e32 v[220:221], v144
	v_pk_fma_f32 v[216:217], v[230:231], v[196:197], v[216:217]
	v_cvt_pk_f32_fp8_e32 v[230:231], v143
	v_pk_fma_f32 v[218:219], v[222:223], v[194:195], v[218:219]
	v_cvt_pk_f32_fp8_sdwa v[222:223], v144 src0_sel:WORD_1
	v_cvt_pk_f32_fp8_sdwa v[232:233], v143 src0_sel:WORD_1
	v_lshl_or_b32 v75, v75, 7, v209
	global_load_dwordx4 v[140:143], v75, s[6:7]
	v_pk_fma_f32 v[218:219], v[224:225], v[198:199], v[218:219]
	v_cvt_pk_f32_fp8_e32 v[224:225], v145
	v_pk_fma_f32 v[218:219], v[226:227], v[184:185], v[218:219]
	v_cvt_pk_f32_fp8_sdwa v[226:227], v145 src0_sel:WORD_1
	v_pk_fma_f32 v[218:219], v[228:229], v[188:189], v[218:219]
	v_cvt_pk_f32_fp8_e32 v[228:229], v146
	v_pk_mul_f32 v[220:221], v[220:221], v[186:187]
	v_pk_fma_f32 v[218:219], v[230:231], v[192:193], v[218:219]
	v_cvt_pk_f32_fp8_sdwa v[230:231], v146 src0_sel:WORD_1
	v_pk_fma_f32 v[220:221], v[222:223], v[190:191], v[220:221]
	v_cvt_pk_f32_fp8_e32 v[222:223], v148
	v_pk_fma_f32 v[218:219], v[232:233], v[196:197], v[218:219]
	v_cvt_pk_f32_fp8_e32 v[232:233], v147
	v_pk_fma_f32 v[220:221], v[224:225], v[194:195], v[220:221]
	v_cvt_pk_f32_fp8_sdwa v[224:225], v148 src0_sel:WORD_1
	v_cvt_pk_f32_fp8_sdwa v[234:235], v147 src0_sel:WORD_1
	v_lshl_or_b32 v68, v68, 7, v209
	global_load_dwordx4 v[144:147], v68, s[6:7]
	v_pk_fma_f32 v[220:221], v[226:227], v[198:199], v[220:221]
	v_cvt_pk_f32_fp8_e32 v[226:227], v149
	v_pk_fma_f32 v[220:221], v[228:229], v[184:185], v[220:221]
	v_cvt_pk_f32_fp8_sdwa v[228:229], v149 src0_sel:WORD_1
	v_pk_fma_f32 v[220:221], v[230:231], v[188:189], v[220:221]
	v_cvt_pk_f32_fp8_e32 v[230:231], v150
	v_pk_mul_f32 v[222:223], v[222:223], v[186:187]
	v_pk_fma_f32 v[220:221], v[232:233], v[192:193], v[220:221]
	v_cvt_pk_f32_fp8_sdwa v[232:233], v150 src0_sel:WORD_1
	v_pk_fma_f32 v[222:223], v[224:225], v[190:191], v[222:223]
	v_cvt_pk_f32_fp8_e32 v[224:225], v152
	v_pk_fma_f32 v[220:221], v[234:235], v[196:197], v[220:221]
	v_cvt_pk_f32_fp8_e32 v[234:235], v151
	v_pk_fma_f32 v[222:223], v[226:227], v[194:195], v[222:223]
	v_cvt_pk_f32_fp8_sdwa v[226:227], v152 src0_sel:WORD_1
	v_cvt_pk_f32_fp8_sdwa v[236:237], v151 src0_sel:WORD_1
	v_lshl_or_b32 v69, v69, 7, v209
	global_load_dwordx4 v[148:151], v69, s[6:7]
	v_pk_fma_f32 v[222:223], v[228:229], v[198:199], v[222:223]
	v_cvt_pk_f32_fp8_e32 v[228:229], v153
	v_pk_fma_f32 v[222:223], v[230:231], v[184:185], v[222:223]
	v_cvt_pk_f32_fp8_sdwa v[230:231], v153 src0_sel:WORD_1
	v_pk_fma_f32 v[222:223], v[232:233], v[188:189], v[222:223]
	v_cvt_pk_f32_fp8_e32 v[232:233], v154
	v_pk_mul_f32 v[224:225], v[224:225], v[186:187]
	v_pk_fma_f32 v[222:223], v[234:235], v[192:193], v[222:223]
	v_cvt_pk_f32_fp8_sdwa v[234:235], v154 src0_sel:WORD_1
	v_pk_fma_f32 v[224:225], v[226:227], v[190:191], v[224:225]
	v_cvt_pk_f32_fp8_e32 v[226:227], v156
	v_pk_fma_f32 v[222:223], v[236:237], v[196:197], v[222:223]
	v_cvt_pk_f32_fp8_e32 v[236:237], v155
	v_pk_fma_f32 v[224:225], v[228:229], v[194:195], v[224:225]
	v_cvt_pk_f32_fp8_sdwa v[228:229], v156 src0_sel:WORD_1
	v_cvt_pk_f32_fp8_sdwa v[238:239], v155 src0_sel:WORD_1
	v_lshl_or_b32 v70, v70, 7, v209
	global_load_dwordx4 v[152:155], v70, s[6:7]
	v_pk_fma_f32 v[224:225], v[230:231], v[198:199], v[224:225]
	v_cvt_pk_f32_fp8_e32 v[230:231], v157
	v_pk_fma_f32 v[224:225], v[232:233], v[184:185], v[224:225]
	v_cvt_pk_f32_fp8_sdwa v[232:233], v157 src0_sel:WORD_1
	v_pk_fma_f32 v[224:225], v[234:235], v[188:189], v[224:225]
	v_cvt_pk_f32_fp8_e32 v[234:235], v158
	v_pk_mul_f32 v[226:227], v[226:227], v[186:187]
	v_pk_fma_f32 v[224:225], v[236:237], v[192:193], v[224:225]
	v_cvt_pk_f32_fp8_sdwa v[236:237], v158 src0_sel:WORD_1
	v_pk_fma_f32 v[226:227], v[228:229], v[190:191], v[226:227]
	v_cvt_pk_f32_fp8_e32 v[228:229], v160
	v_pk_fma_f32 v[224:225], v[238:239], v[196:197], v[224:225]
	v_cvt_pk_f32_fp8_e32 v[238:239], v159
	v_pk_fma_f32 v[226:227], v[230:231], v[194:195], v[226:227]
	v_cvt_pk_f32_fp8_sdwa v[230:231], v160 src0_sel:WORD_1
	v_cvt_pk_f32_fp8_sdwa v[240:241], v159 src0_sel:WORD_1
	v_lshl_or_b32 v71, v71, 7, v209
	global_load_dwordx4 v[156:159], v71, s[6:7]
	v_pk_fma_f32 v[226:227], v[232:233], v[198:199], v[226:227]
	v_cvt_pk_f32_fp8_e32 v[232:233], v161
	v_pk_fma_f32 v[226:227], v[234:235], v[184:185], v[226:227]
	v_cvt_pk_f32_fp8_sdwa v[234:235], v161 src0_sel:WORD_1
	v_pk_fma_f32 v[226:227], v[236:237], v[188:189], v[226:227]
	v_cvt_pk_f32_fp8_e32 v[236:237], v162
	v_pk_mul_f32 v[228:229], v[228:229], v[186:187]
	v_pk_fma_f32 v[226:227], v[238:239], v[192:193], v[226:227]
	v_cvt_pk_f32_fp8_sdwa v[238:239], v162 src0_sel:WORD_1
	v_pk_fma_f32 v[228:229], v[230:231], v[190:191], v[228:229]
	v_cvt_pk_f32_fp8_e32 v[230:231], v164
	v_pk_fma_f32 v[226:227], v[240:241], v[196:197], v[226:227]
	v_cvt_pk_f32_fp8_e32 v[240:241], v163
	v_pk_fma_f32 v[228:229], v[232:233], v[194:195], v[228:229]
	v_cvt_pk_f32_fp8_sdwa v[232:233], v164 src0_sel:WORD_1
	v_cvt_pk_f32_fp8_sdwa v[242:243], v163 src0_sel:WORD_1
	v_lshl_or_b32 v64, v64, 7, v209
	global_load_dwordx4 v[160:163], v64, s[6:7]
	v_pk_fma_f32 v[228:229], v[234:235], v[198:199], v[228:229]
	v_cvt_pk_f32_fp8_e32 v[234:235], v165
	v_pk_fma_f32 v[228:229], v[236:237], v[184:185], v[228:229]
	v_cvt_pk_f32_fp8_sdwa v[236:237], v165 src0_sel:WORD_1
	v_pk_fma_f32 v[228:229], v[238:239], v[188:189], v[228:229]
	v_cvt_pk_f32_fp8_e32 v[238:239], v166
	v_pk_mul_f32 v[230:231], v[230:231], v[186:187]
	v_pk_fma_f32 v[228:229], v[240:241], v[192:193], v[228:229]
	v_cvt_pk_f32_fp8_sdwa v[240:241], v166 src0_sel:WORD_1
	v_pk_fma_f32 v[230:231], v[232:233], v[190:191], v[230:231]
	v_cvt_pk_f32_fp8_e32 v[232:233], v168
	v_pk_fma_f32 v[228:229], v[242:243], v[196:197], v[228:229]
	v_cvt_pk_f32_fp8_e32 v[242:243], v167
	v_pk_fma_f32 v[230:231], v[234:235], v[194:195], v[230:231]
	v_cvt_pk_f32_fp8_sdwa v[234:235], v168 src0_sel:WORD_1
	v_cvt_pk_f32_fp8_sdwa v[244:245], v167 src0_sel:WORD_1
	v_lshl_or_b32 v65, v65, 7, v209
	global_load_dwordx4 v[164:167], v65, s[6:7]
	v_pk_fma_f32 v[230:231], v[236:237], v[198:199], v[230:231]
	v_cvt_pk_f32_fp8_e32 v[236:237], v169
	v_pk_fma_f32 v[230:231], v[238:239], v[184:185], v[230:231]
	v_cvt_pk_f32_fp8_sdwa v[238:239], v169 src0_sel:WORD_1
	v_pk_fma_f32 v[230:231], v[240:241], v[188:189], v[230:231]
	v_cvt_pk_f32_fp8_e32 v[240:241], v170
	v_pk_mul_f32 v[232:233], v[232:233], v[186:187]
	v_pk_fma_f32 v[230:231], v[242:243], v[192:193], v[230:231]
	v_cvt_pk_f32_fp8_sdwa v[242:243], v170 src0_sel:WORD_1
	v_pk_fma_f32 v[232:233], v[234:235], v[190:191], v[232:233]
; #define PD_E(t, E) do { const char* eb_ = eiu + (size_t)(t) * 512; _Pragma("unroll") for (int q = 0; q < 4; ++q) E[q] = *(const i32x4_t*)(eb_ + (eio + 16u * q)); } while (0)
; #define PD_H(t, H) do { const char* hb_ = h2u + (size_t)(t) * 2048; H[0] = *(const u32x4*)(hb_ + h2o); H[1] = *(const u32x4*)(hb_ + (h2o + 16u)); } while (0)
; DI void phase_peerdown(const Params& p, int bid, int nb) {
;     ...
;     const int t3 = t2 + nw; if (t3 < T_) PD_E(t3, eB);
;     PD_MATH(t1, wB, hB);
;     if (t2 >= T_) break;
;     if (t3 < T_) PD_H(t3, hB);
;     t = t2; t1 = t3;
	v_cvt_pk_f32_fp8_e32 v[234:235], v172
	v_pk_fma_f32 v[230:231], v[244:245], v[196:197], v[230:231]
	v_cvt_pk_f32_fp8_e32 v[244:245], v171
	v_pk_fma_f32 v[232:233], v[236:237], v[194:195], v[232:233]
	v_cvt_pk_f32_fp8_sdwa v[236:237], v172 src0_sel:WORD_1
	v_cvt_pk_f32_fp8_sdwa v[246:247], v171 src0_sel:WORD_1
	v_lshl_or_b32 v66, v66, 7, v209
	global_load_dwordx4 v[168:171], v66, s[6:7]
	v_pk_fma_f32 v[232:233], v[238:239], v[198:199], v[232:233]
	v_cvt_pk_f32_fp8_e32 v[238:239], v173
	v_pk_fma_f32 v[232:233], v[240:241], v[184:185], v[232:233]
	v_cvt_pk_f32_fp8_sdwa v[240:241], v173 src0_sel:WORD_1
	v_pk_fma_f32 v[232:233], v[242:243], v[188:189], v[232:233]
	v_cvt_pk_f32_fp8_e32 v[242:243], v174
	v_pk_mul_f32 v[186:187], v[234:235], v[186:187]
	v_pk_fma_f32 v[232:233], v[244:245], v[192:193], v[232:233]
	v_cvt_pk_f32_fp8_sdwa v[244:245], v174 src0_sel:WORD_1
	v_pk_fma_f32 v[186:187], v[236:237], v[190:191], v[186:187]
	v_pk_fma_f32 v[232:233], v[246:247], v[196:197], v[232:233]
	v_cvt_pk_f32_fp8_e32 v[246:247], v175
	v_pk_fma_f32 v[186:187], v[238:239], v[194:195], v[186:187]
	v_cvt_pk_f32_fp8_sdwa v[248:249], v175 src0_sel:WORD_1
	v_lshl_or_b32 v67, v67, 7, v209
	global_load_dwordx4 v[172:175], v67, s[6:7]
	v_pk_fma_f32 v[186:187], v[240:241], v[198:199], v[186:187]
	v_mov_b32_e32 v194, v220
	v_pk_fma_f32 v[184:185], v[242:243], v[184:185], v[186:187]
	v_mov_b32_e32 v186, v200
	v_pk_fma_f32 v[184:185], v[244:245], v[188:189], v[184:185]
	v_mov_b32_e32 v187, v202
	v_pk_fma_f32 v[184:185], v[246:247], v[192:193], v[184:185]
	v_mov_b32_e32 v202, v201
	v_pk_fma_f32 v[184:185], v[248:249], v[196:197], v[184:185]
	v_mov_b32_e32 v195, v222
	v_mov_b32_e32 v222, v221
	v_pk_add_f32 v[186:187], v[186:187], v[202:203]
	v_pk_add_f32 v[194:195], v[194:195], v[222:223]
	v_mov_b32_e32 v200, v232
	v_mov_b32_e32 v201, v184
	v_mov_b32_e32 v184, v233
	v_mov_b32_e32 v188, v204
	v_mov_b32_e32 v189, v210
	v_mov_b32_e32 v210, v205
	v_mov_b32_e32 v196, v224
	v_mov_b32_e32 v197, v226
	v_mov_b32_e32 v226, v225
	v_pk_add_f32 v[184:185], v[200:201], v[184:185]
	v_cndmask_b32_e64 v200, v186, v194, s[4:5]
	v_cndmask_b32_e64 v202, v194, v186, s[4:5]
	v_cndmask_b32_e64 v186, v187, v195, s[4:5]
	v_pk_add_f32 v[188:189], v[188:189], v[210:211]
	v_pk_add_f32 v[196:197], v[196:197], v[226:227]
	v_mov_b32_dpp v200, v200 row_half_mirror row_mask:0xf bank_mask:0xf bound_ctrl:1
	v_cndmask_b32_e64 v203, v195, v187, s[4:5]
	v_mov_b32_dpp v201, v186 row_half_mirror row_mask:0xf bank_mask:0xf bound_ctrl:1
	v_mov_b32_e32 v190, v212
	v_mov_b32_e32 v191, v214
	v_mov_b32_e32 v214, v213
	v_mov_b32_e32 v198, v228
	v_mov_b32_e32 v199, v230
	v_mov_b32_e32 v230, v229
	v_pk_add_f32 v[186:187], v[202:203], v[200:201]
	v_cndmask_b32_e64 v194, v188, v196, s[4:5]
	v_cndmask_b32_e64 v200, v196, v188, s[4:5]
	v_cndmask_b32_e64 v188, v189, v197, s[4:5]
	v_pk_add_f32 v[190:191], v[190:191], v[214:215]
	v_pk_add_f32 v[198:199], v[198:199], v[230:231]
	v_mov_b32_dpp v194, v194 row_half_mirror row_mask:0xf bank_mask:0xf bound_ctrl:1
	v_cndmask_b32_e64 v201, v197, v189, s[4:5]
	v_mov_b32_dpp v195, v188 row_half_mirror row_mask:0xf bank_mask:0xf bound_ctrl:1
	v_mov_b32_e32 v192, v216
	v_mov_b32_e32 v193, v218
	v_mov_b32_e32 v218, v217
	v_pk_add_f32 v[188:189], v[200:201], v[194:195]
	v_cndmask_b32_e64 v194, v190, v198, s[4:5]
	v_cndmask_b32_e64 v196, v198, v190, s[4:5]
	v_cndmask_b32_e64 v190, v191, v199, s[4:5]
	v_pk_add_f32 v[192:193], v[192:193], v[218:219]
	v_mov_b32_dpp v194, v194 row_half_mirror row_mask:0xf bank_mask:0xf bound_ctrl:1
	v_cndmask_b32_e64 v197, v199, v191, s[4:5]
	v_mov_b32_dpp v195, v190 row_half_mirror row_mask:0xf bank_mask:0xf bound_ctrl:1
	v_pk_add_f32 v[190:191], v[196:197], v[194:195]
	v_cndmask_b32_e64 v194, v192, v184, s[4:5]
	v_cndmask_b32_e64 v196, v184, v192, s[4:5]
	v_cndmask_b32_e64 v184, v193, v185, s[4:5]
	v_mov_b32_dpp v194, v194 row_half_mirror row_mask:0xf bank_mask:0xf bound_ctrl:1
	v_cndmask_b32_e64 v197, v185, v193, s[4:5]
	v_mov_b32_dpp v195, v184 row_half_mirror row_mask:0xf bank_mask:0xf bound_ctrl:1
	v_pk_add_f32 v[184:185], v[196:197], v[194:195]
	v_cndmask_b32_e64 v192, v186, v190, s[2:3]
	v_cndmask_b32_e64 v194, v190, v186, s[2:3]
	v_cndmask_b32_e64 v186, v187, v191, s[2:3]
	v_mov_b32_dpp v192, v192 quad_perm:[2,3,0,1] row_mask:0xf bank_mask:0xf bound_ctrl:1
	v_cndmask_b32_e64 v195, v191, v187, s[2:3]
	v_mov_b32_dpp v193, v186 quad_perm:[2,3,0,1] row_mask:0xf bank_mask:0xf bound_ctrl:1
	v_pk_add_f32 v[186:187], v[194:195], v[192:193]
	v_cndmask_b32_e64 v190, v188, v184, s[2:3]
	v_cndmask_b32_e64 v192, v184, v188, s[2:3]
	v_cndmask_b32_e64 v184, v189, v185, s[2:3]
	v_mov_b32_dpp v190, v190 quad_perm:[2,3,0,1] row_mask:0xf bank_mask:0xf bound_ctrl:1
	v_cndmask_b32_e64 v193, v185, v189, s[2:3]
	v_mov_b32_dpp v191, v184 quad_perm:[2,3,0,1] row_mask:0xf bank_mask:0xf bound_ctrl:1
	v_pk_add_f32 v[184:185], v[192:193], v[190:191]
	s_ashr_i32 s11, s10, 31
	v_cndmask_b32_e64 v188, v186, v184, s[0:1]
	v_cndmask_b32_e64 v190, v184, v186, s[0:1]
	v_cndmask_b32_e64 v184, v187, v185, s[0:1]
	v_mov_b32_dpp v188, v188 quad_perm:[1,0,3,2] row_mask:0xf bank_mask:0xf bound_ctrl:1
	v_cndmask_b32_e64 v191, v185, v187, s[0:1]
	v_mov_b32_dpp v189, v184 quad_perm:[1,0,3,2] row_mask:0xf bank_mask:0xf bound_ctrl:1
	v_pk_add_f32 v[184:185], v[190:191], v[188:189]
	s_lshl_b64 s[10:11], s[10:11], 8
	v_cvt_pk_bf16_f32 v186, v184, v185
	v_lshl_add_u64 v[184:185], v[178:179], 0, s[10:11]
	global_store_dword v[184:185], v186, off
	s_add_u32 s20, s12, 0x300
	s_lshl_b32 s20, s20, 11
	v_lshl_add_u64 v[108:109], v[182:183], 0, s[20:21]
	global_load_dwordx4 v[100:103], v[108:109], off offset:16
	s_nop 0
	global_load_dwordx4 v[108:111], v[108:109], off
	s_add_u32 s20, s12, 0x500
	s_lshl_b32 s20, s20, 9
	v_lshl_add_u64 v[80:81], v[180:181], 0, s[20:21]
	global_load_dwordx4 v[64:67], v[80:81], off offset:48
	global_load_dwordx4 v[68:71], v[80:81], off offset:32
	global_load_dwordx4 v[72:75], v[80:81], off offset:16
	s_nop 0
	global_load_dwordx4 v[80:83], v[80:81], off
	s_add_u32 s12, s12, 0x200
	s_sub_u32 s13, s13, 1
	s_cmp_lg_u32 s13, 0
	s_cbranch_scc1 .Lpd2_loop
	s_mov_b32 s14, s12
	s_waitcnt vmcnt(23)
	v_cvt_pk_f32_fp8_e32 v[200:201], v24
	v_cvt_pk_f32_fp8_sdwa v[202:203], v24 src0_sel:WORD_1
	v_cvt_pk_f32_fp8_e32 v[204:205], v25
	v_lshlrev_b32_e32 v186, 16, v20
	v_and_b32_e32 v187, 0xffff0000, v20
	v_cvt_pk_f32_fp8_sdwa v[210:211], v25 src0_sel:WORD_1
	v_lshlrev_b32_e32 v190, 16, v21
	v_and_b32_e32 v191, 0xffff0000, v21
	v_cvt_pk_f32_fp8_e32 v[212:213], v26
	v_pk_mul_f32 v[200:201], v[200:201], v[186:187]
	v_lshlrev_b32_e32 v194, 16, v22
	v_and_b32_e32 v195, 0xffff0000, v22
	v_cvt_pk_f32_fp8_sdwa v[214:215], v26 src0_sel:WORD_1
	v_pk_fma_f32 v[200:201], v[202:203], v[190:191], v[200:201]
	v_cvt_pk_f32_fp8_e32 v[202:203], v28
	v_lshlrev_b32_e32 v198, 16, v23
	v_and_b32_e32 v199, 0xffff0000, v23
	v_cvt_pk_f32_fp8_e32 v[216:217], v27
	v_pk_fma_f32 v[200:201], v[204:205], v[194:195], v[200:201]
	v_cvt_pk_f32_fp8_sdwa v[204:205], v28 src0_sel:WORD_1
	v_lshlrev_b32_e32 v184, 16, v16
	v_and_b32_e32 v185, 0xffff0000, v16
	v_cvt_pk_f32_fp8_sdwa v[218:219], v27 src0_sel:WORD_1
	v_lshl_or_b32 v0, v0, 7, v209
	global_load_dwordx4 v[24:27], v0, s[6:7]
	v_pk_fma_f32 v[200:201], v[210:211], v[198:199], v[200:201]
	v_cvt_pk_f32_fp8_e32 v[210:211], v29
	v_lshlrev_b32_e32 v188, 16, v17
	v_and_b32_e32 v189, 0xffff0000, v17
	v_pk_fma_f32 v[200:201], v[212:213], v[184:185], v[200:201]
	v_cvt_pk_f32_fp8_sdwa v[212:213], v29 src0_sel:WORD_1
	v_lshlrev_b32_e32 v192, 16, v18
	v_and_b32_e32 v193, 0xffff0000, v18
	v_pk_fma_f32 v[200:201], v[214:215], v[188:189], v[200:201]
	v_cvt_pk_f32_fp8_e32 v[214:215], v30
	v_pk_mul_f32 v[202:203], v[202:203], v[186:187]
	v_lshlrev_b32_e32 v196, 16, v19
	v_and_b32_e32 v197, 0xffff0000, v19
	v_pk_fma_f32 v[200:201], v[216:217], v[192:193], v[200:201]
	v_cvt_pk_f32_fp8_sdwa v[216:217], v30 src0_sel:WORD_1
	v_pk_fma_f32 v[202:203], v[204:205], v[190:191], v[202:203]
	v_cvt_pk_f32_fp8_e32 v[204:205], v32
	v_pk_fma_f32 v[200:201], v[218:219], v[196:197], v[200:201]
	v_cvt_pk_f32_fp8_e32 v[218:219], v31
	v_pk_fma_f32 v[202:203], v[210:211], v[194:195], v[202:203]
	v_cvt_pk_f32_fp8_sdwa v[210:211], v32 src0_sel:WORD_1
	v_cvt_pk_f32_fp8_sdwa v[220:221], v31 src0_sel:WORD_1
	v_lshl_or_b32 v1, v1, 7, v209
	global_load_dwordx4 v[28:31], v1, s[6:7]
	v_pk_fma_f32 v[202:203], v[212:213], v[198:199], v[202:203]
	v_cvt_pk_f32_fp8_e32 v[212:213], v33
	v_pk_fma_f32 v[202:203], v[214:215], v[184:185], v[202:203]
	v_cvt_pk_f32_fp8_sdwa v[214:215], v33 src0_sel:WORD_1
	v_pk_fma_f32 v[202:203], v[216:217], v[188:189], v[202:203]
	v_cvt_pk_f32_fp8_e32 v[216:217], v34
	v_pk_mul_f32 v[204:205], v[204:205], v[186:187]
	v_pk_fma_f32 v[202:203], v[218:219], v[192:193], v[202:203]
	v_cvt_pk_f32_fp8_sdwa v[218:219], v34 src0_sel:WORD_1
	v_pk_fma_f32 v[204:205], v[210:211], v[190:191], v[204:205]
	v_cvt_pk_f32_fp8_e32 v[210:211], v36
	v_pk_fma_f32 v[202:203], v[220:221], v[196:197], v[202:203]
	v_cvt_pk_f32_fp8_e32 v[220:221], v35
	v_pk_fma_f32 v[204:205], v[212:213], v[194:195], v[204:205]
	v_cvt_pk_f32_fp8_sdwa v[212:213], v36 src0_sel:WORD_1
	v_cvt_pk_f32_fp8_sdwa v[222:223], v35 src0_sel:WORD_1
	v_lshl_or_b32 v2, v2, 7, v209
	global_load_dwordx4 v[32:35], v2, s[6:7]
	v_pk_fma_f32 v[204:205], v[214:215], v[198:199], v[204:205]
	v_cvt_pk_f32_fp8_e32 v[214:215], v37
	v_pk_fma_f32 v[204:205], v[216:217], v[184:185], v[204:205]
	v_cvt_pk_f32_fp8_sdwa v[216:217], v37 src0_sel:WORD_1
	v_pk_fma_f32 v[204:205], v[218:219], v[188:189], v[204:205]
	v_cvt_pk_f32_fp8_e32 v[218:219], v38
	v_pk_mul_f32 v[210:211], v[210:211], v[186:187]
	v_pk_fma_f32 v[204:205], v[220:221], v[192:193], v[204:205]
	v_cvt_pk_f32_fp8_sdwa v[220:221], v38 src0_sel:WORD_1
	v_pk_fma_f32 v[210:211], v[212:213], v[190:191], v[210:211]
	v_cvt_pk_f32_fp8_e32 v[212:213], v40
	v_pk_fma_f32 v[204:205], v[222:223], v[196:197], v[204:205]
	v_cvt_pk_f32_fp8_e32 v[222:223], v39
	v_pk_fma_f32 v[210:211], v[214:215], v[194:195], v[210:211]
	v_cvt_pk_f32_fp8_sdwa v[214:215], v40 src0_sel:WORD_1
	v_cvt_pk_f32_fp8_sdwa v[224:225], v39 src0_sel:WORD_1
	v_lshl_or_b32 v3, v3, 7, v209
	global_load_dwordx4 v[36:39], v3, s[6:7]
	v_pk_fma_f32 v[210:211], v[216:217], v[198:199], v[210:211]
	v_cvt_pk_f32_fp8_e32 v[216:217], v41
	v_pk_fma_f32 v[210:211], v[218:219], v[184:185], v[210:211]
	v_cvt_pk_f32_fp8_sdwa v[218:219], v41 src0_sel:WORD_1
	v_pk_fma_f32 v[210:211], v[220:221], v[188:189], v[210:211]
	v_cvt_pk_f32_fp8_e32 v[220:221], v42
	v_pk_mul_f32 v[212:213], v[212:213], v[186:187]
	v_pk_fma_f32 v[210:211], v[222:223], v[192:193], v[210:211]
	v_cvt_pk_f32_fp8_sdwa v[222:223], v42 src0_sel:WORD_1
	v_pk_fma_f32 v[212:213], v[214:215], v[190:191], v[212:213]
	v_cvt_pk_f32_fp8_e32 v[214:215], v44
	v_pk_fma_f32 v[210:211], v[224:225], v[196:197], v[210:211]
	v_cvt_pk_f32_fp8_e32 v[224:225], v43
	v_pk_fma_f32 v[212:213], v[216:217], v[194:195], v[212:213]
	v_cvt_pk_f32_fp8_sdwa v[216:217], v44 src0_sel:WORD_1
	v_cvt_pk_f32_fp8_sdwa v[226:227], v43 src0_sel:WORD_1
	v_lshl_or_b32 v4, v4, 7, v209
	global_load_dwordx4 v[40:43], v4, s[6:7]
	v_pk_fma_f32 v[212:213], v[218:219], v[198:199], v[212:213]
	v_cvt_pk_f32_fp8_e32 v[218:219], v45
	v_pk_fma_f32 v[212:213], v[220:221], v[184:185], v[212:213]
	v_cvt_pk_f32_fp8_sdwa v[220:221], v45 src0_sel:WORD_1
	v_pk_fma_f32 v[212:213], v[222:223], v[188:189], v[212:213]
	v_cvt_pk_f32_fp8_e32 v[222:223], v46
	v_pk_mul_f32 v[214:215], v[214:215], v[186:187]
	v_pk_fma_f32 v[212:213], v[224:225], v[192:193], v[212:213]
	v_cvt_pk_f32_fp8_sdwa v[224:225], v46 src0_sel:WORD_1
	v_pk_fma_f32 v[214:215], v[216:217], v[190:191], v[214:215]
	v_cvt_pk_f32_fp8_e32 v[216:217], v48
	v_pk_fma_f32 v[212:213], v[226:227], v[196:197], v[212:213]
	v_cvt_pk_f32_fp8_e32 v[226:227], v47
	v_pk_fma_f32 v[214:215], v[218:219], v[194:195], v[214:215]
	v_cvt_pk_f32_fp8_sdwa v[218:219], v48 src0_sel:WORD_1
	v_cvt_pk_f32_fp8_sdwa v[228:229], v47 src0_sel:WORD_1
	v_lshl_or_b32 v5, v5, 7, v209
	global_load_dwordx4 v[44:47], v5, s[6:7]
	v_pk_fma_f32 v[214:215], v[220:221], v[198:199], v[214:215]
	v_cvt_pk_f32_fp8_e32 v[220:221], v49
	v_pk_fma_f32 v[214:215], v[222:223], v[184:185], v[214:215]
	v_cvt_pk_f32_fp8_sdwa v[222:223], v49 src0_sel:WORD_1
	v_pk_fma_f32 v[214:215], v[224:225], v[188:189], v[214:215]
	v_cvt_pk_f32_fp8_e32 v[224:225], v50
	v_pk_mul_f32 v[216:217], v[216:217], v[186:187]
	v_pk_fma_f32 v[214:215], v[226:227], v[192:193], v[214:215]
	v_cvt_pk_f32_fp8_sdwa v[226:227], v50 src0_sel:WORD_1
	v_pk_fma_f32 v[216:217], v[218:219], v[190:191], v[216:217]
	v_cvt_pk_f32_fp8_e32 v[218:219], v52
	v_pk_fma_f32 v[214:215], v[228:229], v[196:197], v[214:215]
	v_cvt_pk_f32_fp8_e32 v[228:229], v51
	v_pk_fma_f32 v[216:217], v[220:221], v[194:195], v[216:217]
	v_cvt_pk_f32_fp8_sdwa v[220:221], v52 src0_sel:WORD_1
	v_cvt_pk_f32_fp8_sdwa v[230:231], v51 src0_sel:WORD_1
	v_lshl_or_b32 v6, v6, 7, v209
	global_load_dwordx4 v[48:51], v6, s[6:7]
	v_pk_fma_f32 v[216:217], v[222:223], v[198:199], v[216:217]
	v_cvt_pk_f32_fp8_e32 v[222:223], v53
	v_pk_fma_f32 v[216:217], v[224:225], v[184:185], v[216:217]
	v_cvt_pk_f32_fp8_sdwa v[224:225], v53 src0_sel:WORD_1
	v_pk_fma_f32 v[216:217], v[226:227], v[188:189], v[216:217]
	v_cvt_pk_f32_fp8_e32 v[226:227], v54
	v_pk_mul_f32 v[218:219], v[218:219], v[186:187]
	v_pk_fma_f32 v[216:217], v[228:229], v[192:193], v[216:217]
	v_cvt_pk_f32_fp8_sdwa v[228:229], v54 src0_sel:WORD_1
	v_pk_fma_f32 v[218:219], v[220:221], v[190:191], v[218:219]
	v_cvt_pk_f32_fp8_e32 v[220:221], v56
	v_pk_fma_f32 v[216:217], v[230:231], v[196:197], v[216:217]
	v_cvt_pk_f32_fp8_e32 v[230:231], v55
	v_pk_fma_f32 v[218:219], v[222:223], v[194:195], v[218:219]
	v_cvt_pk_f32_fp8_sdwa v[222:223], v56 src0_sel:WORD_1
	v_cvt_pk_f32_fp8_sdwa v[232:233], v55 src0_sel:WORD_1
	v_lshl_or_b32 v7, v7, 7, v209
	global_load_dwordx4 v[52:55], v7, s[6:7]
	v_pk_fma_f32 v[218:219], v[224:225], v[198:199], v[218:219]
	v_cvt_pk_f32_fp8_e32 v[224:225], v57
	v_pk_fma_f32 v[218:219], v[226:227], v[184:185], v[218:219]
	v_cvt_pk_f32_fp8_sdwa v[226:227], v57 src0_sel:WORD_1
	v_pk_fma_f32 v[218:219], v[228:229], v[188:189], v[218:219]
	v_cvt_pk_f32_fp8_e32 v[228:229], v58
	v_pk_mul_f32 v[220:221], v[220:221], v[186:187]
	v_pk_fma_f32 v[218:219], v[230:231], v[192:193], v[218:219]
	v_cvt_pk_f32_fp8_sdwa v[230:231], v58 src0_sel:WORD_1
	v_pk_fma_f32 v[220:221], v[222:223], v[190:191], v[220:221]
	v_cvt_pk_f32_fp8_e32 v[222:223], v60
	v_pk_fma_f32 v[218:219], v[232:233], v[196:197], v[218:219]
	v_cvt_pk_f32_fp8_e32 v[232:233], v59
	v_pk_fma_f32 v[220:221], v[224:225], v[194:195], v[220:221]
	v_cvt_pk_f32_fp8_sdwa v[224:225], v60 src0_sel:WORD_1
	v_cvt_pk_f32_fp8_sdwa v[234:235], v59 src0_sel:WORD_1
	v_lshl_or_b32 v8, v8, 7, v209
	global_load_dwordx4 v[56:59], v8, s[6:7]
	v_pk_fma_f32 v[220:221], v[226:227], v[198:199], v[220:221]
	v_cvt_pk_f32_fp8_e32 v[226:227], v61
	v_pk_fma_f32 v[220:221], v[228:229], v[184:185], v[220:221]
	v_cvt_pk_f32_fp8_sdwa v[228:229], v61 src0_sel:WORD_1
	v_pk_fma_f32 v[220:221], v[230:231], v[188:189], v[220:221]
	v_cvt_pk_f32_fp8_e32 v[230:231], v62
	v_pk_mul_f32 v[222:223], v[222:223], v[186:187]
	v_pk_fma_f32 v[220:221], v[232:233], v[192:193], v[220:221]
	v_cvt_pk_f32_fp8_sdwa v[232:233], v62 src0_sel:WORD_1
	v_pk_fma_f32 v[222:223], v[224:225], v[190:191], v[222:223]
	v_cvt_pk_f32_fp8_e32 v[224:225], v76
	v_pk_fma_f32 v[220:221], v[234:235], v[196:197], v[220:221]
	v_cvt_pk_f32_fp8_e32 v[234:235], v63
	v_pk_fma_f32 v[222:223], v[226:227], v[194:195], v[222:223]
	v_cvt_pk_f32_fp8_sdwa v[226:227], v76 src0_sel:WORD_1
	v_cvt_pk_f32_fp8_sdwa v[236:237], v63 src0_sel:WORD_1
	v_lshl_or_b32 v9, v9, 7, v209
	global_load_dwordx4 v[60:63], v9, s[6:7]
	v_pk_fma_f32 v[222:223], v[228:229], v[198:199], v[222:223]
	v_cvt_pk_f32_fp8_e32 v[228:229], v77
	v_pk_fma_f32 v[222:223], v[230:231], v[184:185], v[222:223]
	v_cvt_pk_f32_fp8_sdwa v[230:231], v77 src0_sel:WORD_1
	v_pk_fma_f32 v[222:223], v[232:233], v[188:189], v[222:223]
	v_cvt_pk_f32_fp8_e32 v[232:233], v78
	v_pk_mul_f32 v[224:225], v[224:225], v[186:187]
	v_pk_fma_f32 v[222:223], v[234:235], v[192:193], v[222:223]
	v_cvt_pk_f32_fp8_sdwa v[234:235], v78 src0_sel:WORD_1
	v_pk_fma_f32 v[224:225], v[226:227], v[190:191], v[224:225]
	v_cvt_pk_f32_fp8_e32 v[226:227], v84
	v_pk_fma_f32 v[222:223], v[236:237], v[196:197], v[222:223]
	v_cvt_pk_f32_fp8_e32 v[236:237], v79
	v_pk_fma_f32 v[224:225], v[228:229], v[194:195], v[224:225]
	v_cvt_pk_f32_fp8_sdwa v[228:229], v84 src0_sel:WORD_1
	v_cvt_pk_f32_fp8_sdwa v[238:239], v79 src0_sel:WORD_1
	v_lshl_or_b32 v10, v10, 7, v209
	global_load_dwordx4 v[76:79], v10, s[6:7]
	v_pk_fma_f32 v[224:225], v[230:231], v[198:199], v[224:225]
	v_cvt_pk_f32_fp8_e32 v[230:231], v85
	v_pk_fma_f32 v[224:225], v[232:233], v[184:185], v[224:225]
	v_cvt_pk_f32_fp8_sdwa v[232:233], v85 src0_sel:WORD_1
	v_pk_fma_f32 v[224:225], v[234:235], v[188:189], v[224:225]
	v_cvt_pk_f32_fp8_e32 v[234:235], v86
	v_pk_mul_f32 v[226:227], v[226:227], v[186:187]
	v_pk_fma_f32 v[224:225], v[236:237], v[192:193], v[224:225]
	v_cvt_pk_f32_fp8_sdwa v[236:237], v86 src0_sel:WORD_1
	v_pk_fma_f32 v[226:227], v[228:229], v[190:191], v[226:227]
	v_cvt_pk_f32_fp8_e32 v[228:229], v88
	v_pk_fma_f32 v[224:225], v[238:239], v[196:197], v[224:225]
	v_cvt_pk_f32_fp8_e32 v[238:239], v87
	v_pk_fma_f32 v[226:227], v[230:231], v[194:195], v[226:227]
	v_cvt_pk_f32_fp8_sdwa v[230:231], v88 src0_sel:WORD_1
	v_cvt_pk_f32_fp8_sdwa v[240:241], v87 src0_sel:WORD_1
	v_lshl_or_b32 v11, v11, 7, v209
	global_load_dwordx4 v[84:87], v11, s[6:7]
	v_pk_fma_f32 v[226:227], v[232:233], v[198:199], v[226:227]
	v_cvt_pk_f32_fp8_e32 v[232:233], v89
	v_pk_fma_f32 v[226:227], v[234:235], v[184:185], v[226:227]
	v_cvt_pk_f32_fp8_sdwa v[234:235], v89 src0_sel:WORD_1
	v_pk_fma_f32 v[226:227], v[236:237], v[188:189], v[226:227]
	v_cvt_pk_f32_fp8_e32 v[236:237], v90
	v_pk_mul_f32 v[228:229], v[228:229], v[186:187]
	v_pk_fma_f32 v[226:227], v[238:239], v[192:193], v[226:227]
	v_cvt_pk_f32_fp8_sdwa v[238:239], v90 src0_sel:WORD_1
	v_pk_fma_f32 v[228:229], v[230:231], v[190:191], v[228:229]
	v_cvt_pk_f32_fp8_e32 v[230:231], v92
	v_pk_fma_f32 v[226:227], v[240:241], v[196:197], v[226:227]
	v_cvt_pk_f32_fp8_e32 v[240:241], v91
	v_pk_fma_f32 v[228:229], v[232:233], v[194:195], v[228:229]
	v_cvt_pk_f32_fp8_sdwa v[232:233], v92 src0_sel:WORD_1
	v_cvt_pk_f32_fp8_sdwa v[242:243], v91 src0_sel:WORD_1
	v_lshl_or_b32 v12, v12, 7, v209
	global_load_dwordx4 v[88:91], v12, s[6:7]
	v_pk_fma_f32 v[228:229], v[234:235], v[198:199], v[228:229]
	v_cvt_pk_f32_fp8_e32 v[234:235], v93
	v_pk_fma_f32 v[228:229], v[236:237], v[184:185], v[228:229]
	v_cvt_pk_f32_fp8_sdwa v[236:237], v93 src0_sel:WORD_1
	v_pk_fma_f32 v[228:229], v[238:239], v[188:189], v[228:229]
	v_cvt_pk_f32_fp8_e32 v[238:239], v94
	v_pk_mul_f32 v[230:231], v[230:231], v[186:187]
	v_pk_fma_f32 v[228:229], v[240:241], v[192:193], v[228:229]
	v_cvt_pk_f32_fp8_sdwa v[240:241], v94 src0_sel:WORD_1
	v_pk_fma_f32 v[230:231], v[232:233], v[190:191], v[230:231]
	v_cvt_pk_f32_fp8_e32 v[232:233], v96
	v_pk_fma_f32 v[228:229], v[242:243], v[196:197], v[228:229]
	v_cvt_pk_f32_fp8_e32 v[242:243], v95
	v_pk_fma_f32 v[230:231], v[234:235], v[194:195], v[230:231]
	v_cvt_pk_f32_fp8_sdwa v[234:235], v96 src0_sel:WORD_1
	v_cvt_pk_f32_fp8_sdwa v[244:245], v95 src0_sel:WORD_1
	v_lshl_or_b32 v13, v13, 7, v209
	global_load_dwordx4 v[92:95], v13, s[6:7]
	v_pk_fma_f32 v[230:231], v[236:237], v[198:199], v[230:231]
	v_cvt_pk_f32_fp8_e32 v[236:237], v97
	v_pk_fma_f32 v[230:231], v[238:239], v[184:185], v[230:231]
	v_cvt_pk_f32_fp8_sdwa v[238:239], v97 src0_sel:WORD_1
	v_pk_fma_f32 v[230:231], v[240:241], v[188:189], v[230:231]
	v_cvt_pk_f32_fp8_e32 v[240:241], v98
	v_pk_mul_f32 v[232:233], v[232:233], v[186:187]
	v_pk_fma_f32 v[230:231], v[242:243], v[192:193], v[230:231]
	v_cvt_pk_f32_fp8_sdwa v[242:243], v98 src0_sel:WORD_1
	v_pk_fma_f32 v[232:233], v[234:235], v[190:191], v[232:233]
	v_cvt_pk_f32_fp8_e32 v[234:235], v104
	v_pk_fma_f32 v[230:231], v[244:245], v[196:197], v[230:231]
	v_cvt_pk_f32_fp8_e32 v[244:245], v99
	v_pk_fma_f32 v[232:233], v[236:237], v[194:195], v[232:233]
	v_cvt_pk_f32_fp8_sdwa v[236:237], v104 src0_sel:WORD_1
	v_cvt_pk_f32_fp8_sdwa v[246:247], v99 src0_sel:WORD_1
	v_lshl_or_b32 v14, v14, 7, v209
	global_load_dwordx4 v[96:99], v14, s[6:7]
	v_pk_fma_f32 v[232:233], v[238:239], v[198:199], v[232:233]
	v_cvt_pk_f32_fp8_e32 v[238:239], v105
	v_pk_fma_f32 v[232:233], v[240:241], v[184:185], v[232:233]
	v_cvt_pk_f32_fp8_sdwa v[240:241], v105 src0_sel:WORD_1
	v_pk_fma_f32 v[232:233], v[242:243], v[188:189], v[232:233]
	v_cvt_pk_f32_fp8_e32 v[242:243], v106
	v_pk_mul_f32 v[186:187], v[234:235], v[186:187]
	v_pk_fma_f32 v[232:233], v[244:245], v[192:193], v[232:233]
	v_cvt_pk_f32_fp8_sdwa v[244:245], v106 src0_sel:WORD_1
	v_pk_fma_f32 v[186:187], v[236:237], v[190:191], v[186:187]
	v_pk_fma_f32 v[232:233], v[246:247], v[196:197], v[232:233]
	v_cvt_pk_f32_fp8_e32 v[246:247], v107
	v_pk_fma_f32 v[186:187], v[238:239], v[194:195], v[186:187]
	v_cvt_pk_f32_fp8_sdwa v[248:249], v107 src0_sel:WORD_1
	v_lshl_or_b32 v15, v15, 7, v209
	global_load_dwordx4 v[104:107], v15, s[6:7]
	v_pk_fma_f32 v[186:187], v[240:241], v[198:199], v[186:187]
	v_mov_b32_e32 v194, v220
	v_pk_fma_f32 v[184:185], v[242:243], v[184:185], v[186:187]
	v_mov_b32_e32 v186, v200
	v_pk_fma_f32 v[184:185], v[244:245], v[188:189], v[184:185]
	v_mov_b32_e32 v187, v202
	v_pk_fma_f32 v[184:185], v[246:247], v[192:193], v[184:185]
	v_mov_b32_e32 v202, v201
	v_pk_fma_f32 v[184:185], v[248:249], v[196:197], v[184:185]
	v_mov_b32_e32 v195, v222
	v_mov_b32_e32 v222, v221
	v_pk_add_f32 v[186:187], v[186:187], v[202:203]
	v_pk_add_f32 v[194:195], v[194:195], v[222:223]
	v_mov_b32_e32 v200, v232
	v_mov_b32_e32 v201, v184
	v_mov_b32_e32 v184, v233
	v_mov_b32_e32 v188, v204
	v_mov_b32_e32 v189, v210
	v_mov_b32_e32 v210, v205
	v_mov_b32_e32 v196, v224
	v_mov_b32_e32 v197, v226
	v_mov_b32_e32 v226, v225
	v_pk_add_f32 v[184:185], v[200:201], v[184:185]
	v_cndmask_b32_e64 v200, v186, v194, s[4:5]
	v_cndmask_b32_e64 v202, v194, v186, s[4:5]
	v_cndmask_b32_e64 v186, v187, v195, s[4:5]
	v_pk_add_f32 v[188:189], v[188:189], v[210:211]
	v_pk_add_f32 v[196:197], v[196:197], v[226:227]
	v_mov_b32_dpp v200, v200 row_half_mirror row_mask:0xf bank_mask:0xf bound_ctrl:1
	v_cndmask_b32_e64 v203, v195, v187, s[4:5]
	v_mov_b32_dpp v201, v186 row_half_mirror row_mask:0xf bank_mask:0xf bound_ctrl:1
	v_mov_b32_e32 v190, v212
	v_mov_b32_e32 v191, v214
	v_mov_b32_e32 v214, v213
	v_mov_b32_e32 v198, v228
	v_mov_b32_e32 v199, v230
	v_mov_b32_e32 v230, v229
	v_pk_add_f32 v[186:187], v[202:203], v[200:201]
	v_cndmask_b32_e64 v194, v188, v196, s[4:5]
	v_cndmask_b32_e64 v200, v196, v188, s[4:5]
	v_cndmask_b32_e64 v188, v189, v197, s[4:5]
	v_pk_add_f32 v[190:191], v[190:191], v[214:215]
	v_pk_add_f32 v[198:199], v[198:199], v[230:231]
	v_mov_b32_dpp v194, v194 row_half_mirror row_mask:0xf bank_mask:0xf bound_ctrl:1
	v_cndmask_b32_e64 v201, v197, v189, s[4:5]
	v_mov_b32_dpp v195, v188 row_half_mirror row_mask:0xf bank_mask:0xf bound_ctrl:1
	v_mov_b32_e32 v192, v216
	v_mov_b32_e32 v193, v218
	v_mov_b32_e32 v218, v217
	v_pk_add_f32 v[188:189], v[200:201], v[194:195]
	v_cndmask_b32_e64 v194, v190, v198, s[4:5]
	v_cndmask_b32_e64 v196, v198, v190, s[4:5]
	v_cndmask_b32_e64 v190, v191, v199, s[4:5]
	v_pk_add_f32 v[192:193], v[192:193], v[218:219]
	v_mov_b32_dpp v194, v194 row_half_mirror row_mask:0xf bank_mask:0xf bound_ctrl:1
	v_cndmask_b32_e64 v197, v199, v191, s[4:5]
	v_mov_b32_dpp v195, v190 row_half_mirror row_mask:0xf bank_mask:0xf bound_ctrl:1
	v_pk_add_f32 v[190:191], v[196:197], v[194:195]
	v_cndmask_b32_e64 v194, v192, v184, s[4:5]
	v_cndmask_b32_e64 v196, v184, v192, s[4:5]
	v_cndmask_b32_e64 v184, v193, v185, s[4:5]
	v_mov_b32_dpp v194, v194 row_half_mirror row_mask:0xf bank_mask:0xf bound_ctrl:1
	v_cndmask_b32_e64 v197, v185, v193, s[4:5]
	v_mov_b32_dpp v195, v184 row_half_mirror row_mask:0xf bank_mask:0xf bound_ctrl:1
	v_pk_add_f32 v[184:185], v[196:197], v[194:195]
	v_cndmask_b32_e64 v192, v186, v190, s[2:3]
	v_cndmask_b32_e64 v194, v190, v186, s[2:3]
	v_cndmask_b32_e64 v186, v187, v191, s[2:3]
	v_mov_b32_dpp v192, v192 quad_perm:[2,3,0,1] row_mask:0xf bank_mask:0xf bound_ctrl:1
	v_cndmask_b32_e64 v195, v191, v187, s[2:3]
	v_mov_b32_dpp v193, v186 quad_perm:[2,3,0,1] row_mask:0xf bank_mask:0xf bound_ctrl:1
	v_pk_add_f32 v[186:187], v[194:195], v[192:193]
	v_cndmask_b32_e64 v190, v188, v184, s[2:3]
	v_cndmask_b32_e64 v192, v184, v188, s[2:3]
	v_cndmask_b32_e64 v184, v189, v185, s[2:3]
	v_mov_b32_dpp v190, v190 quad_perm:[2,3,0,1] row_mask:0xf bank_mask:0xf bound_ctrl:1
	v_cndmask_b32_e64 v193, v185, v189, s[2:3]
	v_mov_b32_dpp v191, v184 quad_perm:[2,3,0,1] row_mask:0xf bank_mask:0xf bound_ctrl:1
	v_pk_add_f32 v[184:185], v[192:193], v[190:191]
	s_ashr_i32 s15, s14, 31
	v_cndmask_b32_e64 v188, v186, v184, s[0:1]
	v_cndmask_b32_e64 v190, v184, v186, s[0:1]
	v_cndmask_b32_e64 v184, v187, v185, s[0:1]
	v_mov_b32_dpp v188, v188 quad_perm:[1,0,3,2] row_mask:0xf bank_mask:0xf bound_ctrl:1
	v_cndmask_b32_e64 v191, v185, v187, s[0:1]
	v_mov_b32_dpp v189, v184 quad_perm:[1,0,3,2] row_mask:0xf bank_mask:0xf bound_ctrl:1
	v_pk_add_f32 v[184:185], v[190:191], v[188:189]
	s_lshl_b64 s[14:15], s[14:15], 8
	v_cvt_pk_bf16_f32 v186, v184, v185
	v_lshl_add_u64 v[184:185], v[178:179], 0, s[14:15]
	global_store_dword v[184:185], v186, off
	s_add_u32 s20, s12, 0x200
	s_lshl_b32 s20, s20, 11
	v_lshl_add_u64 v[20:21], v[182:183], 0, s[20:21]
	global_load_dwordx4 v[16:19], v[20:21], off offset:16
	s_nop 0
	global_load_dwordx4 v[20:23], v[20:21], off
	s_add_u32 s10, s12, 0x100
	s_waitcnt vmcnt(19)
	v_cvt_pk_f32_fp8_e32 v[200:201], v112
	v_cvt_pk_f32_fp8_sdwa v[202:203], v112 src0_sel:WORD_1
	v_cvt_pk_f32_fp8_e32 v[204:205], v113
	v_lshlrev_b32_e32 v186, 16, v108
	v_and_b32_e32 v187, 0xffff0000, v108
	v_cvt_pk_f32_fp8_sdwa v[210:211], v113 src0_sel:WORD_1
	v_lshlrev_b32_e32 v190, 16, v109
	v_and_b32_e32 v191, 0xffff0000, v109
	v_cvt_pk_f32_fp8_e32 v[212:213], v114
	v_pk_mul_f32 v[200:201], v[200:201], v[186:187]
	v_lshlrev_b32_e32 v194, 16, v110
	v_and_b32_e32 v195, 0xffff0000, v110
	v_cvt_pk_f32_fp8_sdwa v[214:215], v114 src0_sel:WORD_1
	v_pk_fma_f32 v[200:201], v[202:203], v[190:191], v[200:201]
	v_cvt_pk_f32_fp8_e32 v[202:203], v116
	v_lshlrev_b32_e32 v198, 16, v111
	v_and_b32_e32 v199, 0xffff0000, v111
	v_cvt_pk_f32_fp8_e32 v[216:217], v115
	v_pk_fma_f32 v[200:201], v[204:205], v[194:195], v[200:201]
	v_cvt_pk_f32_fp8_sdwa v[204:205], v116 src0_sel:WORD_1
	v_lshlrev_b32_e32 v184, 16, v100
	v_and_b32_e32 v185, 0xffff0000, v100
	v_cvt_pk_f32_fp8_sdwa v[218:219], v115 src0_sel:WORD_1
	v_lshl_or_b32 v80, v80, 7, v209
	global_load_dwordx4 v[112:115], v80, s[6:7]
	v_pk_fma_f32 v[200:201], v[210:211], v[198:199], v[200:201]
	v_cvt_pk_f32_fp8_e32 v[210:211], v117
	v_lshlrev_b32_e32 v188, 16, v101
	v_and_b32_e32 v189, 0xffff0000, v101
	v_pk_fma_f32 v[200:201], v[212:213], v[184:185], v[200:201]
	v_cvt_pk_f32_fp8_sdwa v[212:213], v117 src0_sel:WORD_1
	v_lshlrev_b32_e32 v192, 16, v102
	v_and_b32_e32 v193, 0xffff0000, v102
	v_pk_fma_f32 v[200:201], v[214:215], v[188:189], v[200:201]
	v_cvt_pk_f32_fp8_e32 v[214:215], v118
	v_pk_mul_f32 v[202:203], v[202:203], v[186:187]
	v_lshlrev_b32_e32 v196, 16, v103
	v_and_b32_e32 v197, 0xffff0000, v103
	v_pk_fma_f32 v[200:201], v[216:217], v[192:193], v[200:201]
	v_cvt_pk_f32_fp8_sdwa v[216:217], v118 src0_sel:WORD_1
	v_pk_fma_f32 v[202:203], v[204:205], v[190:191], v[202:203]
	v_cvt_pk_f32_fp8_e32 v[204:205], v120
	v_pk_fma_f32 v[200:201], v[218:219], v[196:197], v[200:201]
	v_cvt_pk_f32_fp8_e32 v[218:219], v119
	v_pk_fma_f32 v[202:203], v[210:211], v[194:195], v[202:203]
	v_cvt_pk_f32_fp8_sdwa v[210:211], v120 src0_sel:WORD_1
	v_cvt_pk_f32_fp8_sdwa v[220:221], v119 src0_sel:WORD_1
	v_lshl_or_b32 v81, v81, 7, v209
	global_load_dwordx4 v[116:119], v81, s[6:7]
	v_pk_fma_f32 v[202:203], v[212:213], v[198:199], v[202:203]
	v_cvt_pk_f32_fp8_e32 v[212:213], v121
	v_pk_fma_f32 v[202:203], v[214:215], v[184:185], v[202:203]
	v_cvt_pk_f32_fp8_sdwa v[214:215], v121 src0_sel:WORD_1
	v_pk_fma_f32 v[202:203], v[216:217], v[188:189], v[202:203]
	v_cvt_pk_f32_fp8_e32 v[216:217], v122
	v_pk_mul_f32 v[204:205], v[204:205], v[186:187]
	v_pk_fma_f32 v[202:203], v[218:219], v[192:193], v[202:203]
	v_cvt_pk_f32_fp8_sdwa v[218:219], v122 src0_sel:WORD_1
	v_pk_fma_f32 v[204:205], v[210:211], v[190:191], v[204:205]
	v_cvt_pk_f32_fp8_e32 v[210:211], v124
	v_pk_fma_f32 v[202:203], v[220:221], v[196:197], v[202:203]
	v_cvt_pk_f32_fp8_e32 v[220:221], v123
	v_pk_fma_f32 v[204:205], v[212:213], v[194:195], v[204:205]
	v_cvt_pk_f32_fp8_sdwa v[212:213], v124 src0_sel:WORD_1
	v_cvt_pk_f32_fp8_sdwa v[222:223], v123 src0_sel:WORD_1
	v_lshl_or_b32 v82, v82, 7, v209
	global_load_dwordx4 v[120:123], v82, s[6:7]
	v_pk_fma_f32 v[204:205], v[214:215], v[198:199], v[204:205]
	v_cvt_pk_f32_fp8_e32 v[214:215], v125
	v_pk_fma_f32 v[204:205], v[216:217], v[184:185], v[204:205]
	v_cvt_pk_f32_fp8_sdwa v[216:217], v125 src0_sel:WORD_1
	v_pk_fma_f32 v[204:205], v[218:219], v[188:189], v[204:205]
	v_cvt_pk_f32_fp8_e32 v[218:219], v126
	v_pk_mul_f32 v[210:211], v[210:211], v[186:187]
	v_pk_fma_f32 v[204:205], v[220:221], v[192:193], v[204:205]
	v_cvt_pk_f32_fp8_sdwa v[220:221], v126 src0_sel:WORD_1
	v_pk_fma_f32 v[210:211], v[212:213], v[190:191], v[210:211]
	v_cvt_pk_f32_fp8_e32 v[212:213], v128
	v_pk_fma_f32 v[204:205], v[222:223], v[196:197], v[204:205]
	v_cvt_pk_f32_fp8_e32 v[222:223], v127
	v_pk_fma_f32 v[210:211], v[214:215], v[194:195], v[210:211]
	v_cvt_pk_f32_fp8_sdwa v[214:215], v128 src0_sel:WORD_1
	v_cvt_pk_f32_fp8_sdwa v[224:225], v127 src0_sel:WORD_1
	v_lshl_or_b32 v83, v83, 7, v209
	global_load_dwordx4 v[124:127], v83, s[6:7]
	v_pk_fma_f32 v[210:211], v[216:217], v[198:199], v[210:211]
	v_cvt_pk_f32_fp8_e32 v[216:217], v129
	v_pk_fma_f32 v[210:211], v[218:219], v[184:185], v[210:211]
	v_cvt_pk_f32_fp8_sdwa v[218:219], v129 src0_sel:WORD_1
	v_pk_fma_f32 v[210:211], v[220:221], v[188:189], v[210:211]
	v_cvt_pk_f32_fp8_e32 v[220:221], v130
	v_pk_mul_f32 v[212:213], v[212:213], v[186:187]
	v_pk_fma_f32 v[210:211], v[222:223], v[192:193], v[210:211]
	v_cvt_pk_f32_fp8_sdwa v[222:223], v130 src0_sel:WORD_1
	v_pk_fma_f32 v[212:213], v[214:215], v[190:191], v[212:213]
	v_cvt_pk_f32_fp8_e32 v[214:215], v132
	v_pk_fma_f32 v[210:211], v[224:225], v[196:197], v[210:211]
	v_cvt_pk_f32_fp8_e32 v[224:225], v131
	v_pk_fma_f32 v[212:213], v[216:217], v[194:195], v[212:213]
	v_cvt_pk_f32_fp8_sdwa v[216:217], v132 src0_sel:WORD_1
	v_cvt_pk_f32_fp8_sdwa v[226:227], v131 src0_sel:WORD_1
	v_lshl_or_b32 v72, v72, 7, v209
	global_load_dwordx4 v[128:131], v72, s[6:7]
	v_pk_fma_f32 v[212:213], v[218:219], v[198:199], v[212:213]
	v_cvt_pk_f32_fp8_e32 v[218:219], v133
	v_pk_fma_f32 v[212:213], v[220:221], v[184:185], v[212:213]
	v_cvt_pk_f32_fp8_sdwa v[220:221], v133 src0_sel:WORD_1
	v_pk_fma_f32 v[212:213], v[222:223], v[188:189], v[212:213]
	v_cvt_pk_f32_fp8_e32 v[222:223], v134
	v_pk_mul_f32 v[214:215], v[214:215], v[186:187]
	v_pk_fma_f32 v[212:213], v[224:225], v[192:193], v[212:213]
	v_cvt_pk_f32_fp8_sdwa v[224:225], v134 src0_sel:WORD_1
	v_pk_fma_f32 v[214:215], v[216:217], v[190:191], v[214:215]
	v_cvt_pk_f32_fp8_e32 v[216:217], v136
	v_pk_fma_f32 v[212:213], v[226:227], v[196:197], v[212:213]
	v_cvt_pk_f32_fp8_e32 v[226:227], v135
	v_pk_fma_f32 v[214:215], v[218:219], v[194:195], v[214:215]
	v_cvt_pk_f32_fp8_sdwa v[218:219], v136 src0_sel:WORD_1
	v_cvt_pk_f32_fp8_sdwa v[228:229], v135 src0_sel:WORD_1
	v_lshl_or_b32 v73, v73, 7, v209
	global_load_dwordx4 v[132:135], v73, s[6:7]
	v_pk_fma_f32 v[214:215], v[220:221], v[198:199], v[214:215]
	v_cvt_pk_f32_fp8_e32 v[220:221], v137
	v_pk_fma_f32 v[214:215], v[222:223], v[184:185], v[214:215]
	v_cvt_pk_f32_fp8_sdwa v[222:223], v137 src0_sel:WORD_1
	v_pk_fma_f32 v[214:215], v[224:225], v[188:189], v[214:215]
	v_cvt_pk_f32_fp8_e32 v[224:225], v138
	v_pk_mul_f32 v[216:217], v[216:217], v[186:187]
	v_pk_fma_f32 v[214:215], v[226:227], v[192:193], v[214:215]
	v_cvt_pk_f32_fp8_sdwa v[226:227], v138 src0_sel:WORD_1
	v_pk_fma_f32 v[216:217], v[218:219], v[190:191], v[216:217]
	v_cvt_pk_f32_fp8_e32 v[218:219], v140
	v_pk_fma_f32 v[214:215], v[228:229], v[196:197], v[214:215]
	v_cvt_pk_f32_fp8_e32 v[228:229], v139
	v_pk_fma_f32 v[216:217], v[220:221], v[194:195], v[216:217]
	v_cvt_pk_f32_fp8_sdwa v[220:221], v140 src0_sel:WORD_1
	v_cvt_pk_f32_fp8_sdwa v[230:231], v139 src0_sel:WORD_1
	v_lshl_or_b32 v74, v74, 7, v209
	global_load_dwordx4 v[136:139], v74, s[6:7]
	v_pk_fma_f32 v[216:217], v[222:223], v[198:199], v[216:217]
	v_cvt_pk_f32_fp8_e32 v[222:223], v141
	v_pk_fma_f32 v[216:217], v[224:225], v[184:185], v[216:217]
	v_cvt_pk_f32_fp8_sdwa v[224:225], v141 src0_sel:WORD_1
	v_pk_fma_f32 v[216:217], v[226:227], v[188:189], v[216:217]
	v_cvt_pk_f32_fp8_e32 v[226:227], v142
	v_pk_mul_f32 v[218:219], v[218:219], v[186:187]
	v_pk_fma_f32 v[216:217], v[228:229], v[192:193], v[216:217]
	v_cvt_pk_f32_fp8_sdwa v[228:229], v142 src0_sel:WORD_1
	v_pk_fma_f32 v[218:219], v[220:221], v[190:191], v[218:219]
	v_cvt_pk_f32_fp8_e32 v[220:221], v144
	v_pk_fma_f32 v[216:217], v[230:231], v[196:197], v[216:217]
	v_cvt_pk_f32_fp8_e32 v[230:231], v143
	v_pk_fma_f32 v[218:219], v[222:223], v[194:195], v[218:219]
	v_cvt_pk_f32_fp8_sdwa v[222:223], v144 src0_sel:WORD_1
	v_cvt_pk_f32_fp8_sdwa v[232:233], v143 src0_sel:WORD_1
	v_lshl_or_b32 v75, v75, 7, v209
	global_load_dwordx4 v[140:143], v75, s[6:7]
	v_pk_fma_f32 v[218:219], v[224:225], v[198:199], v[218:219]
	v_cvt_pk_f32_fp8_e32 v[224:225], v145
	v_pk_fma_f32 v[218:219], v[226:227], v[184:185], v[218:219]
	v_cvt_pk_f32_fp8_sdwa v[226:227], v145 src0_sel:WORD_1
	v_pk_fma_f32 v[218:219], v[228:229], v[188:189], v[218:219]
	v_cvt_pk_f32_fp8_e32 v[228:229], v146
	v_pk_mul_f32 v[220:221], v[220:221], v[186:187]
	v_pk_fma_f32 v[218:219], v[230:231], v[192:193], v[218:219]
	v_cvt_pk_f32_fp8_sdwa v[230:231], v146 src0_sel:WORD_1
	v_pk_fma_f32 v[220:221], v[222:223], v[190:191], v[220:221]
	v_cvt_pk_f32_fp8_e32 v[222:223], v148
	v_pk_fma_f32 v[218:219], v[232:233], v[196:197], v[218:219]
	v_cvt_pk_f32_fp8_e32 v[232:233], v147
	v_pk_fma_f32 v[220:221], v[224:225], v[194:195], v[220:221]
	v_cvt_pk_f32_fp8_sdwa v[224:225], v148 src0_sel:WORD_1
	v_cvt_pk_f32_fp8_sdwa v[234:235], v147 src0_sel:WORD_1
	v_lshl_or_b32 v68, v68, 7, v209
	global_load_dwordx4 v[144:147], v68, s[6:7]
	v_pk_fma_f32 v[220:221], v[226:227], v[198:199], v[220:221]
	v_cvt_pk_f32_fp8_e32 v[226:227], v149
	v_pk_fma_f32 v[220:221], v[228:229], v[184:185], v[220:221]
	v_cvt_pk_f32_fp8_sdwa v[228:229], v149 src0_sel:WORD_1
	v_pk_fma_f32 v[220:221], v[230:231], v[188:189], v[220:221]
	v_cvt_pk_f32_fp8_e32 v[230:231], v150
	v_pk_mul_f32 v[222:223], v[222:223], v[186:187]
	v_pk_fma_f32 v[220:221], v[232:233], v[192:193], v[220:221]
	v_cvt_pk_f32_fp8_sdwa v[232:233], v150 src0_sel:WORD_1
	v_pk_fma_f32 v[222:223], v[224:225], v[190:191], v[222:223]
	v_cvt_pk_f32_fp8_e32 v[224:225], v152
	v_pk_fma_f32 v[220:221], v[234:235], v[196:197], v[220:221]
	v_cvt_pk_f32_fp8_e32 v[234:235], v151
	v_pk_fma_f32 v[222:223], v[226:227], v[194:195], v[222:223]
	v_cvt_pk_f32_fp8_sdwa v[226:227], v152 src0_sel:WORD_1
	v_cvt_pk_f32_fp8_sdwa v[236:237], v151 src0_sel:WORD_1
	v_lshl_or_b32 v69, v69, 7, v209
	global_load_dwordx4 v[148:151], v69, s[6:7]
	v_pk_fma_f32 v[222:223], v[228:229], v[198:199], v[222:223]
	v_cvt_pk_f32_fp8_e32 v[228:229], v153
	v_pk_fma_f32 v[222:223], v[230:231], v[184:185], v[222:223]
	v_cvt_pk_f32_fp8_sdwa v[230:231], v153 src0_sel:WORD_1
	v_pk_fma_f32 v[222:223], v[232:233], v[188:189], v[222:223]
	v_cvt_pk_f32_fp8_e32 v[232:233], v154
	v_pk_mul_f32 v[224:225], v[224:225], v[186:187]
	v_pk_fma_f32 v[222:223], v[234:235], v[192:193], v[222:223]
	v_cvt_pk_f32_fp8_sdwa v[234:235], v154 src0_sel:WORD_1
	v_pk_fma_f32 v[224:225], v[226:227], v[190:191], v[224:225]
	v_cvt_pk_f32_fp8_e32 v[226:227], v156
	v_pk_fma_f32 v[222:223], v[236:237], v[196:197], v[222:223]
	v_cvt_pk_f32_fp8_e32 v[236:237], v155
	v_pk_fma_f32 v[224:225], v[228:229], v[194:195], v[224:225]
	v_cvt_pk_f32_fp8_sdwa v[228:229], v156 src0_sel:WORD_1
	v_cvt_pk_f32_fp8_sdwa v[238:239], v155 src0_sel:WORD_1
	v_lshl_or_b32 v70, v70, 7, v209
	global_load_dwordx4 v[152:155], v70, s[6:7]
	v_pk_fma_f32 v[224:225], v[230:231], v[198:199], v[224:225]
	v_cvt_pk_f32_fp8_e32 v[230:231], v157
	v_pk_fma_f32 v[224:225], v[232:233], v[184:185], v[224:225]
	v_cvt_pk_f32_fp8_sdwa v[232:233], v157 src0_sel:WORD_1
	v_pk_fma_f32 v[224:225], v[234:235], v[188:189], v[224:225]
	v_cvt_pk_f32_fp8_e32 v[234:235], v158
	v_pk_mul_f32 v[226:227], v[226:227], v[186:187]
	v_pk_fma_f32 v[224:225], v[236:237], v[192:193], v[224:225]
	v_cvt_pk_f32_fp8_sdwa v[236:237], v158 src0_sel:WORD_1
	v_pk_fma_f32 v[226:227], v[228:229], v[190:191], v[226:227]
	v_cvt_pk_f32_fp8_e32 v[228:229], v160
	v_pk_fma_f32 v[224:225], v[238:239], v[196:197], v[224:225]
	v_cvt_pk_f32_fp8_e32 v[238:239], v159
	v_pk_fma_f32 v[226:227], v[230:231], v[194:195], v[226:227]
	v_cvt_pk_f32_fp8_sdwa v[230:231], v160 src0_sel:WORD_1
	v_cvt_pk_f32_fp8_sdwa v[240:241], v159 src0_sel:WORD_1
	v_lshl_or_b32 v71, v71, 7, v209
	global_load_dwordx4 v[156:159], v71, s[6:7]
	v_pk_fma_f32 v[226:227], v[232:233], v[198:199], v[226:227]
	v_cvt_pk_f32_fp8_e32 v[232:233], v161
	v_pk_fma_f32 v[226:227], v[234:235], v[184:185], v[226:227]
	v_cvt_pk_f32_fp8_sdwa v[234:235], v161 src0_sel:WORD_1
	v_pk_fma_f32 v[226:227], v[236:237], v[188:189], v[226:227]
	v_cvt_pk_f32_fp8_e32 v[236:237], v162
	v_pk_mul_f32 v[228:229], v[228:229], v[186:187]
	v_pk_fma_f32 v[226:227], v[238:239], v[192:193], v[226:227]
	v_cvt_pk_f32_fp8_sdwa v[238:239], v162 src0_sel:WORD_1
	v_pk_fma_f32 v[228:229], v[230:231], v[190:191], v[228:229]
	v_cvt_pk_f32_fp8_e32 v[230:231], v164
	v_pk_fma_f32 v[226:227], v[240:241], v[196:197], v[226:227]
	v_cvt_pk_f32_fp8_e32 v[240:241], v163
	v_pk_fma_f32 v[228:229], v[232:233], v[194:195], v[228:229]
	v_cvt_pk_f32_fp8_sdwa v[232:233], v164 src0_sel:WORD_1
	v_cvt_pk_f32_fp8_sdwa v[242:243], v163 src0_sel:WORD_1
	v_lshl_or_b32 v64, v64, 7, v209
	global_load_dwordx4 v[160:163], v64, s[6:7]
	v_pk_fma_f32 v[228:229], v[234:235], v[198:199], v[228:229]
	v_cvt_pk_f32_fp8_e32 v[234:235], v165
	v_pk_fma_f32 v[228:229], v[236:237], v[184:185], v[228:229]
	v_cvt_pk_f32_fp8_sdwa v[236:237], v165 src0_sel:WORD_1
	v_pk_fma_f32 v[228:229], v[238:239], v[188:189], v[228:229]
	v_cvt_pk_f32_fp8_e32 v[238:239], v166
	v_pk_mul_f32 v[230:231], v[230:231], v[186:187]
	v_pk_fma_f32 v[228:229], v[240:241], v[192:193], v[228:229]
	v_cvt_pk_f32_fp8_sdwa v[240:241], v166 src0_sel:WORD_1
	v_pk_fma_f32 v[230:231], v[232:233], v[190:191], v[230:231]
	v_cvt_pk_f32_fp8_e32 v[232:233], v168
	v_pk_fma_f32 v[228:229], v[242:243], v[196:197], v[228:229]
	v_cvt_pk_f32_fp8_e32 v[242:243], v167
	v_pk_fma_f32 v[230:231], v[234:235], v[194:195], v[230:231]
	v_cvt_pk_f32_fp8_sdwa v[234:235], v168 src0_sel:WORD_1
	v_cvt_pk_f32_fp8_sdwa v[244:245], v167 src0_sel:WORD_1
	v_lshl_or_b32 v65, v65, 7, v209
	global_load_dwordx4 v[164:167], v65, s[6:7]
	v_pk_fma_f32 v[230:231], v[236:237], v[198:199], v[230:231]
	v_cvt_pk_f32_fp8_e32 v[236:237], v169
	v_pk_fma_f32 v[230:231], v[238:239], v[184:185], v[230:231]
	v_cvt_pk_f32_fp8_sdwa v[238:239], v169 src0_sel:WORD_1
	v_pk_fma_f32 v[230:231], v[240:241], v[188:189], v[230:231]
	v_cvt_pk_f32_fp8_e32 v[240:241], v170
	v_pk_mul_f32 v[232:233], v[232:233], v[186:187]
	v_pk_fma_f32 v[230:231], v[242:243], v[192:193], v[230:231]
	v_cvt_pk_f32_fp8_sdwa v[242:243], v170 src0_sel:WORD_1
	v_pk_fma_f32 v[232:233], v[234:235], v[190:191], v[232:233]
	v_cvt_pk_f32_fp8_e32 v[234:235], v172
	v_pk_fma_f32 v[230:231], v[244:245], v[196:197], v[230:231]
	v_cvt_pk_f32_fp8_e32 v[244:245], v171
	v_pk_fma_f32 v[232:233], v[236:237], v[194:195], v[232:233]
	v_cvt_pk_f32_fp8_sdwa v[236:237], v172 src0_sel:WORD_1
	v_cvt_pk_f32_fp8_sdwa v[246:247], v171 src0_sel:WORD_1
	v_lshl_or_b32 v66, v66, 7, v209
	global_load_dwordx4 v[168:171], v66, s[6:7]
	v_pk_fma_f32 v[232:233], v[238:239], v[198:199], v[232:233]
	v_cvt_pk_f32_fp8_e32 v[238:239], v173
	v_pk_fma_f32 v[232:233], v[240:241], v[184:185], v[232:233]
	v_cvt_pk_f32_fp8_sdwa v[240:241], v173 src0_sel:WORD_1
	v_pk_fma_f32 v[232:233], v[242:243], v[188:189], v[232:233]
	v_cvt_pk_f32_fp8_e32 v[242:243], v174
	v_pk_mul_f32 v[186:187], v[234:235], v[186:187]
	v_pk_fma_f32 v[232:233], v[244:245], v[192:193], v[232:233]
	v_cvt_pk_f32_fp8_sdwa v[244:245], v174 src0_sel:WORD_1
	v_pk_fma_f32 v[186:187], v[236:237], v[190:191], v[186:187]
	v_pk_fma_f32 v[232:233], v[246:247], v[196:197], v[232:233]
	v_cvt_pk_f32_fp8_e32 v[246:247], v175
	v_pk_fma_f32 v[186:187], v[238:239], v[194:195], v[186:187]
	v_cvt_pk_f32_fp8_sdwa v[248:249], v175 src0_sel:WORD_1
	v_lshl_or_b32 v67, v67, 7, v209
	global_load_dwordx4 v[172:175], v67, s[6:7]
	v_pk_fma_f32 v[186:187], v[240:241], v[198:199], v[186:187]
	v_mov_b32_e32 v194, v220
	v_pk_fma_f32 v[184:185], v[242:243], v[184:185], v[186:187]
	v_mov_b32_e32 v186, v200
	v_pk_fma_f32 v[184:185], v[244:245], v[188:189], v[184:185]
	v_mov_b32_e32 v187, v202
	v_pk_fma_f32 v[184:185], v[246:247], v[192:193], v[184:185]
	v_mov_b32_e32 v202, v201
	v_pk_fma_f32 v[184:185], v[248:249], v[196:197], v[184:185]
	v_mov_b32_e32 v195, v222
	v_mov_b32_e32 v222, v221
	v_pk_add_f32 v[186:187], v[186:187], v[202:203]
	v_pk_add_f32 v[194:195], v[194:195], v[222:223]
	v_mov_b32_e32 v200, v232
	v_mov_b32_e32 v201, v184
	v_mov_b32_e32 v184, v233
	v_mov_b32_e32 v188, v204
	v_mov_b32_e32 v189, v210
	v_mov_b32_e32 v210, v205
	v_mov_b32_e32 v196, v224
	v_mov_b32_e32 v197, v226
	v_mov_b32_e32 v226, v225
	v_pk_add_f32 v[184:185], v[200:201], v[184:185]
	v_cndmask_b32_e64 v200, v186, v194, s[4:5]
	v_cndmask_b32_e64 v202, v194, v186, s[4:5]
	v_cndmask_b32_e64 v186, v187, v195, s[4:5]
	v_pk_add_f32 v[188:189], v[188:189], v[210:211]
	v_pk_add_f32 v[196:197], v[196:197], v[226:227]
	v_mov_b32_dpp v200, v200 row_half_mirror row_mask:0xf bank_mask:0xf bound_ctrl:1
	v_cndmask_b32_e64 v203, v195, v187, s[4:5]
	v_mov_b32_dpp v201, v186 row_half_mirror row_mask:0xf bank_mask:0xf bound_ctrl:1
	v_mov_b32_e32 v190, v212
	v_mov_b32_e32 v191, v214
	v_mov_b32_e32 v214, v213
	v_mov_b32_e32 v198, v228
	v_mov_b32_e32 v199, v230
	v_mov_b32_e32 v230, v229
	v_pk_add_f32 v[186:187], v[202:203], v[200:201]
	v_cndmask_b32_e64 v194, v188, v196, s[4:5]
	v_cndmask_b32_e64 v200, v196, v188, s[4:5]
	v_cndmask_b32_e64 v188, v189, v197, s[4:5]
	v_pk_add_f32 v[190:191], v[190:191], v[214:215]
	v_pk_add_f32 v[198:199], v[198:199], v[230:231]
	v_mov_b32_dpp v194, v194 row_half_mirror row_mask:0xf bank_mask:0xf bound_ctrl:1
	v_cndmask_b32_e64 v201, v197, v189, s[4:5]
	v_mov_b32_dpp v195, v188 row_half_mirror row_mask:0xf bank_mask:0xf bound_ctrl:1
	v_mov_b32_e32 v192, v216
	v_mov_b32_e32 v193, v218
	v_mov_b32_e32 v218, v217
	v_pk_add_f32 v[188:189], v[200:201], v[194:195]
	v_cndmask_b32_e64 v194, v190, v198, s[4:5]
	v_cndmask_b32_e64 v196, v198, v190, s[4:5]
	v_cndmask_b32_e64 v190, v191, v199, s[4:5]
	v_pk_add_f32 v[192:193], v[192:193], v[218:219]
	v_mov_b32_dpp v194, v194 row_half_mirror row_mask:0xf bank_mask:0xf bound_ctrl:1
	v_cndmask_b32_e64 v197, v199, v191, s[4:5]
	v_mov_b32_dpp v195, v190 row_half_mirror row_mask:0xf bank_mask:0xf bound_ctrl:1
	v_pk_add_f32 v[190:191], v[196:197], v[194:195]
	v_cndmask_b32_e64 v194, v192, v184, s[4:5]
	v_cndmask_b32_e64 v196, v184, v192, s[4:5]
	v_cndmask_b32_e64 v184, v193, v185, s[4:5]
	v_mov_b32_dpp v194, v194 row_half_mirror row_mask:0xf bank_mask:0xf bound_ctrl:1
	v_cndmask_b32_e64 v197, v185, v193, s[4:5]
	v_mov_b32_dpp v195, v184 row_half_mirror row_mask:0xf bank_mask:0xf bound_ctrl:1
	v_pk_add_f32 v[184:185], v[196:197], v[194:195]
	v_cndmask_b32_e64 v192, v186, v190, s[2:3]
	v_cndmask_b32_e64 v194, v190, v186, s[2:3]
	v_cndmask_b32_e64 v186, v187, v191, s[2:3]
	v_mov_b32_dpp v192, v192 quad_perm:[2,3,0,1] row_mask:0xf bank_mask:0xf bound_ctrl:1
	v_cndmask_b32_e64 v195, v191, v187, s[2:3]
	v_mov_b32_dpp v193, v186 quad_perm:[2,3,0,1] row_mask:0xf bank_mask:0xf bound_ctrl:1
	v_pk_add_f32 v[186:187], v[194:195], v[192:193]
	v_cndmask_b32_e64 v190, v188, v184, s[2:3]
	v_cndmask_b32_e64 v192, v184, v188, s[2:3]
	v_cndmask_b32_e64 v184, v189, v185, s[2:3]
	v_mov_b32_dpp v190, v190 quad_perm:[2,3,0,1] row_mask:0xf bank_mask:0xf bound_ctrl:1
	v_cndmask_b32_e64 v193, v185, v189, s[2:3]
	v_mov_b32_dpp v191, v184 quad_perm:[2,3,0,1] row_mask:0xf bank_mask:0xf bound_ctrl:1
	v_pk_add_f32 v[184:185], v[192:193], v[190:191]
	s_ashr_i32 s11, s10, 31
	v_cndmask_b32_e64 v188, v186, v184, s[0:1]
	v_cndmask_b32_e64 v190, v184, v186, s[0:1]
	v_cndmask_b32_e64 v184, v187, v185, s[0:1]
	v_mov_b32_dpp v188, v188 quad_perm:[1,0,3,2] row_mask:0xf bank_mask:0xf bound_ctrl:1
	v_cndmask_b32_e64 v191, v185, v187, s[0:1]
	v_mov_b32_dpp v189, v184 quad_perm:[1,0,3,2] row_mask:0xf bank_mask:0xf bound_ctrl:1
	v_pk_add_f32 v[184:185], v[190:191], v[188:189]
	s_lshl_b64 s[10:11], s[10:11], 8
	v_cvt_pk_bf16_f32 v186, v184, v185
	v_lshl_add_u64 v[184:185], v[178:179], 0, s[10:11]
	global_store_dword v[184:185], v186, off
	s_add_u32 s20, s12, 0x300
	s_lshl_b32 s20, s20, 11
	v_lshl_add_u64 v[108:109], v[182:183], 0, s[20:21]
	global_load_dwordx4 v[100:103], v[108:109], off offset:16
	s_nop 0
	global_load_dwordx4 v[108:111], v[108:109], off
	s_add_u32 s12, s12, 0x200
	s_mov_b32 s14, s12
	s_waitcnt vmcnt(19)
	v_cvt_pk_f32_fp8_e32 v[200:201], v24
	v_cvt_pk_f32_fp8_sdwa v[202:203], v24 src0_sel:WORD_1
	v_cvt_pk_f32_fp8_e32 v[204:205], v25
	v_lshlrev_b32_e32 v186, 16, v20
	v_and_b32_e32 v187, 0xffff0000, v20
	v_cvt_pk_f32_fp8_sdwa v[210:211], v25 src0_sel:WORD_1
	v_lshlrev_b32_e32 v190, 16, v21
	v_and_b32_e32 v191, 0xffff0000, v21
	v_cvt_pk_f32_fp8_e32 v[212:213], v26
	v_pk_mul_f32 v[200:201], v[200:201], v[186:187]
	v_lshlrev_b32_e32 v194, 16, v22
	v_and_b32_e32 v195, 0xffff0000, v22
	v_cvt_pk_f32_fp8_sdwa v[214:215], v26 src0_sel:WORD_1
	v_pk_fma_f32 v[200:201], v[202:203], v[190:191], v[200:201]
	v_cvt_pk_f32_fp8_e32 v[202:203], v28
	v_lshlrev_b32_e32 v198, 16, v23
	v_and_b32_e32 v199, 0xffff0000, v23
	v_cvt_pk_f32_fp8_e32 v[216:217], v27
	v_pk_fma_f32 v[200:201], v[204:205], v[194:195], v[200:201]
	v_cvt_pk_f32_fp8_sdwa v[204:205], v28 src0_sel:WORD_1
	v_lshlrev_b32_e32 v184, 16, v16
	v_and_b32_e32 v185, 0xffff0000, v16
	v_cvt_pk_f32_fp8_sdwa v[218:219], v27 src0_sel:WORD_1
	v_pk_fma_f32 v[200:201], v[210:211], v[198:199], v[200:201]
	v_cvt_pk_f32_fp8_e32 v[210:211], v29
	v_lshlrev_b32_e32 v188, 16, v17
	v_and_b32_e32 v189, 0xffff0000, v17
	v_pk_fma_f32 v[200:201], v[212:213], v[184:185], v[200:201]
	v_cvt_pk_f32_fp8_sdwa v[212:213], v29 src0_sel:WORD_1
	v_lshlrev_b32_e32 v192, 16, v18
	v_and_b32_e32 v193, 0xffff0000, v18
	v_pk_fma_f32 v[200:201], v[214:215], v[188:189], v[200:201]
	v_cvt_pk_f32_fp8_e32 v[214:215], v30
	v_pk_mul_f32 v[202:203], v[202:203], v[186:187]
	v_lshlrev_b32_e32 v196, 16, v19
	v_and_b32_e32 v197, 0xffff0000, v19
	v_pk_fma_f32 v[200:201], v[216:217], v[192:193], v[200:201]
	v_cvt_pk_f32_fp8_sdwa v[216:217], v30 src0_sel:WORD_1
	v_pk_fma_f32 v[202:203], v[204:205], v[190:191], v[202:203]
	v_cvt_pk_f32_fp8_e32 v[204:205], v32
	v_pk_fma_f32 v[200:201], v[218:219], v[196:197], v[200:201]
	v_cvt_pk_f32_fp8_e32 v[218:219], v31
	v_pk_fma_f32 v[202:203], v[210:211], v[194:195], v[202:203]
	v_cvt_pk_f32_fp8_sdwa v[210:211], v32 src0_sel:WORD_1
	v_cvt_pk_f32_fp8_sdwa v[220:221], v31 src0_sel:WORD_1
	v_pk_fma_f32 v[202:203], v[212:213], v[198:199], v[202:203]
	v_cvt_pk_f32_fp8_e32 v[212:213], v33
	v_pk_fma_f32 v[202:203], v[214:215], v[184:185], v[202:203]
	v_cvt_pk_f32_fp8_sdwa v[214:215], v33 src0_sel:WORD_1
	v_pk_fma_f32 v[202:203], v[216:217], v[188:189], v[202:203]
	v_cvt_pk_f32_fp8_e32 v[216:217], v34
	v_pk_mul_f32 v[204:205], v[204:205], v[186:187]
	v_pk_fma_f32 v[202:203], v[218:219], v[192:193], v[202:203]
	v_cvt_pk_f32_fp8_sdwa v[218:219], v34 src0_sel:WORD_1
	v_pk_fma_f32 v[204:205], v[210:211], v[190:191], v[204:205]
	v_cvt_pk_f32_fp8_e32 v[210:211], v36
	v_pk_fma_f32 v[202:203], v[220:221], v[196:197], v[202:203]
	v_cvt_pk_f32_fp8_e32 v[220:221], v35
	v_pk_fma_f32 v[204:205], v[212:213], v[194:195], v[204:205]
	v_cvt_pk_f32_fp8_sdwa v[212:213], v36 src0_sel:WORD_1
	v_cvt_pk_f32_fp8_sdwa v[222:223], v35 src0_sel:WORD_1
	v_pk_fma_f32 v[204:205], v[214:215], v[198:199], v[204:205]
	v_cvt_pk_f32_fp8_e32 v[214:215], v37
	v_pk_fma_f32 v[204:205], v[216:217], v[184:185], v[204:205]
	v_cvt_pk_f32_fp8_sdwa v[216:217], v37 src0_sel:WORD_1
	v_pk_fma_f32 v[204:205], v[218:219], v[188:189], v[204:205]
	v_cvt_pk_f32_fp8_e32 v[218:219], v38
	v_pk_mul_f32 v[210:211], v[210:211], v[186:187]
	v_pk_fma_f32 v[204:205], v[220:221], v[192:193], v[204:205]
	v_cvt_pk_f32_fp8_sdwa v[220:221], v38 src0_sel:WORD_1
	v_pk_fma_f32 v[210:211], v[212:213], v[190:191], v[210:211]
	v_cvt_pk_f32_fp8_e32 v[212:213], v40
	v_pk_fma_f32 v[204:205], v[222:223], v[196:197], v[204:205]
	v_cvt_pk_f32_fp8_e32 v[222:223], v39
	v_pk_fma_f32 v[210:211], v[214:215], v[194:195], v[210:211]
	v_cvt_pk_f32_fp8_sdwa v[214:215], v40 src0_sel:WORD_1
	v_cvt_pk_f32_fp8_sdwa v[224:225], v39 src0_sel:WORD_1
	v_pk_fma_f32 v[210:211], v[216:217], v[198:199], v[210:211]
	v_cvt_pk_f32_fp8_e32 v[216:217], v41
	v_pk_fma_f32 v[210:211], v[218:219], v[184:185], v[210:211]
	v_cvt_pk_f32_fp8_sdwa v[218:219], v41 src0_sel:WORD_1
	v_pk_fma_f32 v[210:211], v[220:221], v[188:189], v[210:211]
	v_cvt_pk_f32_fp8_e32 v[220:221], v42
	v_pk_mul_f32 v[212:213], v[212:213], v[186:187]
	v_pk_fma_f32 v[210:211], v[222:223], v[192:193], v[210:211]
	v_cvt_pk_f32_fp8_sdwa v[222:223], v42 src0_sel:WORD_1
	v_pk_fma_f32 v[212:213], v[214:215], v[190:191], v[212:213]
	v_cvt_pk_f32_fp8_e32 v[214:215], v44
	v_pk_fma_f32 v[210:211], v[224:225], v[196:197], v[210:211]
	v_cvt_pk_f32_fp8_e32 v[224:225], v43
	v_pk_fma_f32 v[212:213], v[216:217], v[194:195], v[212:213]
	v_cvt_pk_f32_fp8_sdwa v[216:217], v44 src0_sel:WORD_1
	v_cvt_pk_f32_fp8_sdwa v[226:227], v43 src0_sel:WORD_1
	v_pk_fma_f32 v[212:213], v[218:219], v[198:199], v[212:213]
	v_cvt_pk_f32_fp8_e32 v[218:219], v45
	v_pk_fma_f32 v[212:213], v[220:221], v[184:185], v[212:213]
	v_cvt_pk_f32_fp8_sdwa v[220:221], v45 src0_sel:WORD_1
	v_pk_fma_f32 v[212:213], v[222:223], v[188:189], v[212:213]
	v_cvt_pk_f32_fp8_e32 v[222:223], v46
	v_pk_mul_f32 v[214:215], v[214:215], v[186:187]
	v_pk_fma_f32 v[212:213], v[224:225], v[192:193], v[212:213]
	v_cvt_pk_f32_fp8_sdwa v[224:225], v46 src0_sel:WORD_1
	v_pk_fma_f32 v[214:215], v[216:217], v[190:191], v[214:215]
	v_cvt_pk_f32_fp8_e32 v[216:217], v48
	v_pk_fma_f32 v[212:213], v[226:227], v[196:197], v[212:213]
	v_cvt_pk_f32_fp8_e32 v[226:227], v47
	v_pk_fma_f32 v[214:215], v[218:219], v[194:195], v[214:215]
	v_cvt_pk_f32_fp8_sdwa v[218:219], v48 src0_sel:WORD_1
	v_cvt_pk_f32_fp8_sdwa v[228:229], v47 src0_sel:WORD_1
	v_pk_fma_f32 v[214:215], v[220:221], v[198:199], v[214:215]
	v_cvt_pk_f32_fp8_e32 v[220:221], v49
	v_pk_fma_f32 v[214:215], v[222:223], v[184:185], v[214:215]
	v_cvt_pk_f32_fp8_sdwa v[222:223], v49 src0_sel:WORD_1
	v_pk_fma_f32 v[214:215], v[224:225], v[188:189], v[214:215]
	v_cvt_pk_f32_fp8_e32 v[224:225], v50
	v_pk_mul_f32 v[216:217], v[216:217], v[186:187]
	v_pk_fma_f32 v[214:215], v[226:227], v[192:193], v[214:215]
	v_cvt_pk_f32_fp8_sdwa v[226:227], v50 src0_sel:WORD_1
	v_pk_fma_f32 v[216:217], v[218:219], v[190:191], v[216:217]
	v_cvt_pk_f32_fp8_e32 v[218:219], v52
	v_pk_fma_f32 v[214:215], v[228:229], v[196:197], v[214:215]
	v_cvt_pk_f32_fp8_e32 v[228:229], v51
	v_pk_fma_f32 v[216:217], v[220:221], v[194:195], v[216:217]
	v_cvt_pk_f32_fp8_sdwa v[220:221], v52 src0_sel:WORD_1
	v_cvt_pk_f32_fp8_sdwa v[230:231], v51 src0_sel:WORD_1
	v_pk_fma_f32 v[216:217], v[222:223], v[198:199], v[216:217]
	v_cvt_pk_f32_fp8_e32 v[222:223], v53
	v_pk_fma_f32 v[216:217], v[224:225], v[184:185], v[216:217]
	v_cvt_pk_f32_fp8_sdwa v[224:225], v53 src0_sel:WORD_1
	v_pk_fma_f32 v[216:217], v[226:227], v[188:189], v[216:217]
	v_cvt_pk_f32_fp8_e32 v[226:227], v54
	v_pk_mul_f32 v[218:219], v[218:219], v[186:187]
	v_pk_fma_f32 v[216:217], v[228:229], v[192:193], v[216:217]
	v_cvt_pk_f32_fp8_sdwa v[228:229], v54 src0_sel:WORD_1
	v_pk_fma_f32 v[218:219], v[220:221], v[190:191], v[218:219]
	v_cvt_pk_f32_fp8_e32 v[220:221], v56
	v_pk_fma_f32 v[216:217], v[230:231], v[196:197], v[216:217]
	v_cvt_pk_f32_fp8_e32 v[230:231], v55
	v_pk_fma_f32 v[218:219], v[222:223], v[194:195], v[218:219]
	v_cvt_pk_f32_fp8_sdwa v[222:223], v56 src0_sel:WORD_1
	v_cvt_pk_f32_fp8_sdwa v[232:233], v55 src0_sel:WORD_1
	v_pk_fma_f32 v[218:219], v[224:225], v[198:199], v[218:219]
	v_cvt_pk_f32_fp8_e32 v[224:225], v57
	v_pk_fma_f32 v[218:219], v[226:227], v[184:185], v[218:219]
	v_cvt_pk_f32_fp8_sdwa v[226:227], v57 src0_sel:WORD_1
	v_pk_fma_f32 v[218:219], v[228:229], v[188:189], v[218:219]
	v_cvt_pk_f32_fp8_e32 v[228:229], v58
	v_pk_mul_f32 v[220:221], v[220:221], v[186:187]
	v_pk_fma_f32 v[218:219], v[230:231], v[192:193], v[218:219]
	v_cvt_pk_f32_fp8_sdwa v[230:231], v58 src0_sel:WORD_1
	v_pk_fma_f32 v[220:221], v[222:223], v[190:191], v[220:221]
	v_cvt_pk_f32_fp8_e32 v[222:223], v60
	v_pk_fma_f32 v[218:219], v[232:233], v[196:197], v[218:219]
	v_cvt_pk_f32_fp8_e32 v[232:233], v59
	v_pk_fma_f32 v[220:221], v[224:225], v[194:195], v[220:221]
	v_cvt_pk_f32_fp8_sdwa v[224:225], v60 src0_sel:WORD_1
	v_cvt_pk_f32_fp8_sdwa v[234:235], v59 src0_sel:WORD_1
	v_pk_fma_f32 v[220:221], v[226:227], v[198:199], v[220:221]
	v_cvt_pk_f32_fp8_e32 v[226:227], v61
	v_pk_fma_f32 v[220:221], v[228:229], v[184:185], v[220:221]
	v_cvt_pk_f32_fp8_sdwa v[228:229], v61 src0_sel:WORD_1
	v_pk_fma_f32 v[220:221], v[230:231], v[188:189], v[220:221]
	v_cvt_pk_f32_fp8_e32 v[230:231], v62
	v_pk_mul_f32 v[222:223], v[222:223], v[186:187]
	v_pk_fma_f32 v[220:221], v[232:233], v[192:193], v[220:221]
	v_cvt_pk_f32_fp8_sdwa v[232:233], v62 src0_sel:WORD_1
	v_pk_fma_f32 v[222:223], v[224:225], v[190:191], v[222:223]
	v_cvt_pk_f32_fp8_e32 v[224:225], v76
	v_pk_fma_f32 v[220:221], v[234:235], v[196:197], v[220:221]
	v_cvt_pk_f32_fp8_e32 v[234:235], v63
	v_pk_fma_f32 v[222:223], v[226:227], v[194:195], v[222:223]
	v_cvt_pk_f32_fp8_sdwa v[226:227], v76 src0_sel:WORD_1
	v_cvt_pk_f32_fp8_sdwa v[236:237], v63 src0_sel:WORD_1
	v_pk_fma_f32 v[222:223], v[228:229], v[198:199], v[222:223]
	v_cvt_pk_f32_fp8_e32 v[228:229], v77
	v_pk_fma_f32 v[222:223], v[230:231], v[184:185], v[222:223]
	v_cvt_pk_f32_fp8_sdwa v[230:231], v77 src0_sel:WORD_1
	v_pk_fma_f32 v[222:223], v[232:233], v[188:189], v[222:223]
	v_cvt_pk_f32_fp8_e32 v[232:233], v78
	v_pk_mul_f32 v[224:225], v[224:225], v[186:187]
	v_pk_fma_f32 v[222:223], v[234:235], v[192:193], v[222:223]
	v_cvt_pk_f32_fp8_sdwa v[234:235], v78 src0_sel:WORD_1
	v_pk_fma_f32 v[224:225], v[226:227], v[190:191], v[224:225]
	v_cvt_pk_f32_fp8_e32 v[226:227], v84
	v_pk_fma_f32 v[222:223], v[236:237], v[196:197], v[222:223]
	v_cvt_pk_f32_fp8_e32 v[236:237], v79
	v_pk_fma_f32 v[224:225], v[228:229], v[194:195], v[224:225]
	v_cvt_pk_f32_fp8_sdwa v[228:229], v84 src0_sel:WORD_1
	v_cvt_pk_f32_fp8_sdwa v[238:239], v79 src0_sel:WORD_1
	v_pk_fma_f32 v[224:225], v[230:231], v[198:199], v[224:225]
	v_cvt_pk_f32_fp8_e32 v[230:231], v85
	v_pk_fma_f32 v[224:225], v[232:233], v[184:185], v[224:225]
	v_cvt_pk_f32_fp8_sdwa v[232:233], v85 src0_sel:WORD_1
	v_pk_fma_f32 v[224:225], v[234:235], v[188:189], v[224:225]
	v_cvt_pk_f32_fp8_e32 v[234:235], v86
	v_pk_mul_f32 v[226:227], v[226:227], v[186:187]
	v_pk_fma_f32 v[224:225], v[236:237], v[192:193], v[224:225]
	v_cvt_pk_f32_fp8_sdwa v[236:237], v86 src0_sel:WORD_1
	v_pk_fma_f32 v[226:227], v[228:229], v[190:191], v[226:227]
	v_cvt_pk_f32_fp8_e32 v[228:229], v88
	v_pk_fma_f32 v[224:225], v[238:239], v[196:197], v[224:225]
	v_cvt_pk_f32_fp8_e32 v[238:239], v87
	v_pk_fma_f32 v[226:227], v[230:231], v[194:195], v[226:227]
	v_cvt_pk_f32_fp8_sdwa v[230:231], v88 src0_sel:WORD_1
	v_cvt_pk_f32_fp8_sdwa v[240:241], v87 src0_sel:WORD_1
	v_pk_fma_f32 v[226:227], v[232:233], v[198:199], v[226:227]
	v_cvt_pk_f32_fp8_e32 v[232:233], v89
	v_pk_fma_f32 v[226:227], v[234:235], v[184:185], v[226:227]
	v_cvt_pk_f32_fp8_sdwa v[234:235], v89 src0_sel:WORD_1
	v_pk_fma_f32 v[226:227], v[236:237], v[188:189], v[226:227]
	v_cvt_pk_f32_fp8_e32 v[236:237], v90
	v_pk_mul_f32 v[228:229], v[228:229], v[186:187]
	v_pk_fma_f32 v[226:227], v[238:239], v[192:193], v[226:227]
	v_cvt_pk_f32_fp8_sdwa v[238:239], v90 src0_sel:WORD_1
	v_pk_fma_f32 v[228:229], v[230:231], v[190:191], v[228:229]
	v_cvt_pk_f32_fp8_e32 v[230:231], v92
	v_pk_fma_f32 v[226:227], v[240:241], v[196:197], v[226:227]
	v_cvt_pk_f32_fp8_e32 v[240:241], v91
	v_pk_fma_f32 v[228:229], v[232:233], v[194:195], v[228:229]
	v_cvt_pk_f32_fp8_sdwa v[232:233], v92 src0_sel:WORD_1
; #define PD_E(t, E) do { const char* eb_ = eiu + (size_t)(t) * 512; _Pragma("unroll") for (int q = 0; q < 4; ++q) E[q] = *(const i32x4_t*)(eb_ + (eio + 16u * q)); } while (0)
; #define PD_H(t, H) do { const char* hb_ = h2u + (size_t)(t) * 2048; H[0] = *(const u32x4*)(hb_ + h2o); H[1] = *(const u32x4*)(hb_ + (h2o + 16u)); } while (0)
; #define PD_TAB(E, W) do { _Pragma("unroll") for (int q = 0; q < 16; ++q) W[q] = *(const u32x4*)(tabu + ((unsigned)E[q >> 2][q & 3] * 128u + tabo)); } while (0)
; DI void phase_peerdown(const Params& p, int bid, int nb) {
;     ...
;     if (t1 < T_) PD_TAB(eB, wB);
;     const int t2 = t1 + nw; if (t2 < T_) PD_E(t2, eA);
;     PD_MATH(t, wA, hA);
;     if (t1 >= T_) break;
;     if (t2 < T_) { PD_H(t2, hA); PD_TAB(eA, wA); }
;     const int t3 = t2 + nw; if (t3 < T_) PD_E(t3, eB);
;     PD_MATH(t1, wB, hB);
;     if (t2 >= T_) break;
;     if (t3 < T_) PD_H(t3, hB);
;     t = t2; t1 = t3;
;   }
	v_cvt_pk_f32_fp8_sdwa v[242:243], v91 src0_sel:WORD_1
	v_pk_fma_f32 v[228:229], v[234:235], v[198:199], v[228:229]
	v_cvt_pk_f32_fp8_e32 v[234:235], v93
	v_pk_fma_f32 v[228:229], v[236:237], v[184:185], v[228:229]
	v_cvt_pk_f32_fp8_sdwa v[236:237], v93 src0_sel:WORD_1
	v_pk_fma_f32 v[228:229], v[238:239], v[188:189], v[228:229]
	v_cvt_pk_f32_fp8_e32 v[238:239], v94
	v_pk_mul_f32 v[230:231], v[230:231], v[186:187]
	v_pk_fma_f32 v[228:229], v[240:241], v[192:193], v[228:229]
	v_cvt_pk_f32_fp8_sdwa v[240:241], v94 src0_sel:WORD_1
	v_pk_fma_f32 v[230:231], v[232:233], v[190:191], v[230:231]
	v_cvt_pk_f32_fp8_e32 v[232:233], v96
	v_pk_fma_f32 v[228:229], v[242:243], v[196:197], v[228:229]
	v_cvt_pk_f32_fp8_e32 v[242:243], v95
	v_pk_fma_f32 v[230:231], v[234:235], v[194:195], v[230:231]
	v_cvt_pk_f32_fp8_sdwa v[234:235], v96 src0_sel:WORD_1
	v_cvt_pk_f32_fp8_sdwa v[244:245], v95 src0_sel:WORD_1
	v_pk_fma_f32 v[230:231], v[236:237], v[198:199], v[230:231]
	v_cvt_pk_f32_fp8_e32 v[236:237], v97
	v_pk_fma_f32 v[230:231], v[238:239], v[184:185], v[230:231]
	v_cvt_pk_f32_fp8_sdwa v[238:239], v97 src0_sel:WORD_1
	v_pk_fma_f32 v[230:231], v[240:241], v[188:189], v[230:231]
	v_cvt_pk_f32_fp8_e32 v[240:241], v98
	v_pk_mul_f32 v[232:233], v[232:233], v[186:187]
	v_pk_fma_f32 v[230:231], v[242:243], v[192:193], v[230:231]
	v_cvt_pk_f32_fp8_sdwa v[242:243], v98 src0_sel:WORD_1
	v_pk_fma_f32 v[232:233], v[234:235], v[190:191], v[232:233]
	v_cvt_pk_f32_fp8_e32 v[234:235], v104
	v_pk_fma_f32 v[230:231], v[244:245], v[196:197], v[230:231]
	v_cvt_pk_f32_fp8_e32 v[244:245], v99
	v_pk_fma_f32 v[232:233], v[236:237], v[194:195], v[232:233]
	v_cvt_pk_f32_fp8_sdwa v[236:237], v104 src0_sel:WORD_1
	v_cvt_pk_f32_fp8_sdwa v[246:247], v99 src0_sel:WORD_1
	v_pk_fma_f32 v[232:233], v[238:239], v[198:199], v[232:233]
	v_cvt_pk_f32_fp8_e32 v[238:239], v105
	v_pk_fma_f32 v[232:233], v[240:241], v[184:185], v[232:233]
	v_cvt_pk_f32_fp8_sdwa v[240:241], v105 src0_sel:WORD_1
	v_pk_fma_f32 v[232:233], v[242:243], v[188:189], v[232:233]
	v_cvt_pk_f32_fp8_e32 v[242:243], v106
	v_pk_mul_f32 v[186:187], v[234:235], v[186:187]
	v_pk_fma_f32 v[232:233], v[244:245], v[192:193], v[232:233]
	v_cvt_pk_f32_fp8_sdwa v[244:245], v106 src0_sel:WORD_1
	v_pk_fma_f32 v[186:187], v[236:237], v[190:191], v[186:187]
	v_pk_fma_f32 v[232:233], v[246:247], v[196:197], v[232:233]
	v_cvt_pk_f32_fp8_e32 v[246:247], v107
	v_pk_fma_f32 v[186:187], v[238:239], v[194:195], v[186:187]
	v_cvt_pk_f32_fp8_sdwa v[248:249], v107 src0_sel:WORD_1
	v_pk_fma_f32 v[186:187], v[240:241], v[198:199], v[186:187]
	v_mov_b32_e32 v194, v220
	v_pk_fma_f32 v[184:185], v[242:243], v[184:185], v[186:187]
	v_mov_b32_e32 v186, v200
	v_pk_fma_f32 v[184:185], v[244:245], v[188:189], v[184:185]
	v_mov_b32_e32 v187, v202
	v_pk_fma_f32 v[184:185], v[246:247], v[192:193], v[184:185]
	v_mov_b32_e32 v202, v201
	v_pk_fma_f32 v[184:185], v[248:249], v[196:197], v[184:185]
	v_mov_b32_e32 v195, v222
	v_mov_b32_e32 v222, v221
	v_pk_add_f32 v[186:187], v[186:187], v[202:203]
	v_pk_add_f32 v[194:195], v[194:195], v[222:223]
	v_mov_b32_e32 v200, v232
	v_mov_b32_e32 v201, v184
	v_mov_b32_e32 v184, v233
	v_mov_b32_e32 v188, v204
	v_mov_b32_e32 v189, v210
	v_mov_b32_e32 v210, v205
	v_mov_b32_e32 v196, v224
	v_mov_b32_e32 v197, v226
	v_mov_b32_e32 v226, v225
	v_pk_add_f32 v[184:185], v[200:201], v[184:185]
	v_cndmask_b32_e64 v200, v186, v194, s[4:5]
	v_cndmask_b32_e64 v202, v194, v186, s[4:5]
	v_cndmask_b32_e64 v186, v187, v195, s[4:5]
	v_pk_add_f32 v[188:189], v[188:189], v[210:211]
	v_pk_add_f32 v[196:197], v[196:197], v[226:227]
	v_mov_b32_dpp v200, v200 row_half_mirror row_mask:0xf bank_mask:0xf bound_ctrl:1
	v_cndmask_b32_e64 v203, v195, v187, s[4:5]
	v_mov_b32_dpp v201, v186 row_half_mirror row_mask:0xf bank_mask:0xf bound_ctrl:1
	v_mov_b32_e32 v190, v212
	v_mov_b32_e32 v191, v214
	v_mov_b32_e32 v214, v213
	v_mov_b32_e32 v198, v228
	v_mov_b32_e32 v199, v230
	v_mov_b32_e32 v230, v229
	v_pk_add_f32 v[186:187], v[202:203], v[200:201]
	v_cndmask_b32_e64 v194, v188, v196, s[4:5]
	v_cndmask_b32_e64 v200, v196, v188, s[4:5]
	v_cndmask_b32_e64 v188, v189, v197, s[4:5]
	v_pk_add_f32 v[190:191], v[190:191], v[214:215]
	v_pk_add_f32 v[198:199], v[198:199], v[230:231]
	v_mov_b32_dpp v194, v194 row_half_mirror row_mask:0xf bank_mask:0xf bound_ctrl:1
	v_cndmask_b32_e64 v201, v197, v189, s[4:5]
	v_mov_b32_dpp v195, v188 row_half_mirror row_mask:0xf bank_mask:0xf bound_ctrl:1
	v_mov_b32_e32 v192, v216
	v_mov_b32_e32 v193, v218
	v_mov_b32_e32 v218, v217
	v_pk_add_f32 v[188:189], v[200:201], v[194:195]
	v_cndmask_b32_e64 v194, v190, v198, s[4:5]
	v_cndmask_b32_e64 v196, v198, v190, s[4:5]
	v_cndmask_b32_e64 v190, v191, v199, s[4:5]
	v_pk_add_f32 v[192:193], v[192:193], v[218:219]
	v_mov_b32_dpp v194, v194 row_half_mirror row_mask:0xf bank_mask:0xf bound_ctrl:1
	v_cndmask_b32_e64 v197, v199, v191, s[4:5]
	v_mov_b32_dpp v195, v190 row_half_mirror row_mask:0xf bank_mask:0xf bound_ctrl:1
	v_pk_add_f32 v[190:191], v[196:197], v[194:195]
	v_cndmask_b32_e64 v194, v192, v184, s[4:5]
	v_cndmask_b32_e64 v196, v184, v192, s[4:5]
	v_cndmask_b32_e64 v184, v193, v185, s[4:5]
	v_mov_b32_dpp v194, v194 row_half_mirror row_mask:0xf bank_mask:0xf bound_ctrl:1
	v_cndmask_b32_e64 v197, v185, v193, s[4:5]
	v_mov_b32_dpp v195, v184 row_half_mirror row_mask:0xf bank_mask:0xf bound_ctrl:1
	v_pk_add_f32 v[184:185], v[196:197], v[194:195]
	v_cndmask_b32_e64 v192, v186, v190, s[2:3]
	v_cndmask_b32_e64 v194, v190, v186, s[2:3]
	v_cndmask_b32_e64 v186, v187, v191, s[2:3]
	v_mov_b32_dpp v192, v192 quad_perm:[2,3,0,1] row_mask:0xf bank_mask:0xf bound_ctrl:1
	v_cndmask_b32_e64 v195, v191, v187, s[2:3]
	v_mov_b32_dpp v193, v186 quad_perm:[2,3,0,1] row_mask:0xf bank_mask:0xf bound_ctrl:1
	v_pk_add_f32 v[186:187], v[194:195], v[192:193]
	v_cndmask_b32_e64 v190, v188, v184, s[2:3]
	v_cndmask_b32_e64 v192, v184, v188, s[2:3]
	v_cndmask_b32_e64 v184, v189, v185, s[2:3]
	v_mov_b32_dpp v190, v190 quad_perm:[2,3,0,1] row_mask:0xf bank_mask:0xf bound_ctrl:1
	v_cndmask_b32_e64 v193, v185, v189, s[2:3]
	v_mov_b32_dpp v191, v184 quad_perm:[2,3,0,1] row_mask:0xf bank_mask:0xf bound_ctrl:1
	v_pk_add_f32 v[184:185], v[192:193], v[190:191]
	s_ashr_i32 s15, s14, 31
	v_cndmask_b32_e64 v188, v186, v184, s[0:1]
	v_cndmask_b32_e64 v190, v184, v186, s[0:1]
	v_cndmask_b32_e64 v184, v187, v185, s[0:1]
	v_mov_b32_dpp v188, v188 quad_perm:[1,0,3,2] row_mask:0xf bank_mask:0xf bound_ctrl:1
	v_cndmask_b32_e64 v191, v185, v187, s[0:1]
	v_mov_b32_dpp v189, v184 quad_perm:[1,0,3,2] row_mask:0xf bank_mask:0xf bound_ctrl:1
	v_pk_add_f32 v[184:185], v[190:191], v[188:189]
	s_lshl_b64 s[14:15], s[14:15], 8
	v_cvt_pk_bf16_f32 v186, v184, v185
	v_lshl_add_u64 v[184:185], v[178:179], 0, s[14:15]
	global_store_dword v[184:185], v186, off
	s_add_u32 s10, s12, 0x100
	s_waitcnt vmcnt(1)
	v_cvt_pk_f32_fp8_e32 v[200:201], v112
	v_cvt_pk_f32_fp8_sdwa v[202:203], v112 src0_sel:WORD_1
	v_cvt_pk_f32_fp8_e32 v[204:205], v113
	v_lshlrev_b32_e32 v186, 16, v108
	v_and_b32_e32 v187, 0xffff0000, v108
	v_cvt_pk_f32_fp8_sdwa v[210:211], v113 src0_sel:WORD_1
	v_lshlrev_b32_e32 v190, 16, v109
	v_and_b32_e32 v191, 0xffff0000, v109
	v_cvt_pk_f32_fp8_e32 v[212:213], v114
	v_pk_mul_f32 v[200:201], v[200:201], v[186:187]
	v_lshlrev_b32_e32 v194, 16, v110
	v_and_b32_e32 v195, 0xffff0000, v110
	v_cvt_pk_f32_fp8_sdwa v[214:215], v114 src0_sel:WORD_1
	v_pk_fma_f32 v[200:201], v[202:203], v[190:191], v[200:201]
	v_cvt_pk_f32_fp8_e32 v[202:203], v116
	v_lshlrev_b32_e32 v198, 16, v111
	v_and_b32_e32 v199, 0xffff0000, v111
	v_cvt_pk_f32_fp8_e32 v[216:217], v115
	v_pk_fma_f32 v[200:201], v[204:205], v[194:195], v[200:201]
	v_cvt_pk_f32_fp8_sdwa v[204:205], v116 src0_sel:WORD_1
	v_lshlrev_b32_e32 v184, 16, v100
	v_and_b32_e32 v185, 0xffff0000, v100
	v_cvt_pk_f32_fp8_sdwa v[218:219], v115 src0_sel:WORD_1
	v_pk_fma_f32 v[200:201], v[210:211], v[198:199], v[200:201]
	v_cvt_pk_f32_fp8_e32 v[210:211], v117
	v_lshlrev_b32_e32 v188, 16, v101
	v_and_b32_e32 v189, 0xffff0000, v101
	v_pk_fma_f32 v[200:201], v[212:213], v[184:185], v[200:201]
	v_cvt_pk_f32_fp8_sdwa v[212:213], v117 src0_sel:WORD_1
	v_lshlrev_b32_e32 v192, 16, v102
	v_and_b32_e32 v193, 0xffff0000, v102
	v_pk_fma_f32 v[200:201], v[214:215], v[188:189], v[200:201]
	v_cvt_pk_f32_fp8_e32 v[214:215], v118
	v_pk_mul_f32 v[202:203], v[202:203], v[186:187]
	v_lshlrev_b32_e32 v196, 16, v103
	v_and_b32_e32 v197, 0xffff0000, v103
	v_pk_fma_f32 v[200:201], v[216:217], v[192:193], v[200:201]
	v_cvt_pk_f32_fp8_sdwa v[216:217], v118 src0_sel:WORD_1
	v_pk_fma_f32 v[202:203], v[204:205], v[190:191], v[202:203]
	v_cvt_pk_f32_fp8_e32 v[204:205], v120
	v_pk_fma_f32 v[200:201], v[218:219], v[196:197], v[200:201]
	v_cvt_pk_f32_fp8_e32 v[218:219], v119
	v_pk_fma_f32 v[202:203], v[210:211], v[194:195], v[202:203]
	v_cvt_pk_f32_fp8_sdwa v[210:211], v120 src0_sel:WORD_1
	v_cvt_pk_f32_fp8_sdwa v[220:221], v119 src0_sel:WORD_1
	v_pk_fma_f32 v[202:203], v[212:213], v[198:199], v[202:203]
	v_cvt_pk_f32_fp8_e32 v[212:213], v121
	v_pk_fma_f32 v[202:203], v[214:215], v[184:185], v[202:203]
	v_cvt_pk_f32_fp8_sdwa v[214:215], v121 src0_sel:WORD_1
	v_pk_fma_f32 v[202:203], v[216:217], v[188:189], v[202:203]
	v_cvt_pk_f32_fp8_e32 v[216:217], v122
	v_pk_mul_f32 v[204:205], v[204:205], v[186:187]
	v_pk_fma_f32 v[202:203], v[218:219], v[192:193], v[202:203]
	v_cvt_pk_f32_fp8_sdwa v[218:219], v122 src0_sel:WORD_1
	v_pk_fma_f32 v[204:205], v[210:211], v[190:191], v[204:205]
	v_cvt_pk_f32_fp8_e32 v[210:211], v124
	v_pk_fma_f32 v[202:203], v[220:221], v[196:197], v[202:203]
	v_cvt_pk_f32_fp8_e32 v[220:221], v123
	v_pk_fma_f32 v[204:205], v[212:213], v[194:195], v[204:205]
	v_cvt_pk_f32_fp8_sdwa v[212:213], v124 src0_sel:WORD_1
	v_cvt_pk_f32_fp8_sdwa v[222:223], v123 src0_sel:WORD_1
	v_pk_fma_f32 v[204:205], v[214:215], v[198:199], v[204:205]
	v_cvt_pk_f32_fp8_e32 v[214:215], v125
	v_pk_fma_f32 v[204:205], v[216:217], v[184:185], v[204:205]
	v_cvt_pk_f32_fp8_sdwa v[216:217], v125 src0_sel:WORD_1
	v_pk_fma_f32 v[204:205], v[218:219], v[188:189], v[204:205]
	v_cvt_pk_f32_fp8_e32 v[218:219], v126
	v_pk_mul_f32 v[210:211], v[210:211], v[186:187]
	v_pk_fma_f32 v[204:205], v[220:221], v[192:193], v[204:205]
	v_cvt_pk_f32_fp8_sdwa v[220:221], v126 src0_sel:WORD_1
	v_pk_fma_f32 v[210:211], v[212:213], v[190:191], v[210:211]
	v_cvt_pk_f32_fp8_e32 v[212:213], v128
	v_pk_fma_f32 v[204:205], v[222:223], v[196:197], v[204:205]
	v_cvt_pk_f32_fp8_e32 v[222:223], v127
	v_pk_fma_f32 v[210:211], v[214:215], v[194:195], v[210:211]
	v_cvt_pk_f32_fp8_sdwa v[214:215], v128 src0_sel:WORD_1
	v_cvt_pk_f32_fp8_sdwa v[224:225], v127 src0_sel:WORD_1
	v_pk_fma_f32 v[210:211], v[216:217], v[198:199], v[210:211]
	v_cvt_pk_f32_fp8_e32 v[216:217], v129
	v_pk_fma_f32 v[210:211], v[218:219], v[184:185], v[210:211]
	v_cvt_pk_f32_fp8_sdwa v[218:219], v129 src0_sel:WORD_1
	v_pk_fma_f32 v[210:211], v[220:221], v[188:189], v[210:211]
	v_cvt_pk_f32_fp8_e32 v[220:221], v130
	v_pk_mul_f32 v[212:213], v[212:213], v[186:187]
	v_pk_fma_f32 v[210:211], v[222:223], v[192:193], v[210:211]
	v_cvt_pk_f32_fp8_sdwa v[222:223], v130 src0_sel:WORD_1
	v_pk_fma_f32 v[212:213], v[214:215], v[190:191], v[212:213]
	v_cvt_pk_f32_fp8_e32 v[214:215], v132
	v_pk_fma_f32 v[210:211], v[224:225], v[196:197], v[210:211]
	v_cvt_pk_f32_fp8_e32 v[224:225], v131
	v_pk_fma_f32 v[212:213], v[216:217], v[194:195], v[212:213]
	v_cvt_pk_f32_fp8_sdwa v[216:217], v132 src0_sel:WORD_1
	v_cvt_pk_f32_fp8_sdwa v[226:227], v131 src0_sel:WORD_1
	v_pk_fma_f32 v[212:213], v[218:219], v[198:199], v[212:213]
	v_cvt_pk_f32_fp8_e32 v[218:219], v133
	v_pk_fma_f32 v[212:213], v[220:221], v[184:185], v[212:213]
	v_cvt_pk_f32_fp8_sdwa v[220:221], v133 src0_sel:WORD_1
	v_pk_fma_f32 v[212:213], v[222:223], v[188:189], v[212:213]
	v_cvt_pk_f32_fp8_e32 v[222:223], v134
	v_pk_mul_f32 v[214:215], v[214:215], v[186:187]
	v_pk_fma_f32 v[212:213], v[224:225], v[192:193], v[212:213]
	v_cvt_pk_f32_fp8_sdwa v[224:225], v134 src0_sel:WORD_1
	v_pk_fma_f32 v[214:215], v[216:217], v[190:191], v[214:215]
	v_cvt_pk_f32_fp8_e32 v[216:217], v136
	v_pk_fma_f32 v[212:213], v[226:227], v[196:197], v[212:213]
	v_cvt_pk_f32_fp8_e32 v[226:227], v135
	v_pk_fma_f32 v[214:215], v[218:219], v[194:195], v[214:215]
	v_cvt_pk_f32_fp8_sdwa v[218:219], v136 src0_sel:WORD_1
	v_cvt_pk_f32_fp8_sdwa v[228:229], v135 src0_sel:WORD_1
	v_pk_fma_f32 v[214:215], v[220:221], v[198:199], v[214:215]
	v_cvt_pk_f32_fp8_e32 v[220:221], v137
	v_pk_fma_f32 v[214:215], v[222:223], v[184:185], v[214:215]
	v_cvt_pk_f32_fp8_sdwa v[222:223], v137 src0_sel:WORD_1
	v_pk_fma_f32 v[214:215], v[224:225], v[188:189], v[214:215]
	v_cvt_pk_f32_fp8_e32 v[224:225], v138
	v_pk_mul_f32 v[216:217], v[216:217], v[186:187]
	v_pk_fma_f32 v[214:215], v[226:227], v[192:193], v[214:215]
	v_cvt_pk_f32_fp8_sdwa v[226:227], v138 src0_sel:WORD_1
	v_pk_fma_f32 v[216:217], v[218:219], v[190:191], v[216:217]
	v_cvt_pk_f32_fp8_e32 v[218:219], v140
	v_pk_fma_f32 v[214:215], v[228:229], v[196:197], v[214:215]
	v_cvt_pk_f32_fp8_e32 v[228:229], v139
	v_pk_fma_f32 v[216:217], v[220:221], v[194:195], v[216:217]
	v_cvt_pk_f32_fp8_sdwa v[220:221], v140 src0_sel:WORD_1
	v_cvt_pk_f32_fp8_sdwa v[230:231], v139 src0_sel:WORD_1
	v_pk_fma_f32 v[216:217], v[222:223], v[198:199], v[216:217]
	v_cvt_pk_f32_fp8_e32 v[222:223], v141
	v_pk_fma_f32 v[216:217], v[224:225], v[184:185], v[216:217]
	v_cvt_pk_f32_fp8_sdwa v[224:225], v141 src0_sel:WORD_1
	v_pk_fma_f32 v[216:217], v[226:227], v[188:189], v[216:217]
	v_cvt_pk_f32_fp8_e32 v[226:227], v142
	v_pk_mul_f32 v[218:219], v[218:219], v[186:187]
	v_pk_fma_f32 v[216:217], v[228:229], v[192:193], v[216:217]
	v_cvt_pk_f32_fp8_sdwa v[228:229], v142 src0_sel:WORD_1
	v_pk_fma_f32 v[218:219], v[220:221], v[190:191], v[218:219]
	v_cvt_pk_f32_fp8_e32 v[220:221], v144
	v_pk_fma_f32 v[216:217], v[230:231], v[196:197], v[216:217]
	v_cvt_pk_f32_fp8_e32 v[230:231], v143
	v_pk_fma_f32 v[218:219], v[222:223], v[194:195], v[218:219]
	v_cvt_pk_f32_fp8_sdwa v[222:223], v144 src0_sel:WORD_1
	v_cvt_pk_f32_fp8_sdwa v[232:233], v143 src0_sel:WORD_1
	v_pk_fma_f32 v[218:219], v[224:225], v[198:199], v[218:219]
	v_cvt_pk_f32_fp8_e32 v[224:225], v145
	v_pk_fma_f32 v[218:219], v[226:227], v[184:185], v[218:219]
	v_cvt_pk_f32_fp8_sdwa v[226:227], v145 src0_sel:WORD_1
	v_pk_fma_f32 v[218:219], v[228:229], v[188:189], v[218:219]
	v_cvt_pk_f32_fp8_e32 v[228:229], v146
	v_pk_mul_f32 v[220:221], v[220:221], v[186:187]
	v_pk_fma_f32 v[218:219], v[230:231], v[192:193], v[218:219]
	v_cvt_pk_f32_fp8_sdwa v[230:231], v146 src0_sel:WORD_1
	v_pk_fma_f32 v[220:221], v[222:223], v[190:191], v[220:221]
	v_cvt_pk_f32_fp8_e32 v[222:223], v148
	v_pk_fma_f32 v[218:219], v[232:233], v[196:197], v[218:219]
	v_cvt_pk_f32_fp8_e32 v[232:233], v147
	v_pk_fma_f32 v[220:221], v[224:225], v[194:195], v[220:221]
	v_cvt_pk_f32_fp8_sdwa v[224:225], v148 src0_sel:WORD_1
	v_cvt_pk_f32_fp8_sdwa v[234:235], v147 src0_sel:WORD_1
	v_pk_fma_f32 v[220:221], v[226:227], v[198:199], v[220:221]
	v_cvt_pk_f32_fp8_e32 v[226:227], v149
	v_pk_fma_f32 v[220:221], v[228:229], v[184:185], v[220:221]
	v_cvt_pk_f32_fp8_sdwa v[228:229], v149 src0_sel:WORD_1
	v_pk_fma_f32 v[220:221], v[230:231], v[188:189], v[220:221]
	v_cvt_pk_f32_fp8_e32 v[230:231], v150
	v_pk_mul_f32 v[222:223], v[222:223], v[186:187]
	v_pk_fma_f32 v[220:221], v[232:233], v[192:193], v[220:221]
	v_cvt_pk_f32_fp8_sdwa v[232:233], v150 src0_sel:WORD_1
	v_pk_fma_f32 v[222:223], v[224:225], v[190:191], v[222:223]
	v_cvt_pk_f32_fp8_e32 v[224:225], v152
	v_pk_fma_f32 v[220:221], v[234:235], v[196:197], v[220:221]
	v_cvt_pk_f32_fp8_e32 v[234:235], v151
	v_pk_fma_f32 v[222:223], v[226:227], v[194:195], v[222:223]
	v_cvt_pk_f32_fp8_sdwa v[226:227], v152 src0_sel:WORD_1
	v_cvt_pk_f32_fp8_sdwa v[236:237], v151 src0_sel:WORD_1
	v_pk_fma_f32 v[222:223], v[228:229], v[198:199], v[222:223]
	v_cvt_pk_f32_fp8_e32 v[228:229], v153
	v_pk_fma_f32 v[222:223], v[230:231], v[184:185], v[222:223]
	v_cvt_pk_f32_fp8_sdwa v[230:231], v153 src0_sel:WORD_1
	v_pk_fma_f32 v[222:223], v[232:233], v[188:189], v[222:223]
	v_cvt_pk_f32_fp8_e32 v[232:233], v154
	v_pk_mul_f32 v[224:225], v[224:225], v[186:187]
	v_pk_fma_f32 v[222:223], v[234:235], v[192:193], v[222:223]
	v_cvt_pk_f32_fp8_sdwa v[234:235], v154 src0_sel:WORD_1
	v_pk_fma_f32 v[224:225], v[226:227], v[190:191], v[224:225]
	v_cvt_pk_f32_fp8_e32 v[226:227], v156
	v_pk_fma_f32 v[222:223], v[236:237], v[196:197], v[222:223]
	v_cvt_pk_f32_fp8_e32 v[236:237], v155
	v_pk_fma_f32 v[224:225], v[228:229], v[194:195], v[224:225]
	v_cvt_pk_f32_fp8_sdwa v[228:229], v156 src0_sel:WORD_1
	v_cvt_pk_f32_fp8_sdwa v[238:239], v155 src0_sel:WORD_1
	v_pk_fma_f32 v[224:225], v[230:231], v[198:199], v[224:225]
	v_cvt_pk_f32_fp8_e32 v[230:231], v157
	v_pk_fma_f32 v[224:225], v[232:233], v[184:185], v[224:225]
	v_cvt_pk_f32_fp8_sdwa v[232:233], v157 src0_sel:WORD_1
	v_pk_fma_f32 v[224:225], v[234:235], v[188:189], v[224:225]
	v_cvt_pk_f32_fp8_e32 v[234:235], v158
	v_pk_mul_f32 v[226:227], v[226:227], v[186:187]
	v_pk_fma_f32 v[224:225], v[236:237], v[192:193], v[224:225]
	v_cvt_pk_f32_fp8_sdwa v[236:237], v158 src0_sel:WORD_1
	v_pk_fma_f32 v[226:227], v[228:229], v[190:191], v[226:227]
	v_cvt_pk_f32_fp8_e32 v[228:229], v160
	v_pk_fma_f32 v[224:225], v[238:239], v[196:197], v[224:225]
	v_cvt_pk_f32_fp8_e32 v[238:239], v159
	v_pk_fma_f32 v[226:227], v[230:231], v[194:195], v[226:227]
	v_cvt_pk_f32_fp8_sdwa v[230:231], v160 src0_sel:WORD_1
	v_cvt_pk_f32_fp8_sdwa v[240:241], v159 src0_sel:WORD_1
	v_pk_fma_f32 v[226:227], v[232:233], v[198:199], v[226:227]
	v_cvt_pk_f32_fp8_e32 v[232:233], v161
	v_pk_fma_f32 v[226:227], v[234:235], v[184:185], v[226:227]
	v_cvt_pk_f32_fp8_sdwa v[234:235], v161 src0_sel:WORD_1
	v_pk_fma_f32 v[226:227], v[236:237], v[188:189], v[226:227]
	v_cvt_pk_f32_fp8_e32 v[236:237], v162
	v_pk_mul_f32 v[228:229], v[228:229], v[186:187]
	v_pk_fma_f32 v[226:227], v[238:239], v[192:193], v[226:227]
	v_cvt_pk_f32_fp8_sdwa v[238:239], v162 src0_sel:WORD_1
	v_pk_fma_f32 v[228:229], v[230:231], v[190:191], v[228:229]
	v_cvt_pk_f32_fp8_e32 v[230:231], v164
	v_pk_fma_f32 v[226:227], v[240:241], v[196:197], v[226:227]
	v_cvt_pk_f32_fp8_e32 v[240:241], v163
; #define PD_H(t, H) do { const char* hb_ = h2u + (size_t)(t) * 2048; H[0] = *(const u32x4*)(hb_ + h2o); H[1] = *(const u32x4*)(hb_ + (h2o + 16u)); } while (0)
; DI void phase_peerdown(const Params& p, int bid, int nb) {
;     ...
;     PD_MATH(t1, wB, hB);
;     if (t2 >= T_) break;
;     if (t3 < T_) PD_H(t3, hB);
;     t = t2; t1 = t3;
	v_pk_fma_f32 v[228:229], v[232:233], v[194:195], v[228:229]
	v_cvt_pk_f32_fp8_sdwa v[232:233], v164 src0_sel:WORD_1
	v_cvt_pk_f32_fp8_sdwa v[242:243], v163 src0_sel:WORD_1
	v_pk_fma_f32 v[228:229], v[234:235], v[198:199], v[228:229]
	v_cvt_pk_f32_fp8_e32 v[234:235], v165
	v_pk_fma_f32 v[228:229], v[236:237], v[184:185], v[228:229]
	v_cvt_pk_f32_fp8_sdwa v[236:237], v165 src0_sel:WORD_1
	v_pk_fma_f32 v[228:229], v[238:239], v[188:189], v[228:229]
	v_cvt_pk_f32_fp8_e32 v[238:239], v166
	v_pk_mul_f32 v[230:231], v[230:231], v[186:187]
	v_pk_fma_f32 v[228:229], v[240:241], v[192:193], v[228:229]
	v_cvt_pk_f32_fp8_sdwa v[240:241], v166 src0_sel:WORD_1
	v_pk_fma_f32 v[230:231], v[232:233], v[190:191], v[230:231]
	v_cvt_pk_f32_fp8_e32 v[232:233], v168
	v_pk_fma_f32 v[228:229], v[242:243], v[196:197], v[228:229]
	v_cvt_pk_f32_fp8_e32 v[242:243], v167
	v_pk_fma_f32 v[230:231], v[234:235], v[194:195], v[230:231]
	v_cvt_pk_f32_fp8_sdwa v[234:235], v168 src0_sel:WORD_1
	v_cvt_pk_f32_fp8_sdwa v[244:245], v167 src0_sel:WORD_1
	v_pk_fma_f32 v[230:231], v[236:237], v[198:199], v[230:231]
	v_cvt_pk_f32_fp8_e32 v[236:237], v169
	v_pk_fma_f32 v[230:231], v[238:239], v[184:185], v[230:231]
	v_cvt_pk_f32_fp8_sdwa v[238:239], v169 src0_sel:WORD_1
	v_pk_fma_f32 v[230:231], v[240:241], v[188:189], v[230:231]
	v_cvt_pk_f32_fp8_e32 v[240:241], v170
	v_pk_mul_f32 v[232:233], v[232:233], v[186:187]
	v_pk_fma_f32 v[230:231], v[242:243], v[192:193], v[230:231]
	v_cvt_pk_f32_fp8_sdwa v[242:243], v170 src0_sel:WORD_1
	v_pk_fma_f32 v[232:233], v[234:235], v[190:191], v[232:233]
	v_cvt_pk_f32_fp8_e32 v[234:235], v172
	v_pk_fma_f32 v[230:231], v[244:245], v[196:197], v[230:231]
	v_cvt_pk_f32_fp8_e32 v[244:245], v171
	v_pk_fma_f32 v[232:233], v[236:237], v[194:195], v[232:233]
	v_cvt_pk_f32_fp8_sdwa v[236:237], v172 src0_sel:WORD_1
	v_cvt_pk_f32_fp8_sdwa v[246:247], v171 src0_sel:WORD_1
	v_pk_fma_f32 v[232:233], v[238:239], v[198:199], v[232:233]
	v_cvt_pk_f32_fp8_e32 v[238:239], v173
	v_pk_fma_f32 v[232:233], v[240:241], v[184:185], v[232:233]
	v_cvt_pk_f32_fp8_sdwa v[240:241], v173 src0_sel:WORD_1
	v_pk_fma_f32 v[232:233], v[242:243], v[188:189], v[232:233]
	v_cvt_pk_f32_fp8_e32 v[242:243], v174
	v_pk_mul_f32 v[186:187], v[234:235], v[186:187]
	v_pk_fma_f32 v[232:233], v[244:245], v[192:193], v[232:233]
	v_cvt_pk_f32_fp8_sdwa v[244:245], v174 src0_sel:WORD_1
	v_pk_fma_f32 v[186:187], v[236:237], v[190:191], v[186:187]
	v_pk_fma_f32 v[232:233], v[246:247], v[196:197], v[232:233]
	v_cvt_pk_f32_fp8_e32 v[246:247], v175
	v_pk_fma_f32 v[186:187], v[238:239], v[194:195], v[186:187]
	v_cvt_pk_f32_fp8_sdwa v[248:249], v175 src0_sel:WORD_1
	v_pk_fma_f32 v[186:187], v[240:241], v[198:199], v[186:187]
	v_mov_b32_e32 v194, v220
	v_pk_fma_f32 v[184:185], v[242:243], v[184:185], v[186:187]
	v_mov_b32_e32 v186, v200
	v_pk_fma_f32 v[184:185], v[244:245], v[188:189], v[184:185]
	v_mov_b32_e32 v187, v202
	v_pk_fma_f32 v[184:185], v[246:247], v[192:193], v[184:185]
	v_mov_b32_e32 v202, v201
	v_pk_fma_f32 v[184:185], v[248:249], v[196:197], v[184:185]
	v_mov_b32_e32 v195, v222
	v_mov_b32_e32 v222, v221
	v_pk_add_f32 v[186:187], v[186:187], v[202:203]
	v_pk_add_f32 v[194:195], v[194:195], v[222:223]
	v_mov_b32_e32 v200, v232
	v_mov_b32_e32 v201, v184
	v_mov_b32_e32 v184, v233
	v_mov_b32_e32 v188, v204
	v_mov_b32_e32 v189, v210
	v_mov_b32_e32 v210, v205
	v_mov_b32_e32 v196, v224
	v_mov_b32_e32 v197, v226
	v_mov_b32_e32 v226, v225
	v_pk_add_f32 v[184:185], v[200:201], v[184:185]
	v_cndmask_b32_e64 v200, v186, v194, s[4:5]
	v_cndmask_b32_e64 v202, v194, v186, s[4:5]
	v_cndmask_b32_e64 v186, v187, v195, s[4:5]
	v_pk_add_f32 v[188:189], v[188:189], v[210:211]
	v_pk_add_f32 v[196:197], v[196:197], v[226:227]
	v_mov_b32_dpp v200, v200 row_half_mirror row_mask:0xf bank_mask:0xf bound_ctrl:1
	v_cndmask_b32_e64 v203, v195, v187, s[4:5]
	v_mov_b32_dpp v201, v186 row_half_mirror row_mask:0xf bank_mask:0xf bound_ctrl:1
	v_mov_b32_e32 v190, v212
	v_mov_b32_e32 v191, v214
	v_mov_b32_e32 v214, v213
	v_mov_b32_e32 v198, v228
	v_mov_b32_e32 v199, v230
	v_mov_b32_e32 v230, v229
	v_pk_add_f32 v[186:187], v[202:203], v[200:201]
	v_cndmask_b32_e64 v194, v188, v196, s[4:5]
	v_cndmask_b32_e64 v200, v196, v188, s[4:5]
	v_cndmask_b32_e64 v188, v189, v197, s[4:5]
	v_pk_add_f32 v[190:191], v[190:191], v[214:215]
	v_pk_add_f32 v[198:199], v[198:199], v[230:231]
	v_mov_b32_dpp v194, v194 row_half_mirror row_mask:0xf bank_mask:0xf bound_ctrl:1
	v_cndmask_b32_e64 v201, v197, v189, s[4:5]
	v_mov_b32_dpp v195, v188 row_half_mirror row_mask:0xf bank_mask:0xf bound_ctrl:1
	v_mov_b32_e32 v192, v216
	v_mov_b32_e32 v193, v218
	v_mov_b32_e32 v218, v217
	v_pk_add_f32 v[188:189], v[200:201], v[194:195]
	v_cndmask_b32_e64 v194, v190, v198, s[4:5]
	v_cndmask_b32_e64 v196, v198, v190, s[4:5]
	v_cndmask_b32_e64 v190, v191, v199, s[4:5]
	v_pk_add_f32 v[192:193], v[192:193], v[218:219]
	v_mov_b32_dpp v194, v194 row_half_mirror row_mask:0xf bank_mask:0xf bound_ctrl:1
	v_cndmask_b32_e64 v197, v199, v191, s[4:5]
	v_mov_b32_dpp v195, v190 row_half_mirror row_mask:0xf bank_mask:0xf bound_ctrl:1
	v_pk_add_f32 v[190:191], v[196:197], v[194:195]
	v_cndmask_b32_e64 v194, v192, v184, s[4:5]
	v_cndmask_b32_e64 v196, v184, v192, s[4:5]
	v_cndmask_b32_e64 v184, v193, v185, s[4:5]
	v_mov_b32_dpp v194, v194 row_half_mirror row_mask:0xf bank_mask:0xf bound_ctrl:1
	v_cndmask_b32_e64 v197, v185, v193, s[4:5]
	v_mov_b32_dpp v195, v184 row_half_mirror row_mask:0xf bank_mask:0xf bound_ctrl:1
	v_pk_add_f32 v[184:185], v[196:197], v[194:195]
	v_cndmask_b32_e64 v192, v186, v190, s[2:3]
	v_cndmask_b32_e64 v194, v190, v186, s[2:3]
	v_cndmask_b32_e64 v186, v187, v191, s[2:3]
	v_mov_b32_dpp v192, v192 quad_perm:[2,3,0,1] row_mask:0xf bank_mask:0xf bound_ctrl:1
	v_cndmask_b32_e64 v195, v191, v187, s[2:3]
	v_mov_b32_dpp v193, v186 quad_perm:[2,3,0,1] row_mask:0xf bank_mask:0xf bound_ctrl:1
	v_pk_add_f32 v[186:187], v[194:195], v[192:193]
	v_cndmask_b32_e64 v190, v188, v184, s[2:3]
	v_cndmask_b32_e64 v192, v184, v188, s[2:3]
	v_cndmask_b32_e64 v184, v189, v185, s[2:3]
	v_mov_b32_dpp v190, v190 quad_perm:[2,3,0,1] row_mask:0xf bank_mask:0xf bound_ctrl:1
	v_cndmask_b32_e64 v193, v185, v189, s[2:3]
	v_mov_b32_dpp v191, v184 quad_perm:[2,3,0,1] row_mask:0xf bank_mask:0xf bound_ctrl:1
	v_pk_add_f32 v[184:185], v[192:193], v[190:191]
	s_ashr_i32 s11, s10, 31
	v_cndmask_b32_e64 v188, v186, v184, s[0:1]
	v_cndmask_b32_e64 v190, v184, v186, s[0:1]
	v_cndmask_b32_e64 v184, v187, v185, s[0:1]
	v_mov_b32_dpp v188, v188 quad_perm:[1,0,3,2] row_mask:0xf bank_mask:0xf bound_ctrl:1
	v_cndmask_b32_e64 v191, v185, v187, s[0:1]
	v_mov_b32_dpp v189, v184 quad_perm:[1,0,3,2] row_mask:0xf bank_mask:0xf bound_ctrl:1
	v_pk_add_f32 v[184:185], v[190:191], v[188:189]
	s_lshl_b64 s[10:11], s[10:11], 8
	v_cvt_pk_bf16_f32 v186, v184, v185
	v_lshl_add_u64 v[184:185], v[178:179], 0, s[10:11]
	global_store_dword v[184:185], v186, off
